# v44 + MLA and NA attention also stage V with image row = key and drop the per-tile P-fragment permlane32_swaps
# speedup vs baseline: 1.0024x; 1.0007x over previous
.LBB0_799:
	v_cndmask_b32_e64 v65, v65, v206, s[58:59]
	v_mul_f32_e32 v65, 0xbe0293ee, v65
	v_fmamk_f32 v67, v113, 0x3e0293ee, v65
	v_exp_f32_e32 v83, v67
	v_fmamk_f32 v67, v112, 0x3e0293ee, v65
	v_exp_f32_e32 v85, v67
	v_fmamk_f32 v67, v111, 0x3e0293ee, v65
	v_exp_f32_e32 v81, v67
	v_fmamk_f32 v67, v110, 0x3e0293ee, v65
	v_exp_f32_e32 v87, v67
	v_fmamk_f32 v67, v109, 0x3e0293ee, v65
	v_exp_f32_e32 v89, v67
	v_fmamk_f32 v67, v108, 0x3e0293ee, v65
	v_exp_f32_e32 v91, v67
	v_fmamk_f32 v67, v107, 0x3e0293ee, v65
	v_exp_f32_e32 v93, v67
	v_fmamk_f32 v67, v106, 0x3e0293ee, v65
	v_exp_f32_e32 v95, v67
	v_fmamk_f32 v67, v105, 0x3e0293ee, v65
	v_exp_f32_e32 v105, v67
	v_fmamk_f32 v67, v104, 0x3e0293ee, v65
	v_exp_f32_e32 v107, v67
	v_fmamk_f32 v67, v103, 0x3e0293ee, v65
	v_exp_f32_e32 v77, v67
	v_fmamk_f32 v67, v102, 0x3e0293ee, v65
	v_exp_f32_e32 v103, v67
	v_fmamk_f32 v67, v99, 0x3e0293ee, v65
	v_exp_f32_e32 v99, v67
	v_fmamk_f32 v67, v98, 0x3e0293ee, v65
	v_exp_f32_e32 v109, v67
	v_fmamk_f32 v67, v97, 0x3e0293ee, v65
	v_exp_f32_e32 v75, v67
	v_fmamk_f32 v67, v96, 0x3e0293ee, v65
	v_exp_f32_e32 v97, v67
	v_fmamk_f32 v67, v79, 0x3e0293ee, v65
	v_fmamk_f32 v69, v125, 0x3e0293ee, v65
	v_fmamk_f32 v70, v124, 0x3e0293ee, v65
	v_fmamk_f32 v73, v123, 0x3e0293ee, v65
	v_fmamk_f32 v78, v122, 0x3e0293ee, v65
	v_fmamk_f32 v79, v121, 0x3e0293ee, v65
	v_fmamk_f32 v80, v120, 0x3e0293ee, v65
	v_fmamk_f32 v72, v72, 0x3e0293ee, v65
	v_fmamk_f32 v71, v71, 0x3e0293ee, v65
	v_fmamk_f32 v82, v119, 0x3e0293ee, v65
	v_fmamk_f32 v76, v118, 0x3e0293ee, v65
	v_fmamk_f32 v84, v117, 0x3e0293ee, v65
	v_fmamk_f32 v86, v116, 0x3e0293ee, v65
	v_fmamk_f32 v88, v115, 0x3e0293ee, v65
	v_fmamk_f32 v74, v114, 0x3e0293ee, v65
	v_fmac_f32_e32 v65, 0x3e0293ee, v64
	v_exp_f32_e32 v96, v65
	v_exp_f32_e32 v74, v74
	v_exp_f32_e32 v94, v72
	v_exp_f32_e32 v92, v80
	v_exp_f32_e32 v108, v88
	v_exp_f32_e32 v90, v79
	v_exp_f32_e32 v98, v86
	v_exp_f32_e32 v88, v78
	v_exp_f32_e32 v102, v84
	v_exp_f32_e32 v86, v73
	v_exp_f32_e32 v76, v76
	v_exp_f32_e32 v104, v71
	v_exp_f32_e32 v80, v70
	v_pk_add_f32 v[70:71], v[96:97], v[74:75]
	v_pk_add_f32 v[72:73], v[94:95], v[92:93]
	v_exp_f32_e32 v106, v82
	v_exp_f32_e32 v84, v69
	v_pk_add_f32 v[70:71], v[108:109], v[70:71]
	v_pk_add_f32 v[72:73], v[90:91], v[72:73]
	v_exp_f32_e32 v82, v67
	v_pk_add_f32 v[70:71], v[98:99], v[70:71]
	v_pk_add_f32 v[72:73], v[88:89], v[72:73]
	v_pk_add_f32 v[70:71], v[102:103], v[70:71]
	v_pk_add_f32 v[72:73], v[86:87], v[72:73]
	v_pk_add_f32 v[70:71], v[76:77], v[70:71]
	v_pk_add_f32 v[72:73], v[80:81], v[72:73]
	v_pk_add_f32 v[70:71], v[106:107], v[70:71]
	v_pk_add_f32 v[72:73], v[84:85], v[72:73]
	v_pk_add_f32 v[70:71], v[104:105], v[70:71]
	v_pk_add_f32 v[72:73], v[82:83], v[72:73]
	s_lshl_b64 s[2:3], s[78:79], 12
	v_pk_add_f32 v[70:71], v[72:73], v[70:71]
	s_add_u32 s6, s35, s2
	v_pk_add_f32 v[70:71], v[70:71], v[70:71] op_sel:[0,1] op_sel_hi:[1,0]
	s_addc_u32 s7, s36, s3
	s_lshl_b32 s2, s15, 7
	v_mov_b32_e32 v69, v70
	s_ashr_i32 s3, s2, 31
	s_nop 0
	v_permlane32_swap_b32_e32 v70, v69
	s_lshl_b64 s[2:3], s[2:3], 1
	v_mul_f32_e32 v64, v162, v187
	v_add_f32_e32 v68, v100, v101
	v_mov_b32_e32 v65, v70
	s_add_u32 s6, s6, s2
	v_pk_add_f32 v[64:65], v[64:65], v[68:69]
	s_addc_u32 s7, s7, s3
	v_fmac_f32_e32 v65, v64, v66
	v_cvt_pk_bf16_f32 v66, v97, v75
	v_cvt_pk_bf16_f32 v67, v109, v99
	v_cvt_pk_bf16_f32 v68, v103, v77
	v_cvt_pk_bf16_f32 v69, v107, v105
	v_cvt_pk_bf16_f32 v70, v95, v93
	v_cvt_pk_bf16_f32 v71, v91, v89
	v_cvt_pk_bf16_f32 v72, v87, v81
	v_cvt_pk_bf16_f32 v73, v85, v83
	v_cvt_pk_bf16_f32 v74, v96, v74
	v_cvt_pk_bf16_f32 v75, v108, v98
	v_cvt_pk_bf16_f32 v76, v102, v76
	v_cvt_pk_bf16_f32 v77, v106, v104
	v_cvt_pk_bf16_f32 v78, v94, v92
	v_cvt_pk_bf16_f32 v79, v90, v88
	v_cvt_pk_bf16_f32 v80, v86, v80
	v_cvt_pk_bf16_f32 v81, v84, v82
	s_cmp_lg_u32 0, -1
	s_cselect_b32 s2, 0, 0
	s_addk_i32 s2, 0x4000
	v_add_u32_e32 v64, s2, v181
	ds_read_b64_tr_b16 v[82:83], v64 offset:0
	ds_read_b64_tr_b16 v[84:85], v64 offset:0x800
	ds_read_b64_tr_b16 v[86:87], v64 offset:0x1000
	ds_read_b64_tr_b16 v[88:89], v64 offset:0x1800
	ds_read_b64_tr_b16 v[90:91], v64 offset:0x2000
	ds_read_b64_tr_b16 v[92:93], v64 offset:0x2800
	ds_read_b64_tr_b16 v[94:95], v64 offset:0x3000
	ds_read_b64_tr_b16 v[96:97], v64 offset:0x3800
	s_waitcnt lgkmcnt(0)
	s_nop 0
	v_mfma_f32_32x32x16_bf16 v[48:63], v[82:85], v[66:69], v[48:63]
	ds_read_b64_tr_b16 v[82:83], v64 offset:0x200
	ds_read_b64_tr_b16 v[84:85], v64 offset:0xa00
	v_mfma_f32_32x32x16_bf16 v[48:63], v[86:89], v[70:73], v[48:63]
	ds_read_b64_tr_b16 v[86:87], v64 offset:0x1200
	ds_read_b64_tr_b16 v[88:89], v64 offset:0x1a00
	v_mfma_f32_32x32x16_bf16 v[48:63], v[90:93], v[74:77], v[48:63]
	ds_read_b64_tr_b16 v[90:91], v64 offset:0x2200
	ds_read_b64_tr_b16 v[92:93], v64 offset:0x2a00
	v_mfma_f32_32x32x16_bf16 v[48:63], v[94:97], v[78:81], v[48:63]
	ds_read_b64_tr_b16 v[94:95], v64 offset:0x3200
	ds_read_b64_tr_b16 v[96:97], v64 offset:0x3a00
	s_waitcnt lgkmcnt(0)
	v_mfma_f32_32x32x16_bf16 v[32:47], v[82:85], v[66:69], v[32:47]
	ds_read_b64_tr_b16 v[82:83], v64 offset:0x400
	ds_read_b64_tr_b16 v[84:85], v64 offset:0xc00
	v_mfma_f32_32x32x16_bf16 v[32:47], v[86:89], v[70:73], v[32:47]
	ds_read_b64_tr_b16 v[86:87], v64 offset:0x1400
	ds_read_b64_tr_b16 v[88:89], v64 offset:0x1c00
	v_mfma_f32_32x32x16_bf16 v[32:47], v[90:93], v[74:77], v[32:47]
	ds_read_b64_tr_b16 v[90:91], v64 offset:0x2400
	ds_read_b64_tr_b16 v[92:93], v64 offset:0x2c00
	v_mfma_f32_32x32x16_bf16 v[32:47], v[94:97], v[78:81], v[32:47]
	ds_read_b64_tr_b16 v[94:95], v64 offset:0x3400
	ds_read_b64_tr_b16 v[96:97], v64 offset:0x3c00
	s_waitcnt lgkmcnt(0)
	v_mfma_f32_32x32x16_bf16 v[16:31], v[82:85], v[66:69], v[16:31]
	ds_read_b64_tr_b16 v[82:83], v64 offset:0x600
	ds_read_b64_tr_b16 v[84:85], v64 offset:0xe00
	v_mfma_f32_32x32x16_bf16 v[16:31], v[86:89], v[70:73], v[16:31]
	ds_read_b64_tr_b16 v[86:87], v64 offset:0x1600
	ds_read_b64_tr_b16 v[88:89], v64 offset:0x1e00
	v_mfma_f32_32x32x16_bf16 v[16:31], v[90:93], v[74:77], v[16:31]
	ds_read_b64_tr_b16 v[90:91], v64 offset:0x2600
	ds_read_b64_tr_b16 v[92:93], v64 offset:0x2e00
	v_mfma_f32_32x32x16_bf16 v[16:31], v[94:97], v[78:81], v[16:31]
	ds_read_b64_tr_b16 v[94:95], v64 offset:0x3600
	ds_read_b64_tr_b16 v[96:97], v64 offset:0x3e00
	s_waitcnt lgkmcnt(0)
	v_mfma_f32_32x32x16_bf16 v[0:15], v[82:85], v[66:69], v[0:15]
	v_rcp_f32_e32 v67, v65
	v_mbcnt_lo_u32_b32 v66, -1, 0
	v_mbcnt_hi_u32_b32 v66, -1, v66
	s_add_i32 s12, s12, 1
	v_add_u32_e32 v64, s80, v66
	v_ashrrev_i32_e32 v64, 1, v64
	v_mul_f32_e32 v48, v67, v48
	v_mul_f32_e32 v49, v67, v49
	v_bfi_b32 v64, s84, v64, v66
	v_cvt_pk_bf16_f32 v48, v48, v49
	v_mul_f32_e32 v49, v67, v50
	v_mul_f32_e32 v50, v67, v51
	v_ashrrev_i32_e32 v65, 31, v64
	v_cvt_pk_bf16_f32 v49, v49, v50
	v_mul_f32_e32 v50, v67, v52
	v_mul_f32_e32 v51, v67, v53
	v_lshlrev_b64 v[64:65], 12, v[64:65]
	v_lshrrev_b32_e32 v66, 1, v66
	v_cvt_pk_bf16_f32 v50, v50, v51
	v_mul_f32_e32 v51, v67, v54
	v_lshl_add_u64 v[64:65], s[6:7], 0, v[64:65]
	v_and_b32_e32 v128, 16, v66
	v_mul_f32_e32 v52, v67, v55
	v_cvt_pk_bf16_f32 v51, v51, v52
	v_lshl_add_u64 v[64:65], v[64:65], 0, v[128:129]
	v_permlane32_swap_b32_e32 v48, v50
	v_permlane32_swap_b32_e32 v49, v51
	global_store_dwordx4 v[64:65], v[48:51], off
	v_mfma_f32_32x32x16_bf16 v[0:15], v[86:89], v[70:73], v[0:15]
	v_mul_f32_e32 v52, v67, v63
	v_mul_f32_e32 v48, v67, v56
	v_mul_f32_e32 v49, v67, v57
	v_cvt_pk_bf16_f32 v48, v48, v49
	v_mul_f32_e32 v49, v67, v58
	v_mul_f32_e32 v50, v67, v59
	v_cvt_pk_bf16_f32 v49, v49, v50
	v_mul_f32_e32 v50, v67, v60
	v_mul_f32_e32 v51, v67, v61
	v_cvt_pk_bf16_f32 v50, v50, v51
	v_mul_f32_e32 v51, v67, v62
	v_cvt_pk_bf16_f32 v51, v51, v52
	v_permlane32_swap_b32_e32 v48, v50
	s_nop 0
	v_permlane32_swap_b32_e32 v49, v51
	v_mul_f32_e32 v32, v67, v32
	v_mul_f32_e32 v33, v67, v33
	global_store_dwordx4 v[64:65], v[48:51], off offset:32
	v_cvt_pk_bf16_f32 v32, v32, v33
	v_mul_f32_e32 v33, v67, v34
	v_mul_f32_e32 v34, v67, v35
	v_cvt_pk_bf16_f32 v33, v33, v34
	v_mul_f32_e32 v34, v67, v36
	v_mul_f32_e32 v35, v67, v37
	v_cvt_pk_bf16_f32 v34, v34, v35
	v_mul_f32_e32 v35, v67, v38
	v_mul_f32_e32 v36, v67, v39
	v_cvt_pk_bf16_f32 v35, v35, v36
	v_permlane32_swap_b32_e32 v32, v34
	v_permlane32_swap_b32_e32 v33, v35
	v_mfma_f32_32x32x16_bf16 v[0:15], v[90:93], v[74:77], v[0:15]
	global_store_dwordx4 v[64:65], v[32:35], off offset:64
	v_mul_f32_e32 v36, v67, v47
	v_mul_f32_e32 v16, v67, v16
	v_mul_f32_e32 v32, v67, v40
	v_mul_f32_e32 v33, v67, v41
	v_cvt_pk_bf16_f32 v32, v32, v33
	v_mul_f32_e32 v33, v67, v42
	v_mul_f32_e32 v34, v67, v43
	v_cvt_pk_bf16_f32 v33, v33, v34
	v_mul_f32_e32 v34, v67, v44
	v_mul_f32_e32 v35, v67, v45
	v_cvt_pk_bf16_f32 v34, v34, v35
	v_mul_f32_e32 v35, v67, v46
	v_cvt_pk_bf16_f32 v35, v35, v36
	v_permlane32_swap_b32_e32 v32, v34
	s_nop 0
	v_permlane32_swap_b32_e32 v33, v35
	v_mul_f32_e32 v17, v67, v17
	global_store_dwordx4 v[64:65], v[32:35], off offset:96
	v_cvt_pk_bf16_f32 v16, v16, v17
	v_mul_f32_e32 v17, v67, v18
	v_mul_f32_e32 v18, v67, v19
	v_cvt_pk_bf16_f32 v17, v17, v18
	v_mul_f32_e32 v18, v67, v20
	v_mul_f32_e32 v19, v67, v21
	v_mfma_f32_32x32x16_bf16 v[0:15], v[94:97], v[78:81], v[0:15]
	v_cvt_pk_bf16_f32 v18, v18, v19
	v_mul_f32_e32 v19, v67, v22
	v_mul_f32_e32 v20, v67, v23
	v_cvt_pk_bf16_f32 v19, v19, v20
	v_permlane32_swap_b32_e32 v16, v18
	v_permlane32_swap_b32_e32 v17, v19
	global_store_dwordx4 v[64:65], v[16:19], off offset:128
	v_mul_f32_e32 v20, v67, v31
	s_nop 5
	v_mul_f32_e32 v0, v67, v0
	v_mul_f32_e32 v16, v67, v24
	v_mul_f32_e32 v17, v67, v25
	v_cvt_pk_bf16_f32 v16, v16, v17
	v_mul_f32_e32 v17, v67, v26
	v_mul_f32_e32 v18, v67, v27
	v_cvt_pk_bf16_f32 v17, v17, v18
	v_mul_f32_e32 v18, v67, v28
	v_mul_f32_e32 v19, v67, v29
	v_cvt_pk_bf16_f32 v18, v18, v19
	v_mul_f32_e32 v19, v67, v30
	v_cvt_pk_bf16_f32 v19, v19, v20
	v_permlane32_swap_b32_e32 v16, v18
	s_nop 0
	v_permlane32_swap_b32_e32 v17, v19
	v_mul_f32_e32 v1, v67, v1
	global_store_dwordx4 v[64:65], v[16:19], off offset:160
	v_cvt_pk_bf16_f32 v0, v0, v1
	v_mul_f32_e32 v1, v67, v2
	v_mul_f32_e32 v2, v67, v3
	v_cvt_pk_bf16_f32 v1, v1, v2
	v_mul_f32_e32 v2, v67, v4
	v_mul_f32_e32 v3, v67, v5
	v_cvt_pk_bf16_f32 v2, v2, v3
	v_mul_f32_e32 v3, v67, v6
	v_mul_f32_e32 v4, v67, v7
	v_cvt_pk_bf16_f32 v3, v3, v4
	v_permlane32_swap_b32_e32 v0, v2
	v_permlane32_swap_b32_e32 v1, v3
	global_store_dwordx4 v[64:65], v[0:3], off offset:192
	v_mul_f32_e32 v4, v67, v15
	s_mov_b64 s[6:7], 0
	v_mul_f32_e32 v0, v67, v8
	v_mul_f32_e32 v1, v67, v9
	v_cvt_pk_bf16_f32 v0, v0, v1
	v_mul_f32_e32 v1, v67, v10
	v_mul_f32_e32 v2, v67, v11
	v_cvt_pk_bf16_f32 v1, v1, v2
	v_mul_f32_e32 v2, v67, v12
	v_mul_f32_e32 v3, v67, v13
	v_cvt_pk_bf16_f32 v2, v2, v3
	v_mul_f32_e32 v3, v67, v14
	v_cvt_pk_bf16_f32 v3, v3, v4
	v_permlane32_swap_b32_e32 v0, v2
	s_nop 0
	v_permlane32_swap_b32_e32 v1, v3
	global_store_dwordx4 v[64:65], v[0:3], off offset:224

.LBB0_812:
	s_or_b64 exec, exec, s[6:7]
	s_lshl_b32 s6, s16, 8
	s_mul_i32 s8, s30, 0x900
	s_ashr_i32 s7, s6, 31
	s_mul_hi_i32 s3, s30, 0x900
	s_add_u32 s78, s8, s6
	s_addc_u32 s79, s3, s7
	s_mul_i32 s6, s78, s69
	s_mul_hi_u32 s7, s78, s68
	s_add_i32 s6, s7, s6
	s_mul_i32 s7, s79, s68
	s_add_i32 s7, s6, s7
	s_mul_i32 s6, s78, s68
	s_lshl_b64 s[6:7], s[6:7], 1
	s_add_u32 s9, s60, s6
	s_mul_i32 s6, s15, s26
	s_addc_u32 s11, s61, s7
	s_ashr_i32 s7, s6, 31
	s_lshl_b64 s[6:7], s[6:7], 1
	s_add_u32 s10, s9, s6
	s_mul_i32 s3, s3, s62
	s_mul_hi_u32 s6, s8, s62
	s_addc_u32 s11, s11, s7
	s_add_i32 s7, s6, s3
	s_mul_i32 s6, s8, s62
	s_lshl_b64 s[8:9], s[6:7], 1
	s_add_u32 s3, s66, s8
	s_addc_u32 s22, s67, s9
	s_abs_i32 s7, s15
	s_mul_hi_u32 s20, s7, s13
	s_mul_i32 s21, s20, s89
	s_sub_i32 s7, s7, s21
	s_ashr_i32 s6, s15, 31
	s_add_i32 s21, s20, 1
	s_sub_i32 s23, s7, s89
	s_cmp_ge_u32 s7, s89
	s_cselect_b32 s20, s21, s20
	v_ashrrev_i32_e32 v20, 4, v8
	v_and_b32_e32 v3, 0xfffff0, v20
	v_lshlrev_b32_e32 v4, 1, v20
	s_cselect_b32 s7, s23, s7
	s_add_i32 s21, s20, 1
	v_lshlrev_b32_e32 v1, 3, v8
	v_and_or_b32 v3, v4, 8, v3
	s_cmp_ge_u32 s7, s89
	v_and_b32_e32 v2, 0x78, v1
	v_lshrrev_b32_e32 v3, 1, v3
	v_bfe_u32 v1, v1, 5, 2
	s_cselect_b32 s7, s21, s20
	v_or_b32_e32 v3, v3, v1
	s_xor_b32 s7, s7, s6
	v_lshrrev_b32_e32 v4, 1, v20
	v_lshlrev_b32_e32 v21, 9, v3
	v_and_b32_e32 v3, 3, v20
	s_sub_i32 s6, s7, s6
	v_and_or_b32 v3, v4, 4, v3
	v_add_u32_e32 v24, 32, v20
	s_mul_i32 s6, s6, s27
	v_lshlrev_b32_e32 v22, 6, v3
	v_and_b32_e32 v3, 0xfffff0, v24
	v_lshlrev_b32_e32 v4, 1, v24
	s_ashr_i32 s7, s6, 31
	v_and_or_b32 v3, v4, 8, v3
	s_lshl_b64 s[20:21], s[6:7], 1
	v_lshrrev_b32_e32 v3, 1, v3
	s_add_u32 s6, s3, s20
	v_or_b32_e32 v1, v3, v1
	s_addc_u32 s7, s22, s21
	v_lshlrev_b32_e32 v25, 9, v1
	v_mul_lo_u32 v1, v20, s62
	s_add_u32 s3, s85, s8
	v_or_b32_e32 v3, v1, v2
	v_add_u32_e32 v1, s14, v1
	s_addc_u32 s9, s81, s9
	v_and_b32_e32 v0, 63, v8
	v_or_b32_e32 v1, v1, v2
	v_lshlrev_b32_e32 v26, 4, v8
	s_add_u32 s8, s3, s20
	v_lshlrev_b32_e32 v23, 1, v2
	v_lshlrev_b32_e32 v178, 1, v1
	v_lshlrev_b32_e32 v0, 3, v0
	v_and_b32_e32 v1, 0xc0, v26
	v_lshlrev_b32_e32 v2, 1, v8
	s_addc_u32 s9, s9, s21
	v_lshlrev_b32_e32 v128, 1, v3
	v_and_or_b32 v1, v0, 24, v1
	v_and_b32_e32 v2, 32, v2
	v_and_b32_e32 v0, 0x100, v0
	v_or3_b32 v181, v1, v2, v0
	global_load_dwordx4 v[10:13], v128, s[8:9]
	global_load_dwordx4 v[14:17], v178, s[8:9]
	global_load_dwordx4 v[4:7], v128, s[6:7]
	global_load_dwordx4 v[0:3], v178, s[6:7]
	v_ashrrev_i32_e32 v27, 1, v8
	v_bfi_b32 v18, s84, v27, v8
	v_ashrrev_i32_e32 v19, 31, v27
	v_mul_lo_u32 v28, s68, v19
	v_mul_lo_u32 v29, s69, v18
	v_mad_u64_u32 v[18:19], s[20:21], s68, v18, 0
	v_bfe_u32 v182, v8, 5, 1
	v_add3_u32 v19, v19, v28, v29
	v_lshl_add_u64 v[18:19], v[18:19], 1, s[10:11]
	v_lshlrev_b32_e32 v32, 4, v182
	v_mov_b32_e32 v33, v129
	v_lshl_add_u64 v[18:19], v[18:19], 0, v[32:33]
	global_load_dwordx4 v[120:123], v[18:19], off
	global_load_dwordx4 v[124:127], v[18:19], off offset:32
	global_load_dwordx4 v[116:119], v[18:19], off offset:64
	global_load_dwordx4 v[112:115], v[18:19], off offset:96
	global_load_dwordx4 v[108:111], v[18:19], off offset:128
	global_load_dwordx4 v[104:107], v[18:19], off offset:160
	global_load_dwordx4 v[100:103], v[18:19], off offset:192
	global_load_dwordx4 v[96:99], v[18:19], off offset:224
	v_and_b32_e32 v18, 48, v23
	v_or3_b32 v19, v21, v22, v18
	v_add_u32_e32 v201, 0, v19
	v_lshrrev_b32_e32 v19, 3, v201
	v_xor_b32_e32 v19, v19, v201
	v_and_b32_e32 v19, 0x100, v19
	v_xor_b32_e32 v201, v201, v19
	v_lshlrev_b32_e32 v19, 3, v19
	v_xor_b32_e32 v201, v201, v19
	v_and_b32_e32 v9, 31, v8
	v_ashrrev_i32_e32 v21, 7, v8
	s_waitcnt vmcnt(0)
	v_and_b32_e32 v8, 0x70, v8
	v_or3_b32 v18, v25, v22, v18
	v_add_u32_e32 v202, 0, v18
	v_lshrrev_b32_e32 v18, 3, v202
	v_xor_b32_e32 v18, v18, v202
	v_and_b32_e32 v18, 0x100, v18
	v_xor_b32_e32 v202, v202, v18
	v_lshlrev_b32_e32 v18, 3, v18
	v_xor_b32_e32 v202, v202, v18
	v_lshlrev_b32_e32 v33, 8, v9
	v_and_b32_e32 v42, 0x70, v26
	v_add_u32_e32 v184, s2, v21
	v_max_i32_e32 v21, 4, v184
	v_add_u32_e32 v21, -4, v21
	v_min_u32_e32 v185, 24, v21
	v_and_or_b32 v183, v27, 32, v9
	v_or_b32_e32 v34, 32, v32
	v_bitop3_b32 v34, v34, v33, v42 bitop3:0xde
	v_add_u32_e32 v200, 0, v34
	s_cmp_lg_u32 0, -1
	s_cselect_b32 s3, 0, 0
	v_add_u32_e32 v186, s3, v181
	v_add_u32_e32 v188, 7, v185
	s_waitcnt vmcnt(11)
	ds_write_b128 v201, v[10:13]
	v_lshlrev_b32_e32 v10, 8, v20
	v_bitop3_b32 v10, v23, v10, v8 bitop3:0xde
	v_add_u32_e32 v203, 0, v10
	s_waitcnt vmcnt(10)
	ds_write_b128 v202, v[14:17]
	s_waitcnt vmcnt(9)
	ds_write_b128 v203, v[4:7] offset:32768
	v_lshlrev_b32_e32 v4, 8, v24
	v_bitop3_b32 v4, v23, v4, v8 bitop3:0xde
	v_add_u32_e32 v204, 0, v4
	s_waitcnt vmcnt(8)
	ds_write_b128 v204, v[0:3] offset:32768
	v_bitop3_b32 v0, v32, v33, v42 bitop3:0xde
	v_add_u32_e32 v198, 0, v0
	s_waitcnt lgkmcnt(0)
	s_barrier
	ds_read_b128 v[0:3], v198 offset:32768
	ds_read_b128 v[4:7], v198 offset:40960
	s_waitcnt vmcnt(7) lgkmcnt(1)
	v_mfma_f32_32x32x16_bf16 v[16:31], v[0:3], v[120:123], 0
	ds_read_b128 v[34:37], v200 offset:32768
	ds_read_b128 v[38:41], v200 offset:40960
	s_waitcnt lgkmcnt(2)
	v_mfma_f32_32x32x16_bf16 v[0:15], v[4:7], v[120:123], 0
	s_waitcnt vmcnt(6) lgkmcnt(1)
	v_mfma_f32_32x32x16_bf16 v[16:31], v[34:37], v[124:127], v[16:31]
	v_or_b32_e32 v34, 64, v32
	v_bitop3_b32 v34, v34, v33, v42 bitop3:0xde
	v_add_u32_e32 v199, 0, v34
	s_waitcnt lgkmcnt(0)
	v_mfma_f32_32x32x16_bf16 v[0:15], v[38:41], v[124:127], v[0:15]
	ds_read_b128 v[34:37], v199 offset:32768
	ds_read_b128 v[38:41], v199 offset:40960
	s_waitcnt vmcnt(5) lgkmcnt(1)
	v_mfma_f32_32x32x16_bf16 v[16:31], v[34:37], v[116:119], v[16:31]
	v_or_b32_e32 v34, 0x60, v32
	v_bitop3_b32 v34, v34, v33, v42 bitop3:0xde
	v_add_u32_e32 v193, 0, v34
	s_waitcnt lgkmcnt(0)
	v_mfma_f32_32x32x16_bf16 v[0:15], v[38:41], v[116:119], v[0:15]
	ds_read_b128 v[34:37], v193 offset:32768
	ds_read_b128 v[38:41], v193 offset:40960
	s_waitcnt vmcnt(4) lgkmcnt(1)
	v_mfma_f32_32x32x16_bf16 v[16:31], v[34:37], v[112:115], v[16:31]
	v_or_b32_e32 v34, 0x80, v32
	v_bitop3_b32 v34, v34, v33, v42 bitop3:0xde
	v_add_u32_e32 v192, 0, v34
	s_waitcnt lgkmcnt(0)
	v_mfma_f32_32x32x16_bf16 v[0:15], v[38:41], v[112:115], v[0:15]
	ds_read_b128 v[34:37], v192 offset:32768
	ds_read_b128 v[38:41], v192 offset:40960
	s_waitcnt vmcnt(3) lgkmcnt(1)
	v_mfma_f32_32x32x16_bf16 v[16:31], v[34:37], v[108:111], v[16:31]
	v_or_b32_e32 v34, 0xa0, v32
	v_bitop3_b32 v34, v34, v33, v42 bitop3:0xde
	v_add_u32_e32 v191, 0, v34
	s_waitcnt lgkmcnt(0)
	v_mfma_f32_32x32x16_bf16 v[0:15], v[38:41], v[108:111], v[0:15]
	ds_read_b128 v[34:37], v191 offset:32768
	ds_read_b128 v[38:41], v191 offset:40960
	s_waitcnt vmcnt(2) lgkmcnt(1)
	v_mfma_f32_32x32x16_bf16 v[16:31], v[34:37], v[104:107], v[16:31]
	v_or_b32_e32 v34, 0xc0, v32
	v_bitop3_b32 v34, v34, v33, v42 bitop3:0xde
	v_add_u32_e32 v190, 0, v34
	v_or_b32_e32 v32, 0xe0, v32
	v_bitop3_b32 v32, v32, v33, v42 bitop3:0xde
	v_add_u32_e32 v189, 0, v32
	s_waitcnt lgkmcnt(0)
	v_mfma_f32_32x32x16_bf16 v[0:15], v[38:41], v[104:107], v[0:15]
	ds_read_b128 v[34:37], v190 offset:32768
	ds_read_b128 v[38:41], v190 offset:40960
	s_waitcnt vmcnt(1) lgkmcnt(1)
	v_mfma_f32_32x32x16_bf16 v[16:31], v[34:37], v[100:103], v[16:31]
	s_waitcnt lgkmcnt(0)
	v_mfma_f32_32x32x16_bf16 v[0:15], v[38:41], v[100:103], v[0:15]
	ds_read_b128 v[32:35], v189 offset:32768
	ds_read_b128 v[36:39], v189 offset:40960
	s_waitcnt vmcnt(0) lgkmcnt(1)
	v_mfma_f32_32x32x16_bf16 v[16:31], v[32:35], v[96:99], v[16:31]
	s_waitcnt lgkmcnt(0)
	v_mfma_f32_32x32x16_bf16 v[0:15], v[36:39], v[96:99], v[0:15]
	s_nop 9
	v_max_f32_e32 v32, v17, v17
	v_max_f32_e32 v33, v16, v16
	v_max_f32_e32 v32, v33, v32
	v_max_f32_e32 v33, v25, v25
	v_max_f32_e32 v34, v24, v24
	v_max_f32_e32 v33, v34, v33
	v_max3_f32 v32, v32, v18, v19
	v_max_f32_e32 v34, v9, v9
	v_max_f32_e32 v35, v8, v8
	v_max_f32_e32 v34, v35, v34
	v_max3_f32 v35, v0, v1, v2
	v_max3_f32 v34, v34, v10, v11
	v_max3_f32 v33, v33, v26, v27
	v_max3_f32 v35, v35, v3, v4
	v_max3_f32 v34, v34, v12, v13
	v_max3_f32 v32, v32, v20, v21
	v_max3_f32 v33, v33, v28, v29
	v_max3_f32 v35, v35, v5, v6
	v_max3_f32 v34, v34, v14, v15
	v_max3_f32 v32, v32, v22, v23
	v_max3_f32 v33, v33, v30, v31
	v_max3_f32 v34, v35, v7, v34
	v_max3_f32 v32, v32, v33, v34
	v_mov_b32_e32 v33, v32
	s_nop 1
	v_permlane32_swap_b32_e32 v32, v33
	v_max_f32_e32 v33, v33, v33
	v_max_f32_e32 v32, v32, v32
	v_max_f32_e32 v32, v32, v33
	v_add_f32_e32 v33, 0x7149f2ca, v32
	v_max_f32_e32 v32, 0xf149f2ca, v32
	v_cmp_ge_f32_e32 vcc, s31, v33
	v_sub_f32_e32 v33, 0xf149f2ca, v32
	v_mul_f32_e32 v33, 0x3e0293ee, v33
	s_cmp_eq_u64 vcc, exec
	v_exp_f32_e32 v33, v33
	s_cselect_b64 vcc, -1, 0
	v_cndmask_b32_e32 v206, v32, v230, vcc
	s_add_u32 s2, s8, s76
	v_mul_f32_e32 v32, 0xbe0293ee, v206
	s_addc_u32 s3, s9, s77
	v_cndmask_b32_e64 v205, v33, 1.0, vcc
	v_mov_b32_e32 v33, v32
	s_add_u32 s10, s6, s76
	v_fmac_f32_e32 v33, 0x3e0293ee, v31
	s_addc_u32 s11, s7, s77
	v_pk_fma_f32 v[146:147], v[14:15], s[52:53], v[32:33] op_sel_hi:[1,0,0]
	v_pk_fma_f32 v[148:149], v[12:13], s[52:53], v[32:33] op_sel_hi:[1,0,0]
	v_pk_fma_f32 v[150:151], v[10:11], s[52:53], v[32:33] op_sel_hi:[1,0,0]
	v_pk_fma_f32 v[152:153], v[8:9], s[52:53], v[32:33] op_sel_hi:[1,0,0]
	v_pk_fma_f32 v[154:155], v[6:7], s[52:53], v[32:33] op_sel_hi:[1,0,0]
	v_pk_fma_f32 v[156:157], v[4:5], s[52:53], v[32:33] op_sel_hi:[1,0,0]
	v_pk_fma_f32 v[158:159], v[2:3], s[52:53], v[32:33] op_sel_hi:[1,0,0]
	v_pk_fma_f32 v[160:161], v[0:1], s[52:53], v[32:33] op_sel_hi:[1,0,0]
	global_load_dwordx4 v[0:3], v128, s[2:3]
	global_load_dwordx4 v[4:7], v178, s[2:3]
	global_load_dwordx4 v[8:11], v128, s[10:11]
	global_load_dwordx4 v[12:15], v178, s[10:11]
	s_add_u32 s2, s2, s76
	s_addc_u32 s3, s3, s77
	s_add_u32 s10, s10, s76
	s_addc_u32 s11, s11, s77
	global_load_dwordx4 v[130:133], v128, s[2:3]
	global_load_dwordx4 v[134:137], v178, s[2:3]
	global_load_dwordx4 v[138:141], v128, s[10:11]
	global_load_dwordx4 v[142:145], v178, s[10:11]
	v_fmamk_f32 v16, v16, 0x3e0293ee, v32
	v_fmamk_f32 v17, v17, 0x3e0293ee, v32
	v_fmamk_f32 v18, v18, 0x3e0293ee, v32
	v_fmamk_f32 v19, v19, 0x3e0293ee, v32
	v_fmamk_f32 v20, v20, 0x3e0293ee, v32
	v_fmamk_f32 v21, v21, 0x3e0293ee, v32
	v_fmamk_f32 v22, v22, 0x3e0293ee, v32
	v_fmamk_f32 v23, v23, 0x3e0293ee, v32
	v_fmamk_f32 v24, v24, 0x3e0293ee, v32
	v_fmamk_f32 v25, v25, 0x3e0293ee, v32
	v_fmamk_f32 v26, v26, 0x3e0293ee, v32
	v_fmamk_f32 v27, v27, 0x3e0293ee, v32
	v_fmamk_f32 v28, v28, 0x3e0293ee, v32
	v_fmamk_f32 v29, v29, 0x3e0293ee, v32
	v_fmamk_f32 v30, v30, 0x3e0293ee, v32
	v_exp_f32_e32 v176, v16
	v_exp_f32_e32 v211, v17
	v_exp_f32_e32 v163, v18
	v_exp_f32_e32 v177, v19
	v_exp_f32_e32 v164, v20
	v_exp_f32_e32 v175, v21
	v_exp_f32_e32 v165, v22
	v_exp_f32_e32 v174, v23
	v_exp_f32_e32 v166, v24
	v_exp_f32_e32 v173, v25
	v_exp_f32_e32 v167, v26
	v_exp_f32_e32 v172, v27
	v_exp_f32_e32 v168, v28
	v_exp_f32_e32 v171, v29
	v_exp_f32_e32 v169, v30
	v_exp_f32_e32 v170, v33
	s_waitcnt vmcnt(4)
	s_waitcnt vmcnt(7)
	ds_write_b128 v201, v[0:3] offset:16384
	s_waitcnt vmcnt(6)
	ds_write_b128 v202, v[4:7] offset:16384
	s_waitcnt vmcnt(5)
	ds_write_b128 v203, v[8:11] offset:49152
	s_waitcnt vmcnt(4)
	ds_write_b128 v204, v[12:15] offset:49152
	v_mov_b32_e32 v15, 0
	s_cmp_lt_i32 s19, 3
	s_waitcnt lgkmcnt(0)
	s_barrier
	s_cbranch_scc1 .LBB0_838
	s_add_i32 s20, s17, -4
	s_add_i32 s21, s19, -1
	s_cmp_lg_u32 0, -1
	s_cselect_b32 s2, 0, 0
	s_addk_i32 s2, 0x4000
	s_movk_i32 s3, 0x7c
	v_add_u32_e32 v207, s2, v181
	s_mul_i32 s2, s17, 0x7c
	v_mul_lo_u32 v0, v184, s3
	v_sub_u32_e32 v0, s2, v0
	s_add_i32 s2, 0, 0x14a2c
	v_mov_b32_e32 v187, 0
	v_mov_b32_e32 v179, v129
	v_add_u32_e32 v208, s2, v0
	s_mov_b32 s23, 4
	s_movk_i32 s22, 0xc0
	v_mov_b32_e32 v48, 0
	v_mov_b32_e32 v49, v187
	v_mov_b32_e32 v50, v187
	v_mov_b32_e32 v51, v187
	v_mov_b32_e32 v52, v187
	v_mov_b32_e32 v53, v187
	v_mov_b32_e32 v54, v187
	v_mov_b32_e32 v55, v187
	v_mov_b32_e32 v56, v187
	v_mov_b32_e32 v57, v187
	v_mov_b32_e32 v58, v187
	v_mov_b32_e32 v59, v187
	v_mov_b32_e32 v60, v187
	v_mov_b32_e32 v61, v187
	v_mov_b32_e32 v62, v187
	v_mov_b32_e32 v63, v187
	v_mov_b32_e32 v32, 0
	v_mov_b32_e32 v33, v187
	v_mov_b32_e32 v34, v187
	v_mov_b32_e32 v35, v187
	v_mov_b32_e32 v36, v187
	v_mov_b32_e32 v37, v187
	v_mov_b32_e32 v38, v187
	v_mov_b32_e32 v39, v187
	v_mov_b32_e32 v40, v187
	v_mov_b32_e32 v41, v187
	v_mov_b32_e32 v42, v187
	v_mov_b32_e32 v43, v187
	v_mov_b32_e32 v44, v187
	v_mov_b32_e32 v45, v187
	v_mov_b32_e32 v46, v187
	v_mov_b32_e32 v47, v187
	v_mov_b32_e32 v16, 0
	v_mov_b32_e32 v17, v187
	v_mov_b32_e32 v18, v187
	v_mov_b32_e32 v19, v187
	v_mov_b32_e32 v20, v187
	v_mov_b32_e32 v21, v187
	v_mov_b32_e32 v22, v187
	v_mov_b32_e32 v23, v187
	v_mov_b32_e32 v24, v187
	v_mov_b32_e32 v25, v187
	v_mov_b32_e32 v26, v187
	v_mov_b32_e32 v27, v187
	v_mov_b32_e32 v28, v187
	v_mov_b32_e32 v29, v187
	v_mov_b32_e32 v30, v187
	v_mov_b32_e32 v31, v187
	v_mov_b32_e32 v0, 0
	v_mov_b32_e32 v1, v187
	v_mov_b32_e32 v2, v187
	v_mov_b32_e32 v3, v187
	v_mov_b32_e32 v4, v187
	v_mov_b32_e32 v5, v187
	v_mov_b32_e32 v6, v187
	v_mov_b32_e32 v7, v187
	v_mov_b32_e32 v8, v187
	v_mov_b32_e32 v9, v187
	v_mov_b32_e32 v10, v187
	v_mov_b32_e32 v11, v187
	v_mov_b32_e32 v12, v187
	v_mov_b32_e32 v13, v187
	v_mov_b32_e32 v14, v187
	v_mov_b32_e32 v15, v187
.LBB0_814:
	s_add_i32 s24, s23, -3
	ds_read_b128 v[64:67], v198 offset:49152
	ds_read_b128 v[68:71], v198 offset:57344
	ds_read_b128 v[212:215], v200 offset:49152
	ds_read_b128 v[216:219], v200 offset:57344
	v_exp_f32_e32 v160, v160
	v_exp_f32_e32 v161, v161
	s_waitcnt lgkmcnt(3)
	v_mfma_f32_32x32x16_bf16 v[80:95], v[64:67], v[120:123], 0
	v_exp_f32_e32 v152, v152
	v_exp_f32_e32 v153, v153
	v_exp_f32_e32 v158, v158
	v_exp_f32_e32 v150, v150
	v_exp_f32_e32 v159, v159
	v_exp_f32_e32 v151, v151
	v_exp_f32_e32 v156, v156
	s_waitcnt lgkmcnt(2)
	v_mfma_f32_32x32x16_bf16 v[64:79], v[68:71], v[120:123], 0
	v_exp_f32_e32 v148, v148
	v_exp_f32_e32 v157, v157
	v_exp_f32_e32 v149, v149
	v_add_f32_e32 v162, v176, v211
	v_add_f32_e32 v180, v166, v173
	v_add_f32_e32 v194, v160, v161
	v_add_f32_e32 v195, v152, v153
	s_waitcnt lgkmcnt(1)
	v_mfma_f32_32x32x16_bf16 v[80:95], v[212:215], v[124:127], v[80:95]
	v_exp_f32_e32 v154, v154
	v_exp_f32_e32 v146, v146
	v_add_f32_e32 v162, v163, v162
	v_add_f32_e32 v180, v167, v180
	v_add_f32_e32 v194, v158, v194
	v_add_f32_e32 v195, v150, v195
	v_exp_f32_e32 v155, v155
	s_waitcnt lgkmcnt(0)
	v_mfma_f32_32x32x16_bf16 v[64:79], v[216:219], v[124:127], v[64:79]
	ds_read_b128 v[212:215], v199 offset:49152
	ds_read_b128 v[216:219], v199 offset:57344
	v_exp_f32_e32 v147, v147
	v_add_f32_e32 v162, v177, v162
	v_add_f32_e32 v180, v172, v180
	v_add_f32_e32 v194, v159, v194
	v_add_f32_e32 v195, v151, v195
	v_add_f32_e32 v162, v164, v162
	s_waitcnt lgkmcnt(1)
	v_mfma_f32_32x32x16_bf16 v[80:95], v[212:215], v[116:119], v[80:95]
	v_add_f32_e32 v180, v168, v180
	v_add_f32_e32 v194, v156, v194
	v_add_f32_e32 v195, v148, v195
	v_add_f32_e32 v162, v175, v162
	v_add_f32_e32 v180, v171, v180
	v_add_f32_e32 v194, v157, v194
	v_add_f32_e32 v195, v149, v195
	s_waitcnt lgkmcnt(0)
	v_mfma_f32_32x32x16_bf16 v[64:79], v[216:219], v[116:119], v[64:79]
	ds_read_b128 v[212:215], v193 offset:49152
	ds_read_b128 v[216:219], v193 offset:57344
	v_add_f32_e32 v162, v165, v162
	v_add_f32_e32 v180, v169, v180
	v_add_f32_e32 v194, v154, v194
	v_add_f32_e32 v195, v146, v195
	v_add_f32_e32 v162, v174, v162
	s_waitcnt lgkmcnt(1)
	v_mfma_f32_32x32x16_bf16 v[80:95], v[212:215], v[112:115], v[80:95]
	v_add_f32_e32 v180, v170, v180
	v_add_f32_e32 v194, v155, v194
	v_add_f32_e32 v195, v147, v195
	v_add_f32_e32 v162, v180, v162
	v_add_f32_e32 v180, v195, v194
	v_add_f32_e32 v209, v162, v180
	v_mov_b32_e32 v210, v209
	s_waitcnt lgkmcnt(0)
	v_mfma_f32_32x32x16_bf16 v[64:79], v[216:219], v[112:115], v[64:79]
	ds_read_b128 v[212:215], v192 offset:49152
	ds_read_b128 v[216:219], v192 offset:57344
	v_permlane32_swap_b32_e32 v209, v210
	s_waitcnt lgkmcnt(1)
	v_mfma_f32_32x32x16_bf16 v[80:95], v[212:215], v[108:111], v[80:95]
	s_waitcnt lgkmcnt(0)
	v_mfma_f32_32x32x16_bf16 v[64:79], v[216:219], v[108:111], v[64:79]
	ds_read_b128 v[212:215], v191 offset:49152
	ds_read_b128 v[216:219], v191 offset:57344
	s_waitcnt lgkmcnt(1)
	v_mfma_f32_32x32x16_bf16 v[80:95], v[212:215], v[104:107], v[80:95]
	s_waitcnt lgkmcnt(0)
	v_mfma_f32_32x32x16_bf16 v[64:79], v[216:219], v[104:107], v[64:79]
	ds_read_b128 v[212:215], v190 offset:49152
	ds_read_b128 v[216:219], v190 offset:57344
	s_waitcnt lgkmcnt(1)
	v_mfma_f32_32x32x16_bf16 v[80:95], v[212:215], v[100:103], v[80:95]
	s_waitcnt lgkmcnt(0)
	v_mfma_f32_32x32x16_bf16 v[64:79], v[216:219], v[100:103], v[64:79]
	ds_read_b128 v[212:215], v189 offset:49152
	ds_read_b128 v[216:219], v189 offset:57344
	v_cvt_pk_bf16_f32 v162, v176, v211
	v_cvt_pk_bf16_f32 v163, v163, v177
	v_cvt_pk_bf16_f32 v164, v164, v175
	v_cvt_pk_bf16_f32 v165, v165, v174
	v_cvt_pk_bf16_f32 v166, v166, v173
	v_cvt_pk_bf16_f32 v167, v167, v172
	s_waitcnt lgkmcnt(1)
	v_mfma_f32_32x32x16_bf16 v[80:95], v[212:215], v[96:99], v[80:95]
	v_cvt_pk_bf16_f32 v168, v168, v171
	v_cvt_pk_bf16_f32 v169, v169, v170
	v_cvt_pk_bf16_f32 v170, v160, v161
	v_cvt_pk_bf16_f32 v171, v158, v159
	v_cvt_pk_bf16_f32 v172, v156, v157
	v_cvt_pk_bf16_f32 v173, v154, v155
	v_cvt_pk_bf16_f32 v174, v152, v153
	s_waitcnt lgkmcnt(0)
	v_mfma_f32_32x32x16_bf16 v[64:79], v[216:219], v[96:99], v[64:79]
	v_cvt_pk_bf16_f32 v175, v150, v151
	v_cvt_pk_bf16_f32 v176, v148, v149
	v_cvt_pk_bf16_f32 v177, v146, v147
	s_cmp_gt_u32 s24, 1
	s_mov_b64 s[10:11], -1
	s_cbranch_scc0 .LBB0_816
	s_add_i32 s25, s17, s23
	s_add_i32 s2, s25, -5
	s_min_i32 s2, s2, s18
	s_lshl_b32 s2, s2, 6
	s_addk_i32 s2, 0x100
	s_mov_b64 s[10:11], 0

.LBB0_825:
	v_cndmask_b32_e64 v206, v65, v206, s[58:59]
	v_mul_f32_e32 v138, 0xbe0293ee, v206
	v_fmamk_f32 v65, v162, 0x3e0293ee, v138
	v_fmamk_f32 v66, v163, 0x3e0293ee, v138
	v_fmamk_f32 v67, v164, 0x3e0293ee, v138
	v_fmamk_f32 v68, v165, 0x3e0293ee, v138
	v_fmamk_f32 v69, v166, 0x3e0293ee, v138
	v_fmamk_f32 v70, v167, 0x3e0293ee, v138
	v_fmamk_f32 v73, v168, 0x3e0293ee, v138
	v_fmamk_f32 v74, v169, 0x3e0293ee, v138
	v_fmamk_f32 v75, v170, 0x3e0293ee, v138
	v_fmamk_f32 v76, v171, 0x3e0293ee, v138
	v_fmamk_f32 v77, v172, 0x3e0293ee, v138
	v_fmamk_f32 v78, v173, 0x3e0293ee, v138
	v_fmamk_f32 v80, v174, 0x3e0293ee, v138
	v_fmamk_f32 v81, v175, 0x3e0293ee, v138
	v_fmamk_f32 v82, v176, 0x3e0293ee, v138
	v_fmamk_f32 v83, v177, 0x3e0293ee, v138
	v_exp_f32_e32 v170, v65
	v_exp_f32_e32 v171, v66
	v_exp_f32_e32 v172, v67
	v_exp_f32_e32 v173, v68
	v_exp_f32_e32 v174, v69
	v_exp_f32_e32 v175, v70
	v_exp_f32_e32 v176, v73
	v_exp_f32_e32 v177, v74
	v_fmamk_f32 v162, v71, 0x3e0293ee, v138
	v_fmamk_f32 v163, v72, 0x3e0293ee, v138
	v_fmamk_f32 v164, v217, 0x3e0293ee, v138
	v_fmamk_f32 v165, v218, 0x3e0293ee, v138
	v_fmamk_f32 v166, v219, 0x3e0293ee, v138
	v_fmamk_f32 v167, v220, 0x3e0293ee, v138
	v_fmamk_f32 v168, v221, 0x3e0293ee, v138
	v_fmamk_f32 v169, v222, 0x3e0293ee, v138
	v_fmamk_f32 v139, v64, 0x3e0293ee, v138
	v_fmamk_f32 v140, v211, 0x3e0293ee, v138
	v_fmamk_f32 v141, v212, 0x3e0293ee, v138
	v_fmamk_f32 v142, v213, 0x3e0293ee, v138
	v_fmamk_f32 v143, v214, 0x3e0293ee, v138
	v_fmamk_f32 v144, v215, 0x3e0293ee, v138
	v_fmamk_f32 v145, v216, 0x3e0293ee, v138
	v_fmac_f32_e32 v138, 0x3e0293ee, v79
	v_exp_f32_e32 v194, v75
	v_exp_f32_e32 v195, v76
	v_exp_f32_e32 v196, v77
	v_exp_f32_e32 v197, v78
	v_exp_f32_e32 v211, v80
	v_exp_f32_e32 v214, v81
	v_exp_f32_e32 v215, v82
	v_exp_f32_e32 v216, v83
	s_waitcnt lgkmcnt(0)
	s_barrier
	ds_read_b128 v[64:67], v198 offset:32768
	ds_read_b128 v[68:71], v198 offset:40960
	ds_read_b128 v[130:133], v200 offset:32768
	ds_read_b128 v[134:137], v200 offset:40960
	v_exp_f32_e32 v138, v138
	s_waitcnt lgkmcnt(3)
	v_mfma_f32_32x32x16_bf16 v[80:95], v[64:67], v[120:123], 0
	s_waitcnt lgkmcnt(2)
	v_mfma_f32_32x32x16_bf16 v[64:79], v[68:71], v[120:123], 0
	s_waitcnt lgkmcnt(1)
	v_mfma_f32_32x32x16_bf16 v[80:95], v[130:133], v[124:127], v[80:95]
	s_waitcnt lgkmcnt(0)
	v_mfma_f32_32x32x16_bf16 v[64:79], v[134:137], v[124:127], v[64:79]
	ds_read_b128 v[130:133], v199 offset:32768
	ds_read_b128 v[134:137], v199 offset:40960
	s_waitcnt lgkmcnt(1)
	v_mfma_f32_32x32x16_bf16 v[80:95], v[130:133], v[116:119], v[80:95]
	s_waitcnt lgkmcnt(0)
	v_mfma_f32_32x32x16_bf16 v[64:79], v[134:137], v[116:119], v[64:79]
	ds_read_b128 v[130:133], v193 offset:32768
	ds_read_b128 v[134:137], v193 offset:40960
	s_waitcnt lgkmcnt(1)
	v_mfma_f32_32x32x16_bf16 v[80:95], v[130:133], v[112:115], v[80:95]
	s_waitcnt lgkmcnt(0)
	v_mfma_f32_32x32x16_bf16 v[64:79], v[134:137], v[112:115], v[64:79]
	ds_read_b128 v[130:133], v192 offset:32768
	ds_read_b128 v[134:137], v192 offset:40960
	s_waitcnt lgkmcnt(1)
	v_mfma_f32_32x32x16_bf16 v[80:95], v[130:133], v[108:111], v[80:95]
	s_waitcnt lgkmcnt(0)
	v_mfma_f32_32x32x16_bf16 v[64:79], v[134:137], v[108:111], v[64:79]
	ds_read_b128 v[130:133], v191 offset:32768
	ds_read_b128 v[134:137], v191 offset:40960
	s_waitcnt lgkmcnt(1)
	v_mfma_f32_32x32x16_bf16 v[80:95], v[130:133], v[104:107], v[80:95]
	s_waitcnt lgkmcnt(0)
	v_mfma_f32_32x32x16_bf16 v[64:79], v[134:137], v[104:107], v[64:79]
	ds_read_b128 v[130:133], v190 offset:32768
	ds_read_b128 v[134:137], v190 offset:40960
	s_waitcnt lgkmcnt(1)
	v_mfma_f32_32x32x16_bf16 v[80:95], v[130:133], v[100:103], v[80:95]
	s_waitcnt lgkmcnt(0)
	v_mfma_f32_32x32x16_bf16 v[64:79], v[134:137], v[100:103], v[64:79]
	ds_read_b128 v[130:133], v189 offset:32768
	ds_read_b128 v[134:137], v189 offset:40960
	s_waitcnt lgkmcnt(1)
	v_mfma_f32_32x32x16_bf16 v[80:95], v[130:133], v[96:99], v[80:95]
	v_exp_f32_e32 v130, v139
	v_exp_f32_e32 v131, v140
	v_exp_f32_e32 v139, v163
	v_exp_f32_e32 v140, v164
	v_exp_f32_e32 v132, v141
	v_exp_f32_e32 v141, v165
	v_exp_f32_e32 v133, v142
	v_exp_f32_e32 v142, v166
	s_waitcnt lgkmcnt(0)
	v_mfma_f32_32x32x16_bf16 v[64:79], v[134:137], v[96:99], v[64:79]
	v_exp_f32_e32 v134, v143
	v_exp_f32_e32 v143, v167
	v_exp_f32_e32 v135, v144
	v_exp_f32_e32 v137, v162
	v_exp_f32_e32 v144, v168
	v_add_f32_e32 v162, v170, v171
	v_add_f32_e32 v163, v194, v195
	v_add_f32_e32 v164, v130, v131
	v_add_f32_e32 v165, v139, v140
	v_exp_f32_e32 v136, v145
	v_exp_f32_e32 v145, v169
	v_add_f32_e32 v162, v172, v162
	v_add_f32_e32 v163, v196, v163
	v_add_f32_e32 v164, v132, v164
	v_add_f32_e32 v165, v141, v165
	v_add_f32_e32 v162, v173, v162
	v_add_f32_e32 v163, v197, v163
	v_add_f32_e32 v164, v133, v164
	v_add_f32_e32 v165, v142, v165
	v_add_f32_e32 v162, v174, v162
	v_add_f32_e32 v163, v211, v163
	v_add_f32_e32 v164, v134, v164
	v_add_f32_e32 v165, v143, v165
	v_add_f32_e32 v162, v175, v162
	v_add_f32_e32 v163, v214, v163
	v_add_f32_e32 v164, v135, v164
	v_add_f32_e32 v165, v144, v165
	v_add_f32_e32 v162, v176, v162
	v_add_f32_e32 v163, v215, v163
	v_add_f32_e32 v164, v136, v164
	v_add_f32_e32 v165, v145, v165
	v_add_f32_e32 v162, v177, v162
	v_add_f32_e32 v163, v216, v163
	v_add_f32_e32 v164, v137, v164
	v_add_f32_e32 v165, v138, v165
	v_add_f32_e32 v162, v163, v162
	v_add_f32_e32 v163, v165, v164
	v_add_f32_e32 v212, v163, v162
	v_mov_b32_e32 v213, v212
	v_cvt_pk_bf16_f32 v162, v170, v171
	v_cvt_pk_bf16_f32 v163, v172, v173
	v_cvt_pk_bf16_f32 v164, v174, v175
	v_cvt_pk_bf16_f32 v165, v176, v177
	v_cvt_pk_bf16_f32 v166, v194, v195
	v_cvt_pk_bf16_f32 v167, v196, v197
	v_cvt_pk_bf16_f32 v168, v211, v214
	v_cvt_pk_bf16_f32 v169, v215, v216
	v_cvt_pk_bf16_f32 v170, v130, v131
	v_cvt_pk_bf16_f32 v171, v132, v133
	v_cvt_pk_bf16_f32 v172, v134, v135
	v_cvt_pk_bf16_f32 v173, v136, v137
	v_cvt_pk_bf16_f32 v174, v139, v140
	v_cvt_pk_bf16_f32 v175, v141, v142
	v_cvt_pk_bf16_f32 v176, v143, v144
	v_cvt_pk_bf16_f32 v177, v145, v138
	s_nop 1
	v_permlane32_swap_b32_e32 v212, v213
	s_min_i32 s3, s23, s21
	s_cmp_gt_i32 s3, 3
	s_mov_b64 s[10:11], -1
	s_cbranch_scc0 .LBB0_827
	s_add_i32 s2, s3, s20
	s_min_i32 s2, s2, s18
	s_lshl_b32 s2, s2, 6
	s_addk_i32 s2, 0x100
	s_mov_b64 s[10:11], 0

.LBB0_839:
	ds_read_b128 v[64:67], v198 offset:49152
	ds_read_b128 v[68:71], v198 offset:57344
	s_waitcnt lgkmcnt(1)
	v_mfma_f32_32x32x16_bf16 v[80:95], v[64:67], v[120:123], 0
	s_waitcnt lgkmcnt(0)
	v_mfma_f32_32x32x16_bf16 v[64:79], v[68:71], v[120:123], 0
	ds_read_b128 v[120:123], v200 offset:49152
	s_waitcnt vmcnt(3)
	ds_read_b128 v[130:133], v200 offset:57344
	s_waitcnt lgkmcnt(0)
	v_mfma_f32_32x32x16_bf16 v[64:79], v[130:133], v[124:127], v[64:79]
	v_mfma_f32_32x32x16_bf16 v[80:95], v[120:123], v[124:127], v[80:95]
	ds_read_b128 v[120:123], v199 offset:49152
	ds_read_b128 v[124:127], v199 offset:57344
	s_waitcnt lgkmcnt(0)
	v_mfma_f32_32x32x16_bf16 v[64:79], v[124:127], v[116:119], v[64:79]
	v_mfma_f32_32x32x16_bf16 v[80:95], v[120:123], v[116:119], v[80:95]
	ds_read_b128 v[116:119], v193 offset:49152
	ds_read_b128 v[120:123], v193 offset:57344
	s_waitcnt lgkmcnt(0)
	v_mfma_f32_32x32x16_bf16 v[64:79], v[120:123], v[112:115], v[64:79]
	v_exp_f32_e32 v120, v146
	v_exp_f32_e32 v121, v147
	v_mfma_f32_32x32x16_bf16 v[80:95], v[116:119], v[112:115], v[80:95]
	ds_read_b128 v[112:115], v192 offset:49152
	ds_read_b128 v[116:119], v192 offset:57344
	s_waitcnt lgkmcnt(0)
	v_mfma_f32_32x32x16_bf16 v[64:79], v[116:119], v[108:111], v[64:79]
	v_exp_f32_e32 v116, v150
	v_exp_f32_e32 v117, v151
	v_exp_f32_e32 v118, v148
	v_exp_f32_e32 v119, v149
	v_mfma_f32_32x32x16_bf16 v[80:95], v[112:115], v[108:111], v[80:95]
	ds_read_b128 v[108:111], v191 offset:49152
	ds_read_b128 v[112:115], v191 offset:57344
	s_waitcnt lgkmcnt(0)
	v_mfma_f32_32x32x16_bf16 v[64:79], v[112:115], v[104:107], v[64:79]
	v_exp_f32_e32 v114, v152
	v_exp_f32_e32 v115, v153
	v_exp_f32_e32 v112, v154
	v_exp_f32_e32 v113, v155
	v_mfma_f32_32x32x16_bf16 v[80:95], v[108:111], v[104:107], v[80:95]
	ds_read_b128 v[104:107], v190 offset:49152
	ds_read_b128 v[108:111], v190 offset:57344
	s_waitcnt lgkmcnt(0)
	v_mfma_f32_32x32x16_bf16 v[64:79], v[108:111], v[100:103], v[64:79]
	v_exp_f32_e32 v108, v158
	v_exp_f32_e32 v109, v159
	v_exp_f32_e32 v110, v156
	v_exp_f32_e32 v111, v157
	v_mfma_f32_32x32x16_bf16 v[80:95], v[104:107], v[100:103], v[80:95]
	ds_read_b128 v[100:103], v189 offset:49152
	ds_read_b128 v[104:107], v189 offset:57344
	s_waitcnt lgkmcnt(0)
	v_mfma_f32_32x32x16_bf16 v[64:79], v[104:107], v[96:99], v[64:79]
	v_exp_f32_e32 v106, v160
	v_exp_f32_e32 v107, v161
	v_mfma_f32_32x32x16_bf16 v[80:95], v[100:103], v[96:99], v[80:95]
	v_add_f32_e32 v96, v176, v211
	v_add_f32_e32 v97, v166, v173
	v_add_f32_e32 v98, v106, v107
	v_add_f32_e32 v99, v114, v115
	v_add_f32_e32 v96, v163, v96
	v_add_f32_e32 v97, v167, v97
	v_add_f32_e32 v98, v108, v98
	v_add_f32_e32 v99, v116, v99
	v_add_f32_e32 v96, v177, v96
	v_add_f32_e32 v97, v172, v97
	v_add_f32_e32 v98, v109, v98
	v_add_f32_e32 v99, v117, v99
	v_add_f32_e32 v96, v164, v96
	v_add_f32_e32 v97, v168, v97
	v_add_f32_e32 v98, v110, v98
	v_add_f32_e32 v99, v118, v99
	v_add_f32_e32 v96, v175, v96
	v_add_f32_e32 v97, v171, v97
	v_add_f32_e32 v98, v111, v98
	v_add_f32_e32 v99, v119, v99
	v_add_f32_e32 v96, v165, v96
	v_add_f32_e32 v97, v169, v97
	v_add_f32_e32 v98, v112, v98
	v_add_f32_e32 v99, v120, v99
	v_add_f32_e32 v96, v174, v96
	v_add_f32_e32 v97, v170, v97
	v_add_f32_e32 v98, v113, v98
	v_add_f32_e32 v99, v121, v99
	v_add_f32_e32 v96, v97, v96
	v_add_f32_e32 v97, v99, v98
	v_add_f32_e32 v100, v97, v96
	v_mov_b32_e32 v101, v100
	s_nop 1
	v_permlane32_swap_b32_e32 v100, v101
	v_cvt_pk_bf16_f32 v96, v176, v211
	v_cvt_pk_bf16_f32 v97, v163, v177
	v_cvt_pk_bf16_f32 v98, v164, v175
	v_cvt_pk_bf16_f32 v99, v165, v174
	v_cvt_pk_bf16_f32 v102, v166, v173
	v_cvt_pk_bf16_f32 v103, v167, v172
	v_cvt_pk_bf16_f32 v104, v168, v171
	v_cvt_pk_bf16_f32 v105, v169, v170
	v_cvt_pk_bf16_f32 v106, v106, v107
	v_cvt_pk_bf16_f32 v107, v108, v109
	v_cvt_pk_bf16_f32 v108, v110, v111
	v_cvt_pk_bf16_f32 v109, v112, v113
	v_cvt_pk_bf16_f32 v110, v114, v115
	v_cvt_pk_bf16_f32 v111, v116, v117
	v_cvt_pk_bf16_f32 v112, v118, v119
	v_cvt_pk_bf16_f32 v113, v120, v121
	ds_read_b64_tr_b16 v[114:115], v186 offset:0
	ds_read_b64_tr_b16 v[116:117], v186 offset:0x800
	ds_read_b64_tr_b16 v[118:119], v186 offset:0x1000
	ds_read_b64_tr_b16 v[120:121], v186 offset:0x1800
	ds_read_b64_tr_b16 v[122:123], v186 offset:0x2000
	ds_read_b64_tr_b16 v[124:125], v186 offset:0x2800
	ds_read_b64_tr_b16 v[130:131], v186 offset:0x3000
	ds_read_b64_tr_b16 v[132:133], v186 offset:0x3800
	s_waitcnt lgkmcnt(0)
	s_cmp_lt_i32 s19, 5
	v_mfma_f32_32x32x16_bf16 v[48:63], v[114:117], v[96:99], v[48:63]
	ds_read_b64_tr_b16 v[114:115], v186 offset:0x200
	ds_read_b64_tr_b16 v[116:117], v186 offset:0xa00
	v_mfma_f32_32x32x16_bf16 v[48:63], v[118:121], v[102:105], v[48:63]
	ds_read_b64_tr_b16 v[118:119], v186 offset:0x1200
	ds_read_b64_tr_b16 v[120:121], v186 offset:0x1a00
	v_mfma_f32_32x32x16_bf16 v[48:63], v[122:125], v[106:109], v[48:63]
	ds_read_b64_tr_b16 v[122:123], v186 offset:0x2200
	ds_read_b64_tr_b16 v[124:125], v186 offset:0x2a00
	v_mfma_f32_32x32x16_bf16 v[48:63], v[130:133], v[110:113], v[48:63]
	ds_read_b64_tr_b16 v[130:131], v186 offset:0x3200
	ds_read_b64_tr_b16 v[132:133], v186 offset:0x3a00
	s_waitcnt lgkmcnt(0)
	v_mfma_f32_32x32x16_bf16 v[32:47], v[114:117], v[96:99], v[32:47]
	ds_read_b64_tr_b16 v[114:115], v186 offset:0x400
	ds_read_b64_tr_b16 v[116:117], v186 offset:0xc00
	v_mfma_f32_32x32x16_bf16 v[32:47], v[118:121], v[102:105], v[32:47]
	ds_read_b64_tr_b16 v[118:119], v186 offset:0x1400
	ds_read_b64_tr_b16 v[120:121], v186 offset:0x1c00
	v_mfma_f32_32x32x16_bf16 v[32:47], v[122:125], v[106:109], v[32:47]
	ds_read_b64_tr_b16 v[122:123], v186 offset:0x2400
	ds_read_b64_tr_b16 v[124:125], v186 offset:0x2c00
	v_mfma_f32_32x32x16_bf16 v[32:47], v[130:133], v[110:113], v[32:47]
	ds_read_b64_tr_b16 v[130:131], v186 offset:0x3400
	ds_read_b64_tr_b16 v[132:133], v186 offset:0x3c00
	s_waitcnt lgkmcnt(0)
	v_mfma_f32_32x32x16_bf16 v[16:31], v[114:117], v[96:99], v[16:31]
	ds_read_b64_tr_b16 v[114:115], v186 offset:0x600
	ds_read_b64_tr_b16 v[116:117], v186 offset:0xe00
	v_mfma_f32_32x32x16_bf16 v[16:31], v[118:121], v[102:105], v[16:31]
	ds_read_b64_tr_b16 v[118:119], v186 offset:0x1600
	ds_read_b64_tr_b16 v[120:121], v186 offset:0x1e00
	v_mfma_f32_32x32x16_bf16 v[16:31], v[122:125], v[106:109], v[16:31]
	ds_read_b64_tr_b16 v[122:123], v186 offset:0x2600
	ds_read_b64_tr_b16 v[124:125], v186 offset:0x2e00
	v_mfma_f32_32x32x16_bf16 v[16:31], v[130:133], v[110:113], v[16:31]
	ds_read_b64_tr_b16 v[130:131], v186 offset:0x3600
	ds_read_b64_tr_b16 v[132:133], v186 offset:0x3e00
	s_waitcnt lgkmcnt(0)
	v_mfma_f32_32x32x16_bf16 v[0:15], v[114:117], v[96:99], v[0:15]
	v_mfma_f32_32x32x16_bf16 v[0:15], v[118:121], v[102:105], v[0:15]
	v_mfma_f32_32x32x16_bf16 v[0:15], v[122:125], v[106:109], v[0:15]
	v_mfma_f32_32x32x16_bf16 v[0:15], v[130:133], v[110:113], v[0:15]
	s_cbranch_scc1 .LBB0_843
	s_add_i32 s2, s19, s17
	s_add_i32 s2, s2, -5
	v_min_i32_e32 v96, s18, v188
	v_cmp_ge_i32_e32 vcc, s2, v185
	v_cmp_le_i32_e64 s[58:59], s2, v96
	s_and_b64 s[8:9], s[58:59], vcc
	v_mov_b32_e32 v113, 0xf149f2ca
	v_mov_b32_e32 v112, 0xf149f2ca
	v_mov_b32_e32 v111, 0xf149f2ca
	v_mov_b32_e32 v110, 0xf149f2ca
	v_mov_b32_e32 v109, 0xf149f2ca
	v_mov_b32_e32 v108, 0xf149f2ca
	v_mov_b32_e32 v107, 0xf149f2ca
	v_mov_b32_e32 v106, 0xf149f2ca
	v_mov_b32_e32 v105, 0xf149f2ca
	v_mov_b32_e32 v104, 0xf149f2ca
	v_mov_b32_e32 v103, 0xf149f2ca
	v_mov_b32_e32 v102, 0xf149f2ca
	v_mov_b32_e32 v99, 0xf149f2ca
	v_mov_b32_e32 v98, 0xf149f2ca
	v_mov_b32_e32 v97, 0xf149f2ca
	v_mov_b32_e32 v96, 0xf149f2ca
	v_mov_b32_e32 v130, 0xf149f2ca
	v_mov_b32_e32 v125, 0xf149f2ca
	v_mov_b32_e32 v124, 0xf149f2ca
	v_mov_b32_e32 v123, 0xf149f2ca
	v_mov_b32_e32 v122, 0xf149f2ca
	v_mov_b32_e32 v121, 0xf149f2ca
	v_mov_b32_e32 v120, 0xf149f2ca
	v_mov_b32_e32 v128, 0xf149f2ca
	v_mov_b32_e32 v127, 0xf149f2ca
	v_mov_b32_e32 v119, 0xf149f2ca
	v_mov_b32_e32 v118, 0xf149f2ca
	v_mov_b32_e32 v117, 0xf149f2ca
	v_mov_b32_e32 v116, 0xf149f2ca
	v_mov_b32_e32 v115, 0xf149f2ca
	v_mov_b32_e32 v114, 0xf149f2ca
	v_mov_b32_e32 v126, 0xf149f2ca
	s_and_saveexec_b64 s[6:7], s[8:9]
	s_cbranch_execz .LBB0_842
	v_sub_u32_e32 v96, s2, v184
	v_max_i32_e32 v97, 8, v183
	v_lshlrev_b32_e32 v98, 2, v182
	v_add_u32_e32 v97, -8, v97
	v_min_u32_e32 v99, 48, v97
	s_movk_i32 s2, 0x7c
	v_sub_u32_e32 v97, v98, v183
	v_mul_lo_u32 v96, v96, s2
	s_add_i32 s2, 0, 0x14800
	v_lshlrev_b32_e32 v97, 2, v97
	v_add3_u32 v114, s2, v96, v97
	ds_read2_b32 v[96:97], v114 offset0:232 offset1:233
	v_sub_u32_e32 v130, v98, v99
	ds_read2_b32 v[98:99], v114 offset0:234 offset1:235
	ds_read2_b32 v[102:103], v114 offset0:240 offset1:241
	ds_read2_b32 v[104:105], v114 offset0:242 offset1:243
	v_add_u32_e32 v107, 1, v130
	v_cmp_gt_u32_e32 vcc, 16, v130
	s_waitcnt lgkmcnt(3)
	v_pk_add_f32 v[80:81], v[80:81], v[96:97]
	v_add_u32_e32 v108, 3, v130
	v_cndmask_b32_e32 v96, v230, v80, vcc
	v_cmp_gt_u32_e32 vcc, 16, v107
	v_add_u32_e32 v107, 2, v130
	v_add_u32_e32 v115, 0x400, v114
	v_cndmask_b32_e32 v97, v230, v81, vcc
	s_waitcnt lgkmcnt(2)
	v_pk_add_f32 v[80:81], v[82:83], v[98:99]
	v_cmp_gt_u32_e32 vcc, 16, v107
	v_add_u32_e32 v82, 8, v130
	v_add_u32_e32 v83, 9, v130
	v_cndmask_b32_e32 v98, v230, v80, vcc
	v_cmp_gt_u32_e32 vcc, 16, v108
	v_add_u32_e32 v106, 0x408, v114
	v_add_u32_e32 v107, 17, v130
	v_cndmask_b32_e32 v99, v230, v81, vcc
	s_waitcnt lgkmcnt(1)
	v_pk_add_f32 v[80:81], v[84:85], v[102:103]
	v_cmp_gt_u32_e32 vcc, 16, v82
	v_add_u32_e32 v82, 10, v130
	v_and_b32_e32 v120, -16, v130
	v_cndmask_b32_e32 v102, v230, v80, vcc
	v_cmp_gt_u32_e32 vcc, 16, v83
	v_add_u32_e32 v83, 11, v130
	s_movk_i32 s2, 0xffd0
	v_cndmask_b32_e32 v103, v230, v81, vcc
	s_waitcnt lgkmcnt(0)
	v_pk_add_f32 v[80:81], v[86:87], v[104:105]
	v_cmp_gt_u32_e32 vcc, 16, v82
	s_nop 1
	v_cndmask_b32_e32 v104, v230, v80, vcc
	v_cmp_gt_u32_e32 vcc, 16, v83
	s_nop 1
	v_cndmask_b32_e32 v105, v230, v81, vcc
	ds_read2_b32 v[80:81], v114 offset0:248 offset1:249
	ds_read2_b32 v[82:83], v114 offset0:250 offset1:251
	ds_read2_b32 v[84:85], v115 offset1:1
	ds_read2_b32 v[86:87], v106 offset1:1
	v_cmp_lt_u32_e32 vcc, s33, v130
	s_waitcnt lgkmcnt(3)
	v_pk_add_f32 v[80:81], v[88:89], v[80:81]
	s_nop 0
	v_cndmask_b32_e32 v106, v230, v80, vcc
	v_cmp_gt_u32_e32 vcc, 16, v107
	v_add_u32_e32 v88, 18, v130
	v_add_u32_e32 v89, 19, v130
	v_cndmask_b32_e32 v107, v230, v81, vcc
	s_waitcnt lgkmcnt(2)
	v_pk_add_f32 v[80:81], v[90:91], v[82:83]
	v_cmp_gt_u32_e32 vcc, 16, v88
	v_add_u32_e32 v82, 24, v130
	v_add_u32_e32 v83, 25, v130
	v_cndmask_b32_e32 v108, v230, v80, vcc
	v_cmp_gt_u32_e32 vcc, 16, v89
	v_add_u32_e32 v88, 0x424, v114
	v_add_u32_e32 v90, 0x444, v114
	v_cndmask_b32_e32 v109, v230, v81, vcc
	s_waitcnt lgkmcnt(1)
	v_pk_add_f32 v[80:81], v[92:93], v[84:85]
	v_cmp_gt_u32_e32 vcc, 16, v82
	v_add_u32_e32 v82, 26, v130
	v_add_u32_e32 v92, 0x464, v114
	v_cndmask_b32_e32 v110, v230, v80, vcc
	v_cmp_gt_u32_e32 vcc, 16, v83
	v_add_u32_e32 v83, 27, v130
	s_nop 0
	v_cndmask_b32_e32 v111, v230, v81, vcc
	s_waitcnt lgkmcnt(0)
	v_pk_add_f32 v[80:81], v[94:95], v[86:87]
	v_cmp_gt_u32_e32 vcc, 16, v82
	v_add_u32_e32 v94, 0x484, v114
	s_nop 0
	v_cndmask_b32_e32 v112, v230, v80, vcc
	v_cmp_gt_u32_e32 vcc, 16, v83
	s_nop 1
	v_cndmask_b32_e32 v113, v230, v81, vcc
	ds_read2_b32 v[80:81], v115 offset0:8 offset1:11
	ds_read2_b32 v[82:83], v115 offset0:16 offset1:19
	ds_read2_b32 v[84:85], v115 offset0:24 offset1:27
	ds_read2_b32 v[88:89], v88 offset1:1
	v_cmp_eq_u32_e32 vcc, s84, v120
	s_waitcnt lgkmcnt(3)
	v_add_f32_e32 v64, v64, v80
	v_add_u32_e32 v80, 33, v130
	v_cndmask_b32_e32 v126, v230, v64, vcc
	v_mov_b32_e32 v64, v65
	v_mov_b32_e32 v65, v66
	ds_read2_b32 v[86:87], v115 offset0:32 offset1:35
	v_add_u32_e32 v115, 34, v130
	s_waitcnt lgkmcnt(1)
	v_pk_add_f32 v[64:65], v[64:65], v[88:89]
	v_cmp_gt_u32_e32 vcc, 16, v80
	v_add_u32_e32 v80, 35, v130
	v_mov_b32_e32 v66, v81
	v_cndmask_b32_e32 v114, v230, v64, vcc
	v_cmp_gt_u32_e32 vcc, 16, v115
	v_mov_b32_e32 v64, v67
	v_mov_b32_e32 v67, v82
	v_cndmask_b32_e32 v115, v230, v65, vcc
	v_mov_b32_e32 v65, v68
	ds_read2_b32 v[90:91], v90 offset1:1
	ds_read2_b32 v[92:93], v92 offset1:1
	ds_read2_b32 v[94:95], v94 offset1:1
	v_add_u32_e32 v88, 40, v130
	v_pk_add_f32 v[64:65], v[64:65], v[66:67]
	v_cmp_gt_u32_e32 vcc, 16, v80
	v_add_u32_e32 v66, 41, v130
	v_add_u32_e32 v67, 42, v130
	v_cndmask_b32_e32 v116, v230, v64, vcc
	v_cmp_gt_u32_e32 vcc, 16, v88
	v_mov_b32_e32 v64, v69
	v_add_u32_e32 v68, 51, v130
	v_cndmask_b32_e32 v117, v230, v65, vcc
	v_mov_b32_e32 v65, v70
	s_waitcnt lgkmcnt(2)
	v_pk_add_f32 v[64:65], v[64:65], v[90:91]
	v_cmp_gt_u32_e32 vcc, 16, v66
	v_add_u32_e32 v66, 49, v130
	v_add_u32_e32 v69, 56, v130
	v_cndmask_b32_e32 v118, v230, v64, vcc
	v_cmp_gt_u32_e32 vcc, 16, v67
	v_add_u32_e32 v64, 43, v130
	v_add_u32_e32 v67, 50, v130
	v_cndmask_b32_e32 v119, v230, v65, vcc
	v_add_f32_e32 v65, v71, v83
	v_cmp_gt_u32_e32 vcc, 16, v64
	v_add_f32_e32 v64, v72, v84
	s_nop 0
	v_cndmask_b32_e32 v127, v230, v65, vcc
	v_cmp_eq_u32_e32 vcc, s2, v120
	v_mov_b32_e32 v65, v74
	s_nop 0
	v_cndmask_b32_e32 v128, v230, v64, vcc
	v_mov_b32_e32 v64, v73
	s_waitcnt lgkmcnt(1)
	v_pk_add_f32 v[64:65], v[64:65], v[92:93]
	v_cmp_gt_u32_e32 vcc, 16, v66
	v_mov_b32_e32 v66, v85
	s_nop 0
	v_cndmask_b32_e32 v120, v230, v64, vcc
	v_cmp_gt_u32_e32 vcc, 16, v67
	v_mov_b32_e32 v64, v75
	v_mov_b32_e32 v67, v86
	v_cndmask_b32_e32 v121, v230, v65, vcc
	v_mov_b32_e32 v65, v76
	v_pk_add_f32 v[64:65], v[64:65], v[66:67]
	v_cmp_gt_u32_e32 vcc, 16, v68
	v_add_u32_e32 v66, 57, v130
	v_add_u32_e32 v67, 58, v130
	v_cndmask_b32_e32 v122, v230, v64, vcc
	v_cmp_gt_u32_e32 vcc, 16, v69
	v_mov_b32_e32 v64, v77
	s_nop 0
	v_cndmask_b32_e32 v123, v230, v65, vcc
	v_mov_b32_e32 v65, v78
	s_waitcnt lgkmcnt(0)
	v_pk_add_f32 v[64:65], v[64:65], v[94:95]
	v_cmp_gt_u32_e32 vcc, 16, v66
	s_nop 1
	v_cndmask_b32_e32 v124, v230, v64, vcc
	v_cmp_gt_u32_e32 vcc, 16, v67
	v_add_u32_e32 v64, 59, v130
	s_nop 0
	v_cndmask_b32_e32 v125, v230, v65, vcc
	v_add_f32_e32 v65, v79, v87
	v_cmp_gt_u32_e32 vcc, 16, v64
	s_nop 1
	v_cndmask_b32_e32 v130, v230, v65, vcc

.LBB0_851:
	v_exp_f32_e32 v101, v80
	v_exp_f32_e32 v103, v81
	v_exp_f32_e32 v111, v88
	v_exp_f32_e32 v89, v89
	v_exp_f32_e32 v105, v82
	v_exp_f32_e32 v113, v90
	v_exp_f32_e32 v83, v83
	v_exp_f32_e32 v91, v91
	v_exp_f32_e32 v107, v84
	v_exp_f32_e32 v115, v92
	v_mov_b32_e32 v100, v64
	v_mov_b32_e32 v102, v65
	v_mov_b32_e32 v110, v72
	v_mov_b32_e32 v88, v73
	v_exp_f32_e32 v85, v85
	v_exp_f32_e32 v93, v93
	v_pk_add_f32 v[80:81], v[100:101], v[102:103]
	v_pk_add_f32 v[118:119], v[110:111], v[88:89]
	v_mov_b32_e32 v104, v66
	v_mov_b32_e32 v112, v74
	v_exp_f32_e32 v109, v86
	v_exp_f32_e32 v117, v94
	v_pk_add_f32 v[80:81], v[104:105], v[80:81]
	v_pk_add_f32 v[118:119], v[112:113], v[118:119]
	v_mov_b32_e32 v82, v67
	v_mov_b32_e32 v90, v75
	v_exp_f32_e32 v87, v87
	v_exp_f32_e32 v95, v95
	v_pk_add_f32 v[80:81], v[82:83], v[80:81]
	v_pk_add_f32 v[118:119], v[90:91], v[118:119]
	v_mov_b32_e32 v106, v68
	v_mov_b32_e32 v114, v76
	v_pk_add_f32 v[80:81], v[106:107], v[80:81]
	v_pk_add_f32 v[118:119], v[114:115], v[118:119]
	v_mov_b32_e32 v84, v69
	v_mov_b32_e32 v92, v77
	v_pk_add_f32 v[80:81], v[84:85], v[80:81]
	v_pk_add_f32 v[118:119], v[92:93], v[118:119]
	v_mov_b32_e32 v108, v70
	v_mov_b32_e32 v116, v78
	v_pk_add_f32 v[80:81], v[108:109], v[80:81]
	v_pk_add_f32 v[118:119], v[116:117], v[118:119]
	v_mov_b32_e32 v86, v71
	v_mov_b32_e32 v94, v79
	v_pk_add_f32 v[80:81], v[86:87], v[80:81]
	v_pk_add_f32 v[118:119], v[94:95], v[118:119]
	s_lshl_b32 s2, s63, 12
	v_pk_add_f32 v[80:81], v[118:119], v[80:81]
	s_add_u32 s16, s35, s2
	v_pk_add_f32 v[80:81], v[80:81], v[80:81] op_sel:[0,1] op_sel_hi:[1,0]
	s_addc_u32 s17, s36, 0
	s_lshl_b32 s2, s33, 7
	v_mov_b32_e32 v99, v80
	s_ashr_i32 s3, s2, 31
	s_nop 0
	v_permlane32_swap_b32_e32 v80, v99
	s_lshl_b64 s[2:3], s[2:3], 1
	v_mul_f32_e32 v96, v210, v200
	v_add_f32_e32 v98, v142, v143
	v_mov_b32_e32 v97, v80
	s_add_u32 s16, s16, s2
	v_pk_add_f32 v[80:81], v[96:97], v[98:99]
	v_cvt_pk_bf16_f32 v64, v64, v65
	v_cvt_pk_bf16_f32 v65, v66, v67
	v_cvt_pk_bf16_f32 v66, v68, v69
	v_cvt_pk_bf16_f32 v67, v70, v71
	v_cvt_pk_bf16_f32 v68, v72, v73
	v_cvt_pk_bf16_f32 v69, v74, v75
	v_cvt_pk_bf16_f32 v70, v76, v77
	v_cvt_pk_bf16_f32 v71, v78, v79
	v_cvt_pk_bf16_f32 v72, v101, v103
	v_cvt_pk_bf16_f32 v73, v105, v83
	v_cvt_pk_bf16_f32 v74, v107, v85
	v_cvt_pk_bf16_f32 v75, v109, v87
	v_cvt_pk_bf16_f32 v76, v111, v89
	v_cvt_pk_bf16_f32 v77, v113, v91
	v_cvt_pk_bf16_f32 v78, v115, v93
	v_cvt_pk_bf16_f32 v79, v117, v95
	s_addc_u32 s17, s17, s3
	v_fmac_f32_e32 v81, v80, v128
	ds_read_b64_tr_b16 v[82:83], v203 offset:0
	ds_read_b64_tr_b16 v[84:85], v203 offset:0x800
	ds_read_b64_tr_b16 v[86:87], v203 offset:0x1000
	ds_read_b64_tr_b16 v[88:89], v203 offset:0x1800
	ds_read_b64_tr_b16 v[90:91], v203 offset:0x2000
	ds_read_b64_tr_b16 v[92:93], v203 offset:0x2800
	ds_read_b64_tr_b16 v[94:95], v203 offset:0x3000
	ds_read_b64_tr_b16 v[96:97], v203 offset:0x3800
	s_waitcnt lgkmcnt(0)
	s_nop 0
	v_mfma_f32_32x32x16_bf16 v[0:15], v[82:85], v[64:67], v[0:15]
	ds_read_b64_tr_b16 v[82:83], v203 offset:0x200
	ds_read_b64_tr_b16 v[84:85], v203 offset:0xa00
	v_mfma_f32_32x32x16_bf16 v[0:15], v[86:89], v[68:71], v[0:15]
	ds_read_b64_tr_b16 v[86:87], v203 offset:0x1200
	ds_read_b64_tr_b16 v[88:89], v203 offset:0x1a00
	v_mfma_f32_32x32x16_bf16 v[0:15], v[90:93], v[72:75], v[0:15]
	ds_read_b64_tr_b16 v[90:91], v203 offset:0x2200
	ds_read_b64_tr_b16 v[92:93], v203 offset:0x2a00
	v_mfma_f32_32x32x16_bf16 v[0:15], v[94:97], v[76:79], v[0:15]
	ds_read_b64_tr_b16 v[94:95], v203 offset:0x3200
	ds_read_b64_tr_b16 v[96:97], v203 offset:0x3a00
	s_waitcnt lgkmcnt(0)
	v_mfma_f32_32x32x16_bf16 v[48:63], v[82:85], v[64:67], v[48:63]
	ds_read_b64_tr_b16 v[82:83], v203 offset:0x400
	ds_read_b64_tr_b16 v[84:85], v203 offset:0xc00
	v_mfma_f32_32x32x16_bf16 v[48:63], v[86:89], v[68:71], v[48:63]
	ds_read_b64_tr_b16 v[86:87], v203 offset:0x1400
	ds_read_b64_tr_b16 v[88:89], v203 offset:0x1c00
	v_mfma_f32_32x32x16_bf16 v[48:63], v[90:93], v[72:75], v[48:63]
	ds_read_b64_tr_b16 v[90:91], v203 offset:0x2400
	ds_read_b64_tr_b16 v[92:93], v203 offset:0x2c00
	v_mfma_f32_32x32x16_bf16 v[48:63], v[94:97], v[76:79], v[48:63]
	ds_read_b64_tr_b16 v[94:95], v203 offset:0x3400
	ds_read_b64_tr_b16 v[96:97], v203 offset:0x3c00
	s_waitcnt lgkmcnt(0)
	v_mfma_f32_32x32x16_bf16 v[32:47], v[82:85], v[64:67], v[32:47]
	ds_read_b64_tr_b16 v[82:83], v203 offset:0x600
	ds_read_b64_tr_b16 v[84:85], v203 offset:0xe00
	v_mfma_f32_32x32x16_bf16 v[32:47], v[86:89], v[68:71], v[32:47]
	ds_read_b64_tr_b16 v[86:87], v203 offset:0x1600
	ds_read_b64_tr_b16 v[88:89], v203 offset:0x1e00
	v_mfma_f32_32x32x16_bf16 v[32:47], v[90:93], v[72:75], v[32:47]
	ds_read_b64_tr_b16 v[90:91], v203 offset:0x2600
	ds_read_b64_tr_b16 v[92:93], v203 offset:0x2e00
	v_mfma_f32_32x32x16_bf16 v[32:47], v[94:97], v[76:79], v[32:47]
	ds_read_b64_tr_b16 v[94:95], v203 offset:0x3600
	ds_read_b64_tr_b16 v[96:97], v203 offset:0x3e00
	s_waitcnt lgkmcnt(0)
	v_mfma_f32_32x32x16_bf16 v[16:31], v[82:85], v[64:67], v[16:31]
	v_rcp_f32_e32 v67, v81
	v_mbcnt_lo_u32_b32 v66, -1, 0
	v_mbcnt_hi_u32_b32 v66, -1, v66
	s_add_i32 s91, s91, 1
	v_add_u32_e32 v64, s80, v66
	v_ashrrev_i32_e32 v64, 1, v64
	v_mul_f32_e32 v0, v67, v0
	v_mul_f32_e32 v1, v67, v1
	v_bfi_b32 v64, s84, v64, v66
	v_cvt_pk_bf16_f32 v0, v0, v1
	v_mul_f32_e32 v1, v67, v2
	v_mul_f32_e32 v2, v67, v3
	v_ashrrev_i32_e32 v65, 31, v64
	v_cvt_pk_bf16_f32 v1, v1, v2
	v_mul_f32_e32 v2, v67, v4
	v_mul_f32_e32 v3, v67, v5
	v_lshlrev_b64 v[64:65], 12, v[64:65]
	v_lshrrev_b32_e32 v66, 1, v66
	v_cvt_pk_bf16_f32 v2, v2, v3
	v_mul_f32_e32 v3, v67, v6
	v_lshl_add_u64 v[64:65], s[16:17], 0, v[64:65]
	v_and_b32_e32 v128, 16, v66
	v_mul_f32_e32 v4, v67, v7
	v_cvt_pk_bf16_f32 v3, v3, v4
	v_lshl_add_u64 v[64:65], v[64:65], 0, v[128:129]
	v_permlane32_swap_b32_e32 v0, v2
	v_permlane32_swap_b32_e32 v1, v3
	global_store_dwordx4 v[64:65], v[0:3], off
	v_mul_f32_e32 v4, v67, v15
	v_mfma_f32_32x32x16_bf16 v[16:31], v[86:89], v[68:71], v[16:31]
	v_mul_f32_e32 v0, v67, v8
	v_mul_f32_e32 v1, v67, v9
	v_cvt_pk_bf16_f32 v0, v0, v1
	v_mul_f32_e32 v1, v67, v10
	v_mul_f32_e32 v2, v67, v11
	v_cvt_pk_bf16_f32 v1, v1, v2
	v_mul_f32_e32 v2, v67, v12
	v_mul_f32_e32 v3, v67, v13
	v_cvt_pk_bf16_f32 v2, v2, v3
	v_mul_f32_e32 v3, v67, v14
	v_cvt_pk_bf16_f32 v3, v3, v4
	v_permlane32_swap_b32_e32 v0, v2
	s_nop 0
	v_permlane32_swap_b32_e32 v1, v3
	global_store_dwordx4 v[64:65], v[0:3], off offset:32
	v_mul_f32_e32 v4, v67, v55
	v_mfma_f32_32x32x16_bf16 v[16:31], v[90:93], v[72:75], v[16:31]
	v_mul_f32_e32 v0, v67, v48
	v_mul_f32_e32 v1, v67, v49
	v_cvt_pk_bf16_f32 v0, v0, v1
	v_mul_f32_e32 v1, v67, v50
	v_mul_f32_e32 v2, v67, v51
	v_cvt_pk_bf16_f32 v1, v1, v2
	v_mul_f32_e32 v2, v67, v52
	v_mul_f32_e32 v3, v67, v53
	v_cvt_pk_bf16_f32 v2, v2, v3
	v_mul_f32_e32 v3, v67, v54
	v_cvt_pk_bf16_f32 v3, v3, v4
	v_permlane32_swap_b32_e32 v0, v2
	s_nop 0
	v_permlane32_swap_b32_e32 v1, v3
	global_store_dwordx4 v[64:65], v[0:3], off offset:64
	v_mul_f32_e32 v4, v67, v63
	v_mfma_f32_32x32x16_bf16 v[16:31], v[94:97], v[76:79], v[16:31]
	v_mul_f32_e32 v0, v67, v56
	v_mul_f32_e32 v1, v67, v57
	v_cvt_pk_bf16_f32 v0, v0, v1
	v_mul_f32_e32 v1, v67, v58
	v_mul_f32_e32 v2, v67, v59
	v_cvt_pk_bf16_f32 v1, v1, v2
	v_mul_f32_e32 v2, v67, v60
	v_mul_f32_e32 v3, v67, v61
	v_cvt_pk_bf16_f32 v2, v2, v3
	v_mul_f32_e32 v3, v67, v62
	v_cvt_pk_bf16_f32 v3, v3, v4
	v_permlane32_swap_b32_e32 v0, v2
	s_nop 0
	v_permlane32_swap_b32_e32 v1, v3
	global_store_dwordx4 v[64:65], v[0:3], off offset:96
	v_mul_f32_e32 v4, v67, v39
	s_lshl_b32 s2, s91, 8
	v_mul_f32_e32 v0, v67, v32
	v_mul_f32_e32 v1, v67, v33
	v_cvt_pk_bf16_f32 v0, v0, v1
	v_mul_f32_e32 v1, v67, v34
	v_mul_f32_e32 v2, v67, v35
	v_cvt_pk_bf16_f32 v1, v1, v2
	v_mul_f32_e32 v2, v67, v36
	v_mul_f32_e32 v3, v67, v37
	v_cvt_pk_bf16_f32 v2, v2, v3
	v_mul_f32_e32 v3, v67, v38
	v_cvt_pk_bf16_f32 v3, v3, v4
	v_permlane32_swap_b32_e32 v0, v2
	s_nop 0
	v_permlane32_swap_b32_e32 v1, v3
	global_store_dwordx4 v[64:65], v[0:3], off offset:128
	v_mul_f32_e32 v4, v67, v47
	s_add_i32 s3, s2, s94
	v_mul_f32_e32 v0, v67, v40
	v_mul_f32_e32 v1, v67, v41
	v_cvt_pk_bf16_f32 v0, v0, v1
	v_mul_f32_e32 v1, v67, v42
	v_mul_f32_e32 v2, v67, v43
	v_cvt_pk_bf16_f32 v1, v1, v2
	v_mul_f32_e32 v2, v67, v44
	v_mul_f32_e32 v3, v67, v45
	v_cvt_pk_bf16_f32 v2, v2, v3
	v_mul_f32_e32 v3, v67, v46
	v_cvt_pk_bf16_f32 v3, v3, v4
	v_permlane32_swap_b32_e32 v0, v2
	s_nop 0
	v_permlane32_swap_b32_e32 v1, v3
	global_store_dwordx4 v[64:65], v[0:3], off offset:160
	v_mul_f32_e32 v4, v67, v23
	s_cmp_lt_i32 s3, s37
	v_mul_f32_e32 v0, v67, v16
	v_mul_f32_e32 v1, v67, v17
	v_cvt_pk_bf16_f32 v0, v0, v1
	v_mul_f32_e32 v1, v67, v18
	v_mul_f32_e32 v2, v67, v19
	v_cvt_pk_bf16_f32 v1, v1, v2
	v_mul_f32_e32 v2, v67, v20
	v_mul_f32_e32 v3, v67, v21
	v_cvt_pk_bf16_f32 v2, v2, v3
	v_mul_f32_e32 v3, v67, v22
	v_cvt_pk_bf16_f32 v3, v3, v4
	v_permlane32_swap_b32_e32 v0, v2
	s_nop 0
	v_permlane32_swap_b32_e32 v1, v3
	global_store_dwordx4 v[64:65], v[0:3], off offset:192
	v_mul_f32_e32 v4, v67, v31
	s_nop 0
	v_mul_f32_e32 v0, v67, v24
	v_mul_f32_e32 v1, v67, v25
	v_cvt_pk_bf16_f32 v0, v0, v1
	v_mul_f32_e32 v1, v67, v26
	v_mul_f32_e32 v2, v67, v27
	v_cvt_pk_bf16_f32 v1, v1, v2
	v_mul_f32_e32 v2, v67, v28
	v_mul_f32_e32 v3, v67, v29
	v_cvt_pk_bf16_f32 v2, v2, v3
	v_mul_f32_e32 v3, v67, v30
	v_cvt_pk_bf16_f32 v3, v3, v4
	v_permlane32_swap_b32_e32 v0, v2
	s_nop 0
	v_permlane32_swap_b32_e32 v1, v3
	global_store_dwordx4 v[64:65], v[0:3], off offset:224
	s_cbranch_scc0 .LBB0_904

.LBB0_860:
	s_waitcnt vmcnt(4)
	v_add_u32_e32 v41, 32, v72
	v_and_b32_e32 v36, 63, v71
	v_and_b32_e32 v37, 0xfffff0, v72
	v_lshlrev_b32_e32 v38, 1, v72
	v_and_b32_e32 v42, 0xfffff0, v41
	v_lshlrev_b32_e32 v43, 1, v41
	v_and_or_b32 v37, v38, 8, v37
	v_and_or_b32 v42, v43, 8, v42
	v_lshlrev_b32_e32 v44, 4, v36
	s_and_b64 s[2:3], s[22:23], exec
	v_lshrrev_b32_e32 v38, 1, v72
	v_lshrrev_b32_e32 v37, 1, v37
	v_lshrrev_b32_e32 v39, 5, v74
	v_and_b32_e32 v40, 3, v72
	v_lshrrev_b32_e32 v42, 1, v42
	v_lshlrev_b32_e32 v43, 3, v36
	v_and_b32_e32 v45, 0xc0, v44
	v_lshlrev_b32_e32 v36, 1, v36
	s_cselect_b32 s22, 4, 36
	v_or_b32_e32 v37, v37, v39
	v_and_or_b32 v38, v38, 4, v40
	v_lshlrev_b32_e32 v40, 1, v74
	v_or_b32_e32 v39, v42, v39
	v_and_or_b32 v45, v43, 24, v45
	v_and_b32_e32 v36, 32, v36
	v_and_b32_e32 v43, 0x100, v43
	s_cmp_lg_u32 0, -1
	v_lshlrev_b32_e32 v37, 9, v37
	v_lshlrev_b32_e32 v38, 6, v38
	v_lshlrev_b32_e32 v39, 9, v39
	v_or3_b32 v48, v45, v36, v43
	v_and_b32_e32 v36, 48, v40
	s_cselect_b32 s24, 0, 0
	s_add_i32 s2, 0, 0x15000
	v_or3_b32 v37, v37, v38, v36
	v_or3_b32 v36, v39, v38, v36
	v_lshl_add_u32 v38, v73, 12, s2
	v_add_u32_e32 v204, v38, v44
	s_waitcnt vmcnt(3)
	ds_write_b128 v204, v[24:27]
	s_waitcnt vmcnt(2)
	ds_write_b128 v204, v[20:23] offset:1024
	s_waitcnt vmcnt(1)
	ds_write_b128 v204, v[32:35] offset:2048
	s_waitcnt vmcnt(0)
	ds_write_b128 v204, v[28:31] offset:3072
	v_add_u32_e32 v205, 0, v37
	v_lshrrev_b32_e32 v37, 3, v205
	v_xor_b32_e32 v37, v37, v205
	v_and_b32_e32 v37, 0x100, v37
	v_xor_b32_e32 v205, v205, v37
	v_lshlrev_b32_e32 v37, 3, v37
	v_xor_b32_e32 v205, v205, v37
	s_waitcnt vmcnt(0)
	ds_write_b128 v205, v[12:15]
	v_lshlrev_b32_e32 v12, 8, v72
	v_and_b32_e32 v13, 0x70, v71
	v_bitop3_b32 v12, v40, v12, v13 bitop3:0xde
	v_add_u32_e32 v206, 0, v36
	v_lshrrev_b32_e32 v36, 3, v206
	v_xor_b32_e32 v36, v36, v206
	v_and_b32_e32 v36, 0x100, v36
	v_xor_b32_e32 v206, v206, v36
	v_lshlrev_b32_e32 v36, 3, v36
	v_xor_b32_e32 v206, v206, v36
	v_add_u32_e32 v207, 0, v12
	ds_write_b128 v206, v[16:19]
	ds_write_b128 v207, v[8:11] offset:32768
	v_lshlrev_b32_e32 v8, 8, v41
	v_bitop3_b32 v8, v40, v8, v13 bitop3:0xde
	v_add_u32_e32 v208, 0, v8
	v_and_b32_e32 v42, 0xffffff80, v96
	ds_write_b128 v208, v[4:7] offset:32768
	v_xor_b32_e32 v4, v96, v71
	s_movk_i32 s2, 0x70
	v_and_or_b32 v49, v4, s2, v42
	s_add_i32 s2, 0, 0x10000
	v_add_u32_e32 v4, s2, v49
	ds_write_b128 v4, v[0:3]
	v_lshlrev_b32_e32 v0, 4, v70
	v_lshlrev_b32_e32 v58, 8, v70
	v_and_b32_e32 v59, 0x70, v0
	v_bitop3_b32 v0, v68, v58, v59 bitop3:0xde
	v_add_u32_e32 v209, 0, v0
	s_waitcnt lgkmcnt(0)
	s_barrier
	ds_read_b128 v[16:19], v209 offset:32768
	ds_read_b128 v[20:23], v209 offset:40960
	s_waitcnt lgkmcnt(1)
	v_mfma_f32_32x32x16_bf16 v[32:47], v[16:19], v[158:161], 0
	v_or_b32_e32 v62, 32, v68
	v_bitop3_b32 v50, v62, v58, v59 bitop3:0xde
	v_add_u32_e32 v211, 0, v50
	ds_read_b128 v[50:53], v211 offset:32768
	ds_read_b128 v[54:57], v211 offset:40960
	v_or_b32_e32 v63, 64, v68
	v_or_b32_e32 v64, 0x60, v68
	v_lshlrev_b32_e32 v65, 7, v70
	s_waitcnt lgkmcnt(2)
	v_mfma_f32_32x32x16_bf16 v[16:31], v[20:23], v[158:161], 0
	s_mov_b32 s72, s73
	s_mov_b32 s74, s73
	s_mov_b32 s75, s73
	s_mov_b32 s76, s73
	s_mov_b32 s77, s73
	s_mov_b32 s78, s73
	s_mov_b32 s79, s73
	s_waitcnt lgkmcnt(1)
	v_mfma_f32_32x32x16_bf16 v[32:47], v[50:53], v[154:157], v[32:47]
	v_bitop3_b32 v50, v63, v58, v59 bitop3:0xde
	v_add_u32_e32 v212, 0, v50
	s_mov_b32 s80, s73
	s_mov_b32 s81, s73
	s_mov_b32 s82, s73
	s_mov_b32 s83, s73
	s_mov_b32 s84, s73
	s_waitcnt lgkmcnt(0)
	v_mfma_f32_32x32x16_bf16 v[16:31], v[54:57], v[154:157], v[16:31]
	ds_read_b128 v[50:53], v212 offset:32768
	ds_read_b128 v[54:57], v212 offset:40960
	s_mov_b32 s85, s73
	s_mov_b32 s86, s73
	s_mov_b32 s87, s73
	v_mov_b64_e32 v[0:1], s[72:73]
	v_mov_b32_e32 v183, v129
	v_mov_b32_e32 v97, v129
	s_waitcnt lgkmcnt(1)
	v_mfma_f32_32x32x16_bf16 v[32:47], v[50:53], v[150:153], v[32:47]
	v_bitop3_b32 v50, v64, v58, v59 bitop3:0xde
	v_add_u32_e32 v213, 0, v50
	v_mov_b64_e32 v[2:3], s[74:75]
	v_mov_b64_e32 v[4:5], s[76:77]
	v_mov_b64_e32 v[6:7], s[78:79]
	v_mov_b64_e32 v[8:9], s[80:81]
	v_mov_b64_e32 v[10:11], s[82:83]
	s_waitcnt lgkmcnt(0)
	v_mfma_f32_32x32x16_bf16 v[16:31], v[54:57], v[150:153], v[16:31]
	ds_read_b128 v[50:53], v213 offset:32768
	ds_read_b128 v[54:57], v213 offset:40960
	v_mov_b64_e32 v[12:13], s[84:85]
	v_mov_b64_e32 v[14:15], s[86:87]
	v_add_u32_e32 v228, 0, v49
	v_add_u32_e32 v201, s24, v48
	v_add_u32_e32 v229, 0x12000, v228
	s_waitcnt lgkmcnt(1)
	v_mfma_f32_32x32x16_bf16 v[32:47], v[50:53], v[146:149], v[32:47]
	v_or_b32_e32 v50, 0x80, v68
	v_bitop3_b32 v50, v50, v58, v59 bitop3:0xde
	v_add_u32_e32 v215, 0, v50
	v_lshl_add_u64 v[184:185], s[58:59], 0, v[96:97]
	v_lshl_add_u64 v[186:187], s[8:9], 0, v[96:97]
	v_mov_b32_e32 v210, 0
	v_readlane_b32 s80, v255, 48
	s_waitcnt lgkmcnt(0)
	v_mfma_f32_32x32x16_bf16 v[16:31], v[54:57], v[146:149], v[16:31]
	ds_read_b128 v[50:53], v215 offset:32768
	ds_read_b128 v[54:57], v215 offset:40960
	s_movk_i32 s84, 0xffe0
	s_waitcnt lgkmcnt(1)
	v_mfma_f32_32x32x16_bf16 v[32:47], v[50:53], v[142:145], v[32:47]
	v_or_b32_e32 v50, 0xa0, v68
	v_bitop3_b32 v50, v50, v58, v59 bitop3:0xde
	v_add_u32_e32 v217, 0, v50
	s_waitcnt lgkmcnt(0)
	v_mfma_f32_32x32x16_bf16 v[16:31], v[54:57], v[142:145], v[16:31]
	ds_read_b128 v[50:53], v217 offset:32768
	ds_read_b128 v[54:57], v217 offset:40960
	s_waitcnt lgkmcnt(1)
	v_mfma_f32_32x32x16_bf16 v[32:47], v[50:53], v[138:141], v[32:47]
	v_or_b32_e32 v50, 0xc0, v68
	v_bitop3_b32 v50, v50, v58, v59 bitop3:0xde
	v_add_u32_e32 v214, 0, v50
	s_waitcnt lgkmcnt(0)
	v_mfma_f32_32x32x16_bf16 v[16:31], v[54:57], v[138:141], v[16:31]
	ds_read_b128 v[50:53], v214 offset:32768
	ds_read_b128 v[54:57], v214 offset:40960
	s_waitcnt lgkmcnt(1)
	v_mfma_f32_32x32x16_bf16 v[32:47], v[50:53], v[134:137], v[32:47]
	v_or_b32_e32 v50, 0xe0, v68
	v_bitop3_b32 v50, v50, v58, v59 bitop3:0xde
	v_add_u32_e32 v216, 0, v50
	s_waitcnt lgkmcnt(0)
	v_mfma_f32_32x32x16_bf16 v[16:31], v[54:57], v[134:137], v[16:31]
	ds_read_b128 v[50:53], v216 offset:32768
	ds_read_b128 v[54:57], v216 offset:40960
	s_waitcnt lgkmcnt(1)
	v_mfma_f32_32x32x16_bf16 v[32:47], v[50:53], v[130:133], v[32:47]
	v_lshlrev_b32_e32 v50, 3, v70
	v_and_b32_e32 v66, 0x70, v50
	v_bitop3_b32 v218, v68, v65, v66 bitop3:0xde
	v_add_u32_e32 v219, s2, v218
	v_bitop3_b32 v220, v62, v65, v66 bitop3:0xde
	v_add_u32_e32 v221, s2, v220
	v_bitop3_b32 v222, v63, v65, v66 bitop3:0xde
	s_waitcnt lgkmcnt(0)
	v_mfma_f32_32x32x16_bf16 v[16:31], v[54:57], v[130:133], v[16:31]
	ds_read_b128 v[50:53], v219
	ds_read_b128 v[54:57], v219 offset:4096
	ds_read_b128 v[58:61], v204
	v_add_u32_e32 v223, s2, v222
	v_bitop3_b32 v224, v64, v65, v66 bitop3:0xde
	v_add_u32_e32 v225, s2, v224
	s_waitcnt lgkmcnt(0)
	v_mfma_f32_32x32x16_bf16 v[32:47], v[50:53], v[58:61], v[32:47]
	v_mfma_f32_32x32x16_bf16 v[16:31], v[54:57], v[58:61], v[16:31]
	ds_read_b128 v[50:53], v221
	ds_read_b128 v[54:57], v221 offset:4096
	ds_read_b128 v[58:61], v204 offset:1024
	s_waitcnt lgkmcnt(0)
	v_mfma_f32_32x32x16_bf16 v[32:47], v[50:53], v[58:61], v[32:47]
	v_mfma_f32_32x32x16_bf16 v[16:31], v[54:57], v[58:61], v[16:31]
	ds_read_b128 v[50:53], v223
	ds_read_b128 v[54:57], v223 offset:4096
	ds_read_b128 v[58:61], v204 offset:2048
	s_waitcnt lgkmcnt(0)
	v_mfma_f32_32x32x16_bf16 v[32:47], v[50:53], v[58:61], v[32:47]
	v_mfma_f32_32x32x16_bf16 v[16:31], v[54:57], v[58:61], v[16:31]
	ds_read_b128 v[50:53], v225
	ds_read_b128 v[54:57], v225 offset:4096
	ds_read_b128 v[58:61], v204 offset:3072
	s_waitcnt lgkmcnt(0)
	v_mfma_f32_32x32x16_bf16 v[32:47], v[50:53], v[58:61], v[32:47]
	v_mfma_f32_32x32x16_bf16 v[16:31], v[54:57], v[58:61], v[16:31]
	s_nop 10
	v_max_f32_e32 v50, v33, v33
	v_max_f32_e32 v51, v32, v32
	v_max_f32_e32 v50, v51, v50
	v_max_f32_e32 v51, v41, v41
	v_max_f32_e32 v52, v40, v40
	v_max_f32_e32 v51, v52, v51
	v_max3_f32 v50, v50, v34, v35
	v_max_f32_e32 v52, v25, v25
	v_max_f32_e32 v53, v24, v24
	v_max_f32_e32 v52, v53, v52
	v_max3_f32 v53, v16, v17, v18
	v_max3_f32 v52, v52, v26, v27
	v_max3_f32 v51, v51, v42, v43
	v_max3_f32 v53, v53, v19, v20
	v_max3_f32 v52, v52, v28, v29
	v_max3_f32 v50, v50, v36, v37
	v_max3_f32 v51, v51, v44, v45
	v_max3_f32 v53, v53, v21, v22
	v_max3_f32 v52, v52, v30, v31
	v_max3_f32 v50, v50, v38, v39
	v_max3_f32 v51, v51, v46, v47
	v_max3_f32 v52, v53, v23, v52
	v_max3_f32 v50, v50, v51, v52
	v_mov_b32_e32 v51, v50
	s_nop 1
	v_permlane32_swap_b32_e32 v50, v51
	v_max_f32_e32 v51, v51, v51
	v_max_f32_e32 v50, v50, v50
	v_max_f32_e32 v50, v50, v51
	v_add_f32_e32 v51, 0x7149f2ca, v50
	v_max_f32_e32 v50, 0xf149f2ca, v50
	v_cmp_ge_f32_e32 vcc, s34, v51
	v_sub_f32_e32 v51, 0xf149f2ca, v50
	v_mul_f32_e32 v51, 0x3dd53b94, v51
	s_cmp_eq_u64 vcc, exec
	v_exp_f32_e32 v51, v51
	s_cselect_b64 vcc, -1, 0
	v_cndmask_b32_e32 v227, v50, v230, vcc
	v_mul_f32_e32 v50, 0xbdd53b94, v227
	v_cndmask_b32_e64 v226, v51, 1.0, vcc
	v_mov_b32_e32 v51, v50
	s_add_u32 s2, s18, s92
	v_fmac_f32_e32 v51, 0x3dd53b94, v47
	s_addc_u32 s3, s19, s93
	v_fmamk_f32 v32, v32, 0x3dd53b94, v50
	v_fmamk_f32 v33, v33, 0x3dd53b94, v50
	v_pk_fma_f32 v[80:81], v[16:17], s[54:55], v[50:51] op_sel_hi:[1,0,0]
	s_add_u32 s74, s16, s92
	v_lshl_add_u64 v[16:17], s[2:3], 0, v[128:129]
	v_fmamk_f32 v34, v34, 0x3dd53b94, v50
	v_fmamk_f32 v35, v35, 0x3dd53b94, v50
	v_pk_fma_f32 v[84:85], v[20:21], s[54:55], v[50:51] op_sel_hi:[1,0,0]
	v_pk_fma_f32 v[82:83], v[18:19], s[54:55], v[50:51] op_sel_hi:[1,0,0]
	v_exp_f32_e32 v64, v32
	v_exp_f32_e32 v65, v33
	s_addc_u32 s75, s17, s93
	global_load_dwordx4 v[16:19], v[16:17], off
	v_lshl_add_u64 v[20:21], s[2:3], 0, v[182:183]
	v_lshl_add_u64 v[32:33], s[96:97], 0, v[96:97]
	v_pk_fma_f32 v[88:89], v[24:25], s[54:55], v[50:51] op_sel_hi:[1,0,0]
	v_pk_fma_f32 v[86:87], v[22:23], s[54:55], v[50:51] op_sel_hi:[1,0,0]
	v_exp_f32_e32 v66, v34
	v_exp_f32_e32 v67, v35
	global_load_dwordx4 v[20:23], v[20:21], off
	v_lshl_add_u64 v[24:25], s[74:75], 0, v[128:129]
	global_load_dwordx4 v[32:35], v[32:33], off
	v_pk_fma_f32 v[92:93], v[28:29], s[54:55], v[50:51] op_sel_hi:[1,0,0]
	v_pk_fma_f32 v[90:91], v[26:27], s[54:55], v[50:51] op_sel_hi:[1,0,0]
	global_load_dwordx4 v[24:27], v[24:25], off
	v_lshl_add_u64 v[28:29], s[74:75], 0, v[182:183]
	v_pk_fma_f32 v[94:95], v[30:31], s[54:55], v[50:51] op_sel_hi:[1,0,0]
	global_load_dwordx4 v[28:31], v[28:29], off
	v_fmamk_f32 v36, v36, 0x3dd53b94, v50
	v_fmamk_f32 v37, v37, 0x3dd53b94, v50
	v_fmamk_f32 v38, v38, 0x3dd53b94, v50
	v_fmamk_f32 v39, v39, 0x3dd53b94, v50
	v_fmamk_f32 v40, v40, 0x3dd53b94, v50
	v_fmamk_f32 v41, v41, 0x3dd53b94, v50
	v_fmamk_f32 v42, v42, 0x3dd53b94, v50
	v_fmamk_f32 v43, v43, 0x3dd53b94, v50
	v_fmamk_f32 v44, v44, 0x3dd53b94, v50
	v_fmamk_f32 v45, v45, 0x3dd53b94, v50
	v_fmamk_f32 v46, v46, 0x3dd53b94, v50
	v_exp_f32_e32 v68, v36
	v_exp_f32_e32 v69, v37
	v_exp_f32_e32 v70, v38
	v_exp_f32_e32 v71, v39
	v_exp_f32_e32 v72, v40
	v_exp_f32_e32 v73, v41
	v_exp_f32_e32 v74, v42
	v_exp_f32_e32 v75, v43
	v_exp_f32_e32 v76, v44
	v_exp_f32_e32 v77, v45
	v_exp_f32_e32 v78, v46
	v_exp_f32_e32 v79, v51
	s_waitcnt vmcnt(0)
	s_waitcnt vmcnt(4)
	ds_write_b128 v205, v[16:19] offset:16384
	s_waitcnt vmcnt(3)
	ds_write_b128 v206, v[20:23] offset:16384
	s_waitcnt vmcnt(1)
	ds_write_b128 v207, v[24:27] offset:49152
	s_waitcnt vmcnt(0)
	ds_write_b128 v208, v[28:31] offset:49152
	s_addk_i32 s24, 0x4000
	v_lshl_add_u64 v[16:17], s[20:21], 0, v[128:129]
	v_lshl_add_u64 v[18:19], s[20:21], 0, v[182:183]
	ds_write_b128 v229, v[32:35]
	v_add_u32_e32 v203, s24, v48
	v_lshl_add_u64 v[188:189], s[12:13], 0, v[16:17]
	v_lshl_add_u64 v[190:191], s[12:13], 0, v[18:19]
	v_lshl_add_u64 v[192:193], s[14:15], 0, v[16:17]
	v_lshl_add_u64 v[198:199], s[14:15], 0, v[18:19]
	v_mov_b64_e32 v[62:63], v[14:15]
	v_mov_b64_e32 v[46:47], v[14:15]
	v_mov_b64_e32 v[30:31], v[14:15]
	s_add_i32 s23, s22, -1
	s_mov_b32 s20, 2
	v_mov_b64_e32 v[60:61], v[12:13]
	v_mov_b64_e32 v[58:59], v[10:11]
	v_mov_b64_e32 v[56:57], v[8:9]
	v_mov_b64_e32 v[54:55], v[6:7]
	v_mov_b64_e32 v[52:53], v[4:5]
	v_mov_b64_e32 v[50:51], v[2:3]
	v_mov_b64_e32 v[48:49], v[0:1]
	v_mov_b64_e32 v[44:45], v[12:13]
	v_mov_b64_e32 v[42:43], v[10:11]
	v_mov_b64_e32 v[40:41], v[8:9]
	v_mov_b64_e32 v[38:39], v[6:7]
	v_mov_b64_e32 v[36:37], v[4:5]
	v_mov_b64_e32 v[34:35], v[2:3]
	v_mov_b64_e32 v[32:33], v[0:1]
	v_mov_b64_e32 v[28:29], v[12:13]
	v_mov_b64_e32 v[26:27], v[10:11]
	v_mov_b64_e32 v[24:25], v[8:9]
	v_mov_b64_e32 v[22:23], v[6:7]
	v_mov_b64_e32 v[20:21], v[4:5]
	v_mov_b64_e32 v[18:19], v[2:3]
	v_mov_b64_e32 v[16:17], v[0:1]
	v_readlane_b32 s21, v252, 17
	s_waitcnt lgkmcnt(0)
	s_barrier
.LBB0_861:
	ds_read_b128 v[96:99], v209 offset:49152
	ds_read_b128 v[100:103], v209 offset:57344
	ds_read_b128 v[162:165], v211 offset:49152
	ds_read_b128 v[166:169], v211 offset:57344
	s_add_i32 s2, 0, 0x12000
	v_add_u32_e32 v233, s2, v218
	s_waitcnt lgkmcnt(3)
	v_mfma_f32_32x32x16_bf16 v[112:127], v[96:99], v[158:161], 0
	v_add_u32_e32 v234, s2, v220
	v_add_u32_e32 v236, s2, v222
	v_add_u32_e32 v235, s2, v224
	v_exp_f32_e32 v80, v80
	v_exp_f32_e32 v81, v81
	v_exp_f32_e32 v82, v82
	v_exp_f32_e32 v83, v83
	s_waitcnt lgkmcnt(2)
	v_mfma_f32_32x32x16_bf16 v[96:111], v[100:103], v[158:161], 0
	v_exp_f32_e32 v84, v84
	v_exp_f32_e32 v92, v92
	v_exp_f32_e32 v85, v85
	v_exp_f32_e32 v93, v93
	v_exp_f32_e32 v86, v86
	v_exp_f32_e32 v94, v94
	v_exp_f32_e32 v87, v87
	s_waitcnt lgkmcnt(1)
	v_mfma_f32_32x32x16_bf16 v[112:127], v[162:165], v[154:157], v[112:127]
	v_exp_f32_e32 v95, v95
	s_waitcnt lgkmcnt(0)
	v_mfma_f32_32x32x16_bf16 v[96:111], v[166:169], v[154:157], v[96:111]
	ds_read_b128 v[162:165], v212 offset:49152
	ds_read_b128 v[166:169], v212 offset:57344
	s_waitcnt lgkmcnt(1)
	v_mfma_f32_32x32x16_bf16 v[112:127], v[162:165], v[150:153], v[112:127]
	s_waitcnt lgkmcnt(0)
	v_mfma_f32_32x32x16_bf16 v[96:111], v[166:169], v[150:153], v[96:111]
	ds_read_b128 v[162:165], v213 offset:49152
	ds_read_b128 v[166:169], v213 offset:57344
	s_waitcnt lgkmcnt(1)
	v_mfma_f32_32x32x16_bf16 v[112:127], v[162:165], v[146:149], v[112:127]
	s_waitcnt lgkmcnt(0)
	v_mfma_f32_32x32x16_bf16 v[96:111], v[166:169], v[146:149], v[96:111]
	ds_read_b128 v[162:165], v215 offset:49152
	ds_read_b128 v[166:169], v215 offset:57344
	s_waitcnt lgkmcnt(1)
	v_mfma_f32_32x32x16_bf16 v[112:127], v[162:165], v[142:145], v[112:127]
	s_waitcnt lgkmcnt(0)
	v_mfma_f32_32x32x16_bf16 v[96:111], v[166:169], v[142:145], v[96:111]
	ds_read_b128 v[162:165], v217 offset:49152
	ds_read_b128 v[166:169], v217 offset:57344
	s_waitcnt lgkmcnt(1)
	v_mfma_f32_32x32x16_bf16 v[112:127], v[162:165], v[138:141], v[112:127]
	s_waitcnt lgkmcnt(0)
	v_mfma_f32_32x32x16_bf16 v[96:111], v[166:169], v[138:141], v[96:111]
	ds_read_b128 v[162:165], v214 offset:49152
	ds_read_b128 v[166:169], v214 offset:57344
	s_waitcnt lgkmcnt(1)
	v_mfma_f32_32x32x16_bf16 v[112:127], v[162:165], v[134:137], v[112:127]
	s_waitcnt lgkmcnt(0)
	v_mfma_f32_32x32x16_bf16 v[96:111], v[166:169], v[134:137], v[96:111]
	ds_read_b128 v[162:165], v216 offset:49152
	ds_read_b128 v[166:169], v216 offset:57344
	s_waitcnt lgkmcnt(1)
	v_mfma_f32_32x32x16_bf16 v[112:127], v[162:165], v[130:133], v[112:127]
	s_waitcnt lgkmcnt(0)
	v_mfma_f32_32x32x16_bf16 v[96:111], v[166:169], v[130:133], v[96:111]
	ds_read_b128 v[162:165], v233
	ds_read_b128 v[166:169], v233 offset:4096
	ds_read_b128 v[170:173], v204
	s_waitcnt lgkmcnt(0)
	v_mfma_f32_32x32x16_bf16 v[112:127], v[162:165], v[170:173], v[112:127]
	v_mfma_f32_32x32x16_bf16 v[96:111], v[166:169], v[170:173], v[96:111]
	ds_read_b128 v[162:165], v234
	ds_read_b128 v[166:169], v234 offset:4096
	ds_read_b128 v[170:173], v204 offset:1024
	s_waitcnt lgkmcnt(0)
	v_mfma_f32_32x32x16_bf16 v[112:127], v[162:165], v[170:173], v[112:127]
	v_mfma_f32_32x32x16_bf16 v[96:111], v[166:169], v[170:173], v[96:111]
	ds_read_b128 v[162:165], v236
	ds_read_b128 v[166:169], v236 offset:4096
	ds_read_b128 v[170:173], v204 offset:2048
	s_waitcnt lgkmcnt(0)
	v_mfma_f32_32x32x16_bf16 v[112:127], v[162:165], v[170:173], v[112:127]
	v_mfma_f32_32x32x16_bf16 v[96:111], v[166:169], v[170:173], v[96:111]
	ds_read_b128 v[162:165], v235
	ds_read_b128 v[166:169], v235 offset:4096
	ds_read_b128 v[170:173], v204 offset:3072
	s_waitcnt lgkmcnt(0)
	v_mfma_f32_32x32x16_bf16 v[112:127], v[162:165], v[170:173], v[112:127]
	v_exp_f32_e32 v162, v88
	v_exp_f32_e32 v163, v89
	v_exp_f32_e32 v164, v90
	v_exp_f32_e32 v165, v91
	v_add_f32_e32 v88, v64, v65
	v_add_f32_e32 v89, v72, v73
	v_add_f32_e32 v90, v80, v81
	v_add_f32_e32 v91, v162, v163
	v_add_f32_e32 v88, v66, v88
	v_add_f32_e32 v89, v74, v89
	v_add_f32_e32 v90, v82, v90
	v_add_f32_e32 v91, v164, v91
	v_add_f32_e32 v88, v67, v88
	v_add_f32_e32 v89, v75, v89
	v_add_f32_e32 v90, v83, v90
	v_add_f32_e32 v91, v165, v91
	v_add_f32_e32 v88, v68, v88
	v_add_f32_e32 v89, v76, v89
	v_add_f32_e32 v90, v84, v90
	v_add_f32_e32 v91, v92, v91
	v_add_f32_e32 v88, v69, v88
	v_add_f32_e32 v89, v77, v89
	v_add_f32_e32 v90, v85, v90
	v_add_f32_e32 v91, v93, v91
	v_add_f32_e32 v88, v70, v88
	v_add_f32_e32 v89, v78, v89
	v_add_f32_e32 v90, v86, v90
	v_add_f32_e32 v91, v94, v91
	v_add_f32_e32 v88, v71, v88
	v_add_f32_e32 v89, v79, v89
	v_add_f32_e32 v90, v87, v90
	v_add_f32_e32 v91, v95, v91
	v_add_f32_e32 v88, v89, v88
	v_add_f32_e32 v89, v91, v90
	v_add_f32_e32 v237, v88, v89
	v_mov_b32_e32 v238, v237
	v_cvt_pk_bf16_f32 v88, v64, v65
	v_cvt_pk_bf16_f32 v89, v66, v67
	v_cvt_pk_bf16_f32 v90, v68, v69
	v_cvt_pk_bf16_f32 v91, v70, v71
	s_nop 1
	v_permlane32_swap_b32_e32 v237, v238
	v_cvt_pk_bf16_f32 v72, v72, v73
	v_cvt_pk_bf16_f32 v73, v74, v75
	v_cvt_pk_bf16_f32 v74, v76, v77
	v_cvt_pk_bf16_f32 v75, v78, v79
	v_cvt_pk_bf16_f32 v64, v80, v81
	v_cvt_pk_bf16_f32 v65, v82, v83
	v_cvt_pk_bf16_f32 v66, v84, v85
	v_cvt_pk_bf16_f32 v67, v86, v87
	v_cvt_pk_bf16_f32 v68, v162, v163
	v_cvt_pk_bf16_f32 v69, v164, v165
	v_cvt_pk_bf16_f32 v70, v92, v93
	v_cvt_pk_bf16_f32 v71, v94, v95
	v_mfma_f32_32x32x16_bf16 v[96:111], v[166:169], v[170:173], v[96:111]
	v_lshl_add_u64 v[80:81], v[190:191], 0, s[6:7]
	global_load_dwordx4 v[162:165], v[80:81], off
	v_lshl_add_u64 v[80:81], v[192:193], 0, s[6:7]
	v_lshl_add_u64 v[76:77], v[188:189], 0, s[6:7]
	global_load_dwordx4 v[166:169], v[80:81], off
	v_lshl_add_u64 v[80:81], v[198:199], 0, s[6:7]
	global_load_dwordx4 v[76:79], v[76:77], off
	s_nop 0
	global_load_dwordx4 v[174:177], v[80:81], off
	global_load_dwordx4 v[170:173], v[186:187], off
	ds_read_b64_tr_b16 v[80:81], v201 offset:0
	ds_read_b64_tr_b16 v[82:83], v201 offset:0x800
	ds_read_b64_tr_b16 v[84:85], v201 offset:0x1000
	ds_read_b64_tr_b16 v[86:87], v201 offset:0x1800
	ds_read_b64_tr_b16 v[92:93], v201 offset:0x2000
	ds_read_b64_tr_b16 v[94:95], v201 offset:0x2800
	ds_read_b64_tr_b16 v[178:179], v201 offset:0x3000
	ds_read_b64_tr_b16 v[180:181], v201 offset:0x3800
	s_waitcnt lgkmcnt(0)
	s_nop 0
	v_mfma_f32_32x32x16_bf16 v[0:15], v[80:83], v[88:91], v[0:15]
	v_max_f32_e32 v80, v96, v97
	v_max3_f32 v81, v112, v113, v114
	v_max3_f32 v80, v80, v98, v99
	v_max3_f32 v81, v81, v115, v116
	v_max3_f32 v80, v80, v100, v101
	v_mfma_f32_32x32x16_bf16 v[0:15], v[84:87], v[72:75], v[0:15]
	v_max3_f32 v81, v81, v117, v118
	v_max3_f32 v80, v80, v102, v103
	v_max3_f32 v81, v81, v119, v120
	v_max3_f32 v80, v80, v104, v105
	v_max3_f32 v81, v81, v121, v122
	v_max3_f32 v80, v80, v106, v107
	v_max3_f32 v81, v81, v123, v124
	v_mfma_f32_32x32x16_bf16 v[0:15], v[92:95], v[64:67], v[0:15]
	v_max3_f32 v80, v80, v108, v109
	v_max3_f32 v81, v81, v125, v126
	v_max3_f32 v80, v80, v110, v111
	v_max3_f32 v194, v81, v127, v80
	ds_read_b64_tr_b16 v[80:81], v201 offset:0x200
	ds_read_b64_tr_b16 v[82:83], v201 offset:0xa00
	ds_read_b64_tr_b16 v[84:85], v201 offset:0x1200
	v_mfma_f32_32x32x16_bf16 v[0:15], v[178:181], v[68:71], v[0:15]
	ds_read_b64_tr_b16 v[86:87], v201 offset:0x1a00
	ds_read_b64_tr_b16 v[92:93], v201 offset:0x2200
	ds_read_b64_tr_b16 v[94:95], v201 offset:0x2a00
	ds_read_b64_tr_b16 v[178:179], v201 offset:0x3200
	ds_read_b64_tr_b16 v[180:181], v201 offset:0x3a00
	s_waitcnt lgkmcnt(0)
	v_mfma_f32_32x32x16_bf16 v[48:63], v[80:83], v[88:91], v[48:63]
	v_mov_b32_e32 v80, v194
	s_nop 1
	v_permlane32_swap_b32_e32 v194, v80
	v_max_f32_e32 v80, v194, v80
	v_sub_f32_e32 v81, v80, v227
	v_mfma_f32_32x32x16_bf16 v[48:63], v[84:87], v[72:75], v[48:63]
	v_cmp_ge_f32_e32 vcc, s34, v81
	v_max_f32_e32 v80, v227, v80
	v_sub_f32_e32 v81, v227, v80
	v_mul_f32_e32 v81, 0x3dd53b94, v81
	v_exp_f32_e32 v81, v81
	s_cmp_eq_u64 vcc, exec
	v_mfma_f32_32x32x16_bf16 v[48:63], v[92:95], v[64:67], v[48:63]
	s_cselect_b64 vcc, -1, 0
	v_cndmask_b32_e64 v202, v81, 1.0, vcc
	v_cndmask_b32_e32 v227, v80, v227, vcc
	ds_read_b64_tr_b16 v[80:81], v201 offset:0x400
	ds_read_b64_tr_b16 v[82:83], v201 offset:0xc00
	ds_read_b64_tr_b16 v[84:85], v201 offset:0x1400
	ds_read_b64_tr_b16 v[86:87], v201 offset:0x1c00
	v_mfma_f32_32x32x16_bf16 v[48:63], v[178:181], v[68:71], v[48:63]
	ds_read_b64_tr_b16 v[92:93], v201 offset:0x2400
	v_mul_f32_e32 v178, 0xbdd53b94, v227
	ds_read_b64_tr_b16 v[94:95], v201 offset:0x2c00
	v_fmamk_f32 v179, v112, 0x3dd53b94, v178
	v_fmamk_f32 v180, v113, 0x3dd53b94, v178
	ds_read_b64_tr_b16 v[112:113], v201 offset:0x3400
	v_fmamk_f32 v181, v114, 0x3dd53b94, v178
	v_fmamk_f32 v194, v115, 0x3dd53b94, v178
	ds_read_b64_tr_b16 v[114:115], v201 offset:0x3c00
	s_waitcnt lgkmcnt(0)
	v_fmamk_f32 v195, v116, 0x3dd53b94, v178
	v_fmamk_f32 v196, v117, 0x3dd53b94, v178
	v_fmamk_f32 v197, v118, 0x3dd53b94, v178
	v_fmamk_f32 v200, v119, 0x3dd53b94, v178
	v_fmamk_f32 v239, v120, 0x3dd53b94, v178
	v_fmamk_f32 v240, v121, 0x3dd53b94, v178
	v_fmamk_f32 v241, v122, 0x3dd53b94, v178
	v_fmamk_f32 v242, v123, 0x3dd53b94, v178
	v_fmamk_f32 v243, v124, 0x3dd53b94, v178
	v_fmamk_f32 v244, v125, 0x3dd53b94, v178
	v_fmamk_f32 v245, v126, 0x3dd53b94, v178
	v_fmamk_f32 v246, v127, 0x3dd53b94, v178
	v_mfma_f32_32x32x16_bf16 v[32:47], v[80:83], v[88:91], v[32:47]
	v_fma_f32 v116, v100, s54, v178
	v_fma_f32 v117, v101, s54, v178
	v_fma_f32 v118, v102, s54, v178
	v_fma_f32 v119, v103, s54, v178
	v_fma_f32 v120, v104, s54, v178
	v_fma_f32 v121, v105, s54, v178
	v_pk_fma_f32 v[122:123], v[106:107], s[54:55], v[178:179] op_sel_hi:[1,0,0]
	v_exp_f32_e32 v80, v179
	v_exp_f32_e32 v81, v180
	v_exp_f32_e32 v82, v181
	v_mfma_f32_32x32x16_bf16 v[32:47], v[84:87], v[72:75], v[32:47]
	v_exp_f32_e32 v83, v194
	v_exp_f32_e32 v84, v195
	v_exp_f32_e32 v85, v196
	v_exp_f32_e32 v86, v197
	v_exp_f32_e32 v87, v200
	v_pk_fma_f32 v[126:127], v[110:111], s[54:55], v[178:179] op_sel_hi:[1,0,0]
	v_pk_fma_f32 v[124:125], v[108:109], s[54:55], v[178:179] op_sel_hi:[1,0,0]
	v_mfma_f32_32x32x16_bf16 v[32:47], v[92:95], v[64:67], v[32:47]
	ds_read_b64_tr_b16 v[92:93], v201 offset:0x600
	ds_read_b64_tr_b16 v[94:95], v201 offset:0xe00
	v_mfma_f32_32x32x16_bf16 v[32:47], v[112:115], v[68:71], v[32:47]
	v_fma_f32 v112, v96, s54, v178
	v_fma_f32 v113, v97, s54, v178
	ds_read_b64_tr_b16 v[96:97], v201 offset:0x1600
	v_fma_f32 v114, v98, s54, v178
	v_fma_f32 v115, v99, s54, v178
	ds_read_b64_tr_b16 v[98:99], v201 offset:0x1e00
	ds_read_b64_tr_b16 v[100:101], v201 offset:0x2600
	ds_read_b64_tr_b16 v[102:103], v201 offset:0x2e00
	ds_read_b64_tr_b16 v[104:105], v201 offset:0x3600
	ds_read_b64_tr_b16 v[106:107], v201 offset:0x3e00
	s_waitcnt lgkmcnt(0)
	v_mfma_f32_32x32x16_bf16 v[16:31], v[92:95], v[88:91], v[16:31]
	v_exp_f32_e32 v88, v239
	v_exp_f32_e32 v89, v240
	v_exp_f32_e32 v90, v241
	v_exp_f32_e32 v91, v242
	v_exp_f32_e32 v92, v243
	v_exp_f32_e32 v93, v244
	v_exp_f32_e32 v94, v245
	v_mfma_f32_32x32x16_bf16 v[16:31], v[96:99], v[72:75], v[16:31]
	v_exp_f32_e32 v95, v246
	s_barrier
	s_waitcnt vmcnt(0)
	v_cmp_gt_f32_e32 vcc, 1.0, v202
	v_mfma_f32_32x32x16_bf16 v[16:31], v[100:103], v[64:67], v[16:31]
	v_add_u32_e32 v64, 0x10000, v228
	s_waitcnt vmcnt(2)
	ds_write_b128 v205, v[76:79]
	ds_write_b128 v206, v[162:165]
	ds_write_b128 v207, v[166:169] offset:32768
	s_waitcnt vmcnt(1)
	ds_write_b128 v208, v[174:177] offset:32768
	s_waitcnt vmcnt(0)
	ds_write_b128 v64, v[170:173]
	v_mfma_f32_32x32x16_bf16 v[16:31], v[104:107], v[68:71], v[16:31]
	s_cbranch_vccz .LBB0_863
	v_pk_mul_f32 v[14:15], v[14:15], v[202:203] op_sel_hi:[1,0]
	v_pk_mul_f32 v[12:13], v[12:13], v[202:203] op_sel_hi:[1,0]
	v_pk_mul_f32 v[10:11], v[10:11], v[202:203] op_sel_hi:[1,0]
	v_pk_mul_f32 v[8:9], v[8:9], v[202:203] op_sel_hi:[1,0]
	v_pk_mul_f32 v[6:7], v[6:7], v[202:203] op_sel_hi:[1,0]
	v_pk_mul_f32 v[4:5], v[4:5], v[202:203] op_sel_hi:[1,0]
	v_pk_mul_f32 v[2:3], v[2:3], v[202:203] op_sel_hi:[1,0]
	v_pk_mul_f32 v[0:1], v[0:1], v[202:203] op_sel_hi:[1,0]
	v_pk_mul_f32 v[62:63], v[62:63], v[202:203] op_sel_hi:[1,0]
	v_pk_mul_f32 v[60:61], v[60:61], v[202:203] op_sel_hi:[1,0]
	v_pk_mul_f32 v[58:59], v[58:59], v[202:203] op_sel_hi:[1,0]
	v_pk_mul_f32 v[56:57], v[56:57], v[202:203] op_sel_hi:[1,0]
	v_pk_mul_f32 v[54:55], v[54:55], v[202:203] op_sel_hi:[1,0]
	v_pk_mul_f32 v[52:53], v[52:53], v[202:203] op_sel_hi:[1,0]
	v_pk_mul_f32 v[50:51], v[50:51], v[202:203] op_sel_hi:[1,0]
	v_pk_mul_f32 v[48:49], v[48:49], v[202:203] op_sel_hi:[1,0]
	v_pk_mul_f32 v[46:47], v[202:203], v[46:47] op_sel_hi:[0,1]
	v_pk_mul_f32 v[44:45], v[202:203], v[44:45] op_sel_hi:[0,1]
	v_pk_mul_f32 v[42:43], v[202:203], v[42:43] op_sel_hi:[0,1]
	v_pk_mul_f32 v[40:41], v[202:203], v[40:41] op_sel_hi:[0,1]
	v_pk_mul_f32 v[38:39], v[202:203], v[38:39] op_sel_hi:[0,1]
	v_pk_mul_f32 v[36:37], v[202:203], v[36:37] op_sel_hi:[0,1]
	v_pk_mul_f32 v[34:35], v[202:203], v[34:35] op_sel_hi:[0,1]
	v_pk_mul_f32 v[32:33], v[202:203], v[32:33] op_sel_hi:[0,1]
	v_pk_mul_f32 v[30:31], v[202:203], v[30:31] op_sel_hi:[0,1]
	v_pk_mul_f32 v[28:29], v[202:203], v[28:29] op_sel_hi:[0,1]
	v_pk_mul_f32 v[26:27], v[202:203], v[26:27] op_sel_hi:[0,1]
	v_pk_mul_f32 v[24:25], v[202:203], v[24:25] op_sel_hi:[0,1]
	v_pk_mul_f32 v[22:23], v[202:203], v[22:23] op_sel_hi:[0,1]
	v_pk_mul_f32 v[20:21], v[202:203], v[20:21] op_sel_hi:[0,1]
	v_pk_mul_f32 v[18:19], v[202:203], v[18:19] op_sel_hi:[0,1]
	v_pk_mul_f32 v[16:17], v[202:203], v[16:17] op_sel_hi:[0,1]
.LBB0_863:
	s_waitcnt lgkmcnt(0)
	s_barrier
	ds_read_b128 v[64:67], v209 offset:32768
	ds_read_b128 v[68:71], v209 offset:40960
	ds_read_b128 v[162:165], v211 offset:32768
	ds_read_b128 v[166:169], v211 offset:40960
	v_exp_f32_e32 v112, v112
	v_exp_f32_e32 v113, v113
	s_waitcnt lgkmcnt(3)
	v_mfma_f32_32x32x16_bf16 v[96:111], v[64:67], v[158:161], 0
	v_exp_f32_e32 v114, v114
	v_exp_f32_e32 v115, v115
	v_exp_f32_e32 v116, v116
	v_exp_f32_e32 v117, v117
	v_exp_f32_e32 v118, v118
	v_exp_f32_e32 v119, v119
	s_waitcnt lgkmcnt(2)
	v_mfma_f32_32x32x16_bf16 v[64:79], v[68:71], v[158:161], 0
	s_waitcnt lgkmcnt(1)
	v_mfma_f32_32x32x16_bf16 v[96:111], v[162:165], v[154:157], v[96:111]
	s_waitcnt lgkmcnt(0)
	v_mfma_f32_32x32x16_bf16 v[64:79], v[166:169], v[154:157], v[64:79]
	ds_read_b128 v[162:165], v212 offset:32768
	ds_read_b128 v[166:169], v212 offset:40960
	s_waitcnt lgkmcnt(1)
	v_mfma_f32_32x32x16_bf16 v[96:111], v[162:165], v[150:153], v[96:111]
	s_waitcnt lgkmcnt(0)
	v_mfma_f32_32x32x16_bf16 v[64:79], v[166:169], v[150:153], v[64:79]
	ds_read_b128 v[162:165], v213 offset:32768
	ds_read_b128 v[166:169], v213 offset:40960
	s_waitcnt lgkmcnt(1)
	v_mfma_f32_32x32x16_bf16 v[96:111], v[162:165], v[146:149], v[96:111]
	s_waitcnt lgkmcnt(0)
	v_mfma_f32_32x32x16_bf16 v[64:79], v[166:169], v[146:149], v[64:79]
	ds_read_b128 v[162:165], v215 offset:32768
	ds_read_b128 v[166:169], v215 offset:40960
	s_waitcnt lgkmcnt(1)
	v_mfma_f32_32x32x16_bf16 v[96:111], v[162:165], v[142:145], v[96:111]
	s_waitcnt lgkmcnt(0)
	v_mfma_f32_32x32x16_bf16 v[64:79], v[166:169], v[142:145], v[64:79]
	ds_read_b128 v[162:165], v217 offset:32768
	ds_read_b128 v[166:169], v217 offset:40960
	s_waitcnt lgkmcnt(1)
	v_mfma_f32_32x32x16_bf16 v[96:111], v[162:165], v[138:141], v[96:111]
	s_waitcnt lgkmcnt(0)
	v_mfma_f32_32x32x16_bf16 v[64:79], v[166:169], v[138:141], v[64:79]
	ds_read_b128 v[162:165], v214 offset:32768
	ds_read_b128 v[166:169], v214 offset:40960
	s_waitcnt lgkmcnt(1)
	v_mfma_f32_32x32x16_bf16 v[96:111], v[162:165], v[134:137], v[96:111]
	s_waitcnt lgkmcnt(0)
	v_mfma_f32_32x32x16_bf16 v[64:79], v[166:169], v[134:137], v[64:79]
	ds_read_b128 v[162:165], v216 offset:32768
	ds_read_b128 v[166:169], v216 offset:40960
	s_waitcnt lgkmcnt(1)
	v_mfma_f32_32x32x16_bf16 v[96:111], v[162:165], v[130:133], v[96:111]
	s_waitcnt lgkmcnt(0)
	v_mfma_f32_32x32x16_bf16 v[64:79], v[166:169], v[130:133], v[64:79]
	ds_read_b128 v[162:165], v219
	ds_read_b128 v[166:169], v219 offset:4096
	ds_read_b128 v[170:173], v204
	s_waitcnt lgkmcnt(0)
	v_mfma_f32_32x32x16_bf16 v[96:111], v[162:165], v[170:173], v[96:111]
	v_mfma_f32_32x32x16_bf16 v[64:79], v[166:169], v[170:173], v[64:79]
	ds_read_b128 v[162:165], v221
	ds_read_b128 v[166:169], v221 offset:4096
	ds_read_b128 v[170:173], v204 offset:1024
	s_waitcnt lgkmcnt(0)
	v_mfma_f32_32x32x16_bf16 v[96:111], v[162:165], v[170:173], v[96:111]
	v_mfma_f32_32x32x16_bf16 v[64:79], v[166:169], v[170:173], v[64:79]
	ds_read_b128 v[162:165], v223
	ds_read_b128 v[166:169], v223 offset:4096
	ds_read_b128 v[170:173], v204 offset:2048
	s_waitcnt lgkmcnt(0)
	v_mfma_f32_32x32x16_bf16 v[96:111], v[162:165], v[170:173], v[96:111]
	v_mfma_f32_32x32x16_bf16 v[64:79], v[166:169], v[170:173], v[64:79]
	ds_read_b128 v[162:165], v225
	ds_read_b128 v[166:169], v225 offset:4096
	ds_read_b128 v[170:173], v204 offset:3072
	s_waitcnt lgkmcnt(0)
	v_mfma_f32_32x32x16_bf16 v[96:111], v[162:165], v[170:173], v[96:111]
	v_exp_f32_e32 v162, v120
	v_exp_f32_e32 v163, v121
	v_exp_f32_e32 v164, v122
	v_exp_f32_e32 v165, v123
	v_add_f32_e32 v120, v80, v81
	v_add_f32_e32 v121, v88, v89
	v_add_f32_e32 v122, v112, v113
	v_mfma_f32_32x32x16_bf16 v[64:79], v[166:169], v[170:173], v[64:79]
	v_exp_f32_e32 v166, v124
	v_exp_f32_e32 v167, v125
	v_add_f32_e32 v123, v162, v163
	v_exp_f32_e32 v168, v126
	v_add_f32_e32 v120, v82, v120
	v_add_f32_e32 v121, v90, v121
	v_add_f32_e32 v122, v114, v122
	v_add_f32_e32 v123, v164, v123
	v_exp_f32_e32 v169, v127
	v_add_f32_e32 v120, v83, v120
	v_add_f32_e32 v121, v91, v121
	v_add_f32_e32 v122, v115, v122
	v_add_f32_e32 v123, v165, v123
	v_add_f32_e32 v120, v84, v120
	v_add_f32_e32 v121, v92, v121
	v_add_f32_e32 v122, v116, v122
	v_add_f32_e32 v123, v166, v123
	v_add_f32_e32 v120, v85, v120
	v_add_f32_e32 v121, v93, v121
	v_add_f32_e32 v122, v117, v122
	v_add_f32_e32 v123, v167, v123
	v_add_f32_e32 v120, v86, v120
	v_add_f32_e32 v121, v94, v121
	v_add_f32_e32 v122, v118, v122
	v_add_f32_e32 v123, v168, v123
	v_add_f32_e32 v120, v87, v120
	v_add_f32_e32 v121, v95, v121
	v_add_f32_e32 v122, v119, v122
	v_add_f32_e32 v123, v169, v123
	v_add_f32_e32 v120, v121, v120
	v_add_f32_e32 v121, v123, v122
	v_add_f32_e32 v239, v120, v121
	v_mov_b32_e32 v240, v239
	s_nop 1
	v_permlane32_swap_b32_e32 v239, v240
	v_cvt_pk_bf16_f32 v124, v80, v81
	v_cvt_pk_bf16_f32 v125, v82, v83
	v_cvt_pk_bf16_f32 v126, v84, v85
	v_cvt_pk_bf16_f32 v127, v86, v87
	v_cvt_pk_bf16_f32 v120, v88, v89
	v_cvt_pk_bf16_f32 v121, v90, v91
	v_cvt_pk_bf16_f32 v122, v92, v93
	v_cvt_pk_bf16_f32 v123, v94, v95
	v_cvt_pk_bf16_f32 v112, v112, v113
	v_cvt_pk_bf16_f32 v113, v114, v115
	v_cvt_pk_bf16_f32 v114, v116, v117
	v_cvt_pk_bf16_f32 v115, v118, v119
	v_cvt_pk_bf16_f32 v116, v162, v163
	v_cvt_pk_bf16_f32 v117, v164, v165
	v_cvt_pk_bf16_f32 v118, v166, v167
	v_cvt_pk_bf16_f32 v119, v168, v169
	s_add_i32 s2, s20, 1
	s_min_i32 s2, s2, s23
	s_lshl_b32 s72, s2, 6
	s_mul_i32 s2, s72, s62
	s_mov_b32 s3, s73
	s_lshl_b64 s[2:3], s[2:3], 1
	s_add_u32 s24, s18, s2
	s_addc_u32 s25, s19, s3
	s_add_u32 s2, s16, s2
	s_addc_u32 s3, s17, s3
	global_load_dwordx4 v[162:165], v128, s[24:25]
	global_load_dwordx4 v[166:169], v182, s[24:25]
	global_load_dwordx4 v[170:173], v128, s[2:3]
	global_load_dwordx4 v[174:177], v182, s[2:3]
	s_lshl_b64 s[2:3], s[72:73], 7
	v_lshl_add_u64 v[80:81], v[184:185], 0, s[2:3]
	global_load_dwordx4 v[178:181], v[80:81], off
	ds_read_b64_tr_b16 v[80:81], v203 offset:0
	ds_read_b64_tr_b16 v[82:83], v203 offset:0x800
	ds_read_b64_tr_b16 v[84:85], v203 offset:0x1000
	ds_read_b64_tr_b16 v[86:87], v203 offset:0x1800
	ds_read_b64_tr_b16 v[88:89], v203 offset:0x2000
	ds_read_b64_tr_b16 v[90:91], v203 offset:0x2800
	ds_read_b64_tr_b16 v[92:93], v203 offset:0x3000
	ds_read_b64_tr_b16 v[94:95], v203 offset:0x3800
	s_waitcnt lgkmcnt(0)
	s_nop 0
	v_mfma_f32_32x32x16_bf16 v[0:15], v[80:83], v[124:127], v[0:15]
	v_max_f32_e32 v80, v64, v65
	v_max3_f32 v81, v96, v97, v98
	v_max3_f32 v80, v80, v66, v67
	v_max3_f32 v81, v81, v99, v100
	v_max3_f32 v80, v80, v68, v69
	v_mfma_f32_32x32x16_bf16 v[0:15], v[84:87], v[120:123], v[0:15]
	v_max3_f32 v81, v81, v101, v102
	v_max3_f32 v80, v80, v70, v71
	v_max3_f32 v81, v81, v103, v104
	v_max3_f32 v80, v80, v72, v73
	v_max3_f32 v81, v81, v105, v106
	v_max3_f32 v80, v80, v74, v75
	v_max3_f32 v81, v81, v107, v108
	v_mfma_f32_32x32x16_bf16 v[0:15], v[88:91], v[112:115], v[0:15]
	v_max3_f32 v80, v80, v76, v77
	v_max3_f32 v81, v81, v109, v110
	v_max3_f32 v80, v80, v78, v79
	v_max3_f32 v194, v81, v111, v80
	ds_read_b64_tr_b16 v[80:81], v203 offset:0x200
	ds_read_b64_tr_b16 v[82:83], v203 offset:0xa00
	ds_read_b64_tr_b16 v[84:85], v203 offset:0x1200
	v_mfma_f32_32x32x16_bf16 v[0:15], v[92:95], v[116:119], v[0:15]
	ds_read_b64_tr_b16 v[86:87], v203 offset:0x1a00
	ds_read_b64_tr_b16 v[88:89], v203 offset:0x2200
	ds_read_b64_tr_b16 v[90:91], v203 offset:0x2a00
	ds_read_b64_tr_b16 v[92:93], v203 offset:0x3200
	ds_read_b64_tr_b16 v[94:95], v203 offset:0x3a00
	s_waitcnt lgkmcnt(0)
	v_mfma_f32_32x32x16_bf16 v[48:63], v[80:83], v[124:127], v[48:63]
	v_mov_b32_e32 v80, v194
	s_nop 1
	v_permlane32_swap_b32_e32 v194, v80
	v_max_f32_e32 v80, v194, v80
	v_sub_f32_e32 v81, v80, v227
	v_mfma_f32_32x32x16_bf16 v[48:63], v[84:87], v[120:123], v[48:63]
	v_cmp_ge_f32_e32 vcc, s34, v81
	v_max_f32_e32 v80, v227, v80
	v_sub_f32_e32 v81, v227, v80
	v_mul_f32_e32 v81, 0x3dd53b94, v81
	v_exp_f32_e32 v81, v81
	s_cmp_eq_u64 vcc, exec
	v_mfma_f32_32x32x16_bf16 v[48:63], v[88:91], v[112:115], v[48:63]
	s_cselect_b64 vcc, -1, 0
	v_cndmask_b32_e64 v200, v81, 1.0, vcc
	v_cndmask_b32_e32 v227, v80, v227, vcc
	ds_read_b64_tr_b16 v[80:81], v203 offset:0x400
	ds_read_b64_tr_b16 v[82:83], v203 offset:0xc00
	ds_read_b64_tr_b16 v[84:85], v203 offset:0x1400
	ds_read_b64_tr_b16 v[86:87], v203 offset:0x1c00
	v_mfma_f32_32x32x16_bf16 v[48:63], v[92:95], v[116:119], v[48:63]
	ds_read_b64_tr_b16 v[88:89], v203 offset:0x2400
	ds_read_b64_tr_b16 v[90:91], v203 offset:0x2c00
	ds_read_b64_tr_b16 v[92:93], v203 offset:0x3400
	ds_read_b64_tr_b16 v[94:95], v203 offset:0x3c00
	s_waitcnt lgkmcnt(0)
	v_mul_f32_e32 v242, 0xbdd53b94, v227
	v_fmamk_f32 v96, v96, 0x3dd53b94, v242
	v_fmamk_f32 v97, v97, 0x3dd53b94, v242
	v_fmamk_f32 v98, v98, 0x3dd53b94, v242
	v_fmamk_f32 v99, v99, 0x3dd53b94, v242
	v_fmamk_f32 v100, v100, 0x3dd53b94, v242
	v_fmamk_f32 v101, v101, 0x3dd53b94, v242
	v_fmamk_f32 v102, v102, 0x3dd53b94, v242
	v_fmamk_f32 v103, v103, 0x3dd53b94, v242
	v_fmamk_f32 v194, v104, 0x3dd53b94, v242
	v_fmamk_f32 v195, v105, 0x3dd53b94, v242
	v_fmamk_f32 v196, v106, 0x3dd53b94, v242
	v_fmamk_f32 v197, v107, 0x3dd53b94, v242
	v_fmamk_f32 v108, v108, 0x3dd53b94, v242
	v_fmamk_f32 v109, v109, 0x3dd53b94, v242
	v_fmamk_f32 v110, v110, 0x3dd53b94, v242
	v_fmamk_f32 v111, v111, 0x3dd53b94, v242
	v_mfma_f32_32x32x16_bf16 v[32:47], v[80:83], v[124:127], v[32:47]
	v_fma_f32 v80, v64, s54, v242
	v_fma_f32 v81, v65, s54, v242
	v_exp_f32_e32 v64, v96
	v_exp_f32_e32 v65, v97
	v_pk_fma_f32 v[82:83], v[66:67], s[54:55], v[242:243] op_sel_hi:[1,0,0]
	v_exp_f32_e32 v66, v98
	v_exp_f32_e32 v67, v99
	v_mfma_f32_32x32x16_bf16 v[32:47], v[84:87], v[120:123], v[32:47]
	v_fma_f32 v84, v68, s54, v242
	v_fma_f32 v85, v69, s54, v242
	v_exp_f32_e32 v68, v100
	v_exp_f32_e32 v69, v101
	v_pk_fma_f32 v[86:87], v[70:71], s[54:55], v[242:243] op_sel_hi:[1,0,0]
	v_exp_f32_e32 v70, v102
	v_exp_f32_e32 v71, v103
	v_mfma_f32_32x32x16_bf16 v[32:47], v[88:91], v[112:115], v[32:47]
	v_fma_f32 v88, v72, s54, v242
	v_fma_f32 v89, v73, s54, v242
	ds_read_b64_tr_b16 v[72:73], v203 offset:0x600
	v_fma_f32 v90, v74, s54, v242
	v_fma_f32 v91, v75, s54, v242
	ds_read_b64_tr_b16 v[74:75], v203 offset:0xe00
	ds_read_b64_tr_b16 v[96:97], v203 offset:0x1600
	ds_read_b64_tr_b16 v[98:99], v203 offset:0x1e00
	ds_read_b64_tr_b16 v[100:101], v203 offset:0x2600
	v_mfma_f32_32x32x16_bf16 v[32:47], v[92:95], v[116:119], v[32:47]
	ds_read_b64_tr_b16 v[102:103], v203 offset:0x2e00
	ds_read_b64_tr_b16 v[104:105], v203 offset:0x3600
	ds_read_b64_tr_b16 v[106:107], v203 offset:0x3e00
	s_waitcnt lgkmcnt(0)
	v_fma_f32 v94, v78, s54, v242
	v_fma_f32 v95, v79, s54, v242
	v_fma_f32 v92, v76, s54, v242
	v_fma_f32 v93, v77, s54, v242
	v_mfma_f32_32x32x16_bf16 v[16:31], v[72:75], v[124:127], v[16:31]
	v_exp_f32_e32 v72, v194
	v_exp_f32_e32 v73, v195
	v_exp_f32_e32 v74, v196
	v_exp_f32_e32 v75, v197
	v_exp_f32_e32 v76, v108
	v_exp_f32_e32 v77, v109
	v_exp_f32_e32 v78, v110
	v_mfma_f32_32x32x16_bf16 v[16:31], v[96:99], v[120:123], v[16:31]
	v_exp_f32_e32 v79, v111
	s_barrier
	s_waitcnt vmcnt(0)
	v_cmp_gt_f32_e32 vcc, 1.0, v200
	v_mfma_f32_32x32x16_bf16 v[16:31], v[100:103], v[112:115], v[16:31]
	s_waitcnt vmcnt(4)
	ds_write_b128 v205, v[162:165] offset:16384
	s_waitcnt vmcnt(3)
	ds_write_b128 v206, v[166:169] offset:16384
	s_waitcnt vmcnt(2)
	ds_write_b128 v207, v[170:173] offset:49152
	s_waitcnt vmcnt(1)
	ds_write_b128 v208, v[174:177] offset:49152
	s_waitcnt vmcnt(0)
	ds_write_b128 v229, v[178:181]
	v_mfma_f32_32x32x16_bf16 v[16:31], v[104:107], v[116:119], v[16:31]
	s_cbranch_vccz .LBB0_865
	v_pk_mul_f32 v[14:15], v[14:15], v[200:201] op_sel_hi:[1,0]
	v_pk_mul_f32 v[12:13], v[12:13], v[200:201] op_sel_hi:[1,0]
	v_pk_mul_f32 v[10:11], v[10:11], v[200:201] op_sel_hi:[1,0]
	v_pk_mul_f32 v[8:9], v[8:9], v[200:201] op_sel_hi:[1,0]
	v_pk_mul_f32 v[6:7], v[6:7], v[200:201] op_sel_hi:[1,0]
	v_pk_mul_f32 v[4:5], v[4:5], v[200:201] op_sel_hi:[1,0]
	v_pk_mul_f32 v[2:3], v[2:3], v[200:201] op_sel_hi:[1,0]
	v_pk_mul_f32 v[0:1], v[0:1], v[200:201] op_sel_hi:[1,0]
	v_pk_mul_f32 v[62:63], v[62:63], v[200:201] op_sel_hi:[1,0]
	v_pk_mul_f32 v[60:61], v[60:61], v[200:201] op_sel_hi:[1,0]
	v_pk_mul_f32 v[58:59], v[58:59], v[200:201] op_sel_hi:[1,0]
	v_pk_mul_f32 v[56:57], v[56:57], v[200:201] op_sel_hi:[1,0]
	v_pk_mul_f32 v[54:55], v[54:55], v[200:201] op_sel_hi:[1,0]
	v_pk_mul_f32 v[52:53], v[52:53], v[200:201] op_sel_hi:[1,0]
	v_pk_mul_f32 v[50:51], v[50:51], v[200:201] op_sel_hi:[1,0]
	v_pk_mul_f32 v[48:49], v[48:49], v[200:201] op_sel_hi:[1,0]
	v_pk_mul_f32 v[46:47], v[200:201], v[46:47] op_sel_hi:[0,1]
	v_pk_mul_f32 v[44:45], v[200:201], v[44:45] op_sel_hi:[0,1]
	v_pk_mul_f32 v[42:43], v[200:201], v[42:43] op_sel_hi:[0,1]
	v_pk_mul_f32 v[40:41], v[200:201], v[40:41] op_sel_hi:[0,1]
	v_pk_mul_f32 v[38:39], v[200:201], v[38:39] op_sel_hi:[0,1]
	v_pk_mul_f32 v[36:37], v[200:201], v[36:37] op_sel_hi:[0,1]
	v_pk_mul_f32 v[34:35], v[200:201], v[34:35] op_sel_hi:[0,1]
	v_pk_mul_f32 v[32:33], v[200:201], v[32:33] op_sel_hi:[0,1]
	v_pk_mul_f32 v[30:31], v[200:201], v[30:31] op_sel_hi:[0,1]
	v_pk_mul_f32 v[28:29], v[200:201], v[28:29] op_sel_hi:[0,1]
	v_pk_mul_f32 v[26:27], v[200:201], v[26:27] op_sel_hi:[0,1]
	v_pk_mul_f32 v[24:25], v[200:201], v[24:25] op_sel_hi:[0,1]
	v_pk_mul_f32 v[22:23], v[200:201], v[22:23] op_sel_hi:[0,1]
	v_pk_mul_f32 v[20:21], v[200:201], v[20:21] op_sel_hi:[0,1]
	v_pk_mul_f32 v[18:19], v[200:201], v[18:19] op_sel_hi:[0,1]
	v_pk_mul_f32 v[16:17], v[200:201], v[16:17] op_sel_hi:[0,1]

.LBB0_867:
	ds_read_b128 v[96:99], v209 offset:49152
	ds_read_b128 v[100:103], v209 offset:57344
	v_exp_f32_e32 v80, v80
	v_exp_f32_e32 v81, v81
	v_exp_f32_e32 v88, v88
	s_waitcnt lgkmcnt(1)
	v_mfma_f32_32x32x16_bf16 v[112:127], v[96:99], v[158:161], 0
	v_exp_f32_e32 v89, v89
	v_exp_f32_e32 v82, v82
	v_exp_f32_e32 v90, v90
	v_exp_f32_e32 v83, v83
	v_exp_f32_e32 v91, v91
	v_exp_f32_e32 v84, v84
	v_exp_f32_e32 v92, v92
	s_waitcnt lgkmcnt(0)
	v_mfma_f32_32x32x16_bf16 v[96:111], v[100:103], v[158:161], 0
	ds_read_b128 v[158:161], v211 offset:49152
	ds_read_b128 v[162:165], v211 offset:57344
	v_exp_f32_e32 v85, v85
	v_exp_f32_e32 v93, v93
	v_add_f32_e32 v128, v64, v65
	v_exp_f32_e32 v86, v86
	v_exp_f32_e32 v94, v94
	v_add_f32_e32 v128, v66, v128
	s_waitcnt lgkmcnt(1)
	v_mfma_f32_32x32x16_bf16 v[112:127], v[158:161], v[154:157], v[112:127]
	v_exp_f32_e32 v87, v87
	v_exp_f32_e32 v95, v95
	v_add_f32_e32 v128, v67, v128
	v_add_f32_e32 v128, v68, v128
	v_add_f32_e32 v128, v69, v128
	v_add_f32_e32 v128, v70, v128
	v_add_f32_e32 v128, v71, v128
	s_waitcnt lgkmcnt(0)
	v_mfma_f32_32x32x16_bf16 v[96:111], v[162:165], v[154:157], v[96:111]
	ds_read_b128 v[154:157], v212 offset:49152
	ds_read_b128 v[158:161], v212 offset:57344
	s_waitcnt lgkmcnt(1)
	v_mfma_f32_32x32x16_bf16 v[112:127], v[154:157], v[150:153], v[112:127]
	s_waitcnt lgkmcnt(0)
	v_mfma_f32_32x32x16_bf16 v[96:111], v[158:161], v[150:153], v[96:111]
	ds_read_b128 v[150:153], v213 offset:49152
	ds_read_b128 v[154:157], v213 offset:57344
	s_waitcnt lgkmcnt(1)
	v_mfma_f32_32x32x16_bf16 v[112:127], v[150:153], v[146:149], v[112:127]
	s_waitcnt lgkmcnt(0)
	v_mfma_f32_32x32x16_bf16 v[96:111], v[154:157], v[146:149], v[96:111]
	ds_read_b128 v[146:149], v215 offset:49152
	ds_read_b128 v[150:153], v215 offset:57344
	s_waitcnt lgkmcnt(1)
	v_mfma_f32_32x32x16_bf16 v[112:127], v[146:149], v[142:145], v[112:127]
	s_waitcnt lgkmcnt(0)
	v_mfma_f32_32x32x16_bf16 v[96:111], v[150:153], v[142:145], v[96:111]
	ds_read_b128 v[142:145], v217 offset:49152
	ds_read_b128 v[146:149], v217 offset:57344
	s_waitcnt lgkmcnt(1)
	v_mfma_f32_32x32x16_bf16 v[112:127], v[142:145], v[138:141], v[112:127]
	s_waitcnt lgkmcnt(0)
	v_mfma_f32_32x32x16_bf16 v[96:111], v[146:149], v[138:141], v[96:111]
	ds_read_b128 v[138:141], v214 offset:49152
	ds_read_b128 v[142:145], v214 offset:57344
	s_waitcnt lgkmcnt(1)
	v_mfma_f32_32x32x16_bf16 v[112:127], v[138:141], v[134:137], v[112:127]
	s_waitcnt lgkmcnt(0)
	v_mfma_f32_32x32x16_bf16 v[96:111], v[142:145], v[134:137], v[96:111]
	ds_read_b128 v[134:137], v216 offset:49152
	ds_read_b128 v[138:141], v216 offset:57344
	s_waitcnt lgkmcnt(1)
	v_mfma_f32_32x32x16_bf16 v[112:127], v[134:137], v[130:133], v[112:127]
	s_waitcnt lgkmcnt(0)
	v_mfma_f32_32x32x16_bf16 v[96:111], v[138:141], v[130:133], v[96:111]
	ds_read_b128 v[130:133], v233
	ds_read_b128 v[134:137], v233 offset:4096
	ds_read_b128 v[138:141], v204
	s_waitcnt lgkmcnt(0)
	v_mfma_f32_32x32x16_bf16 v[112:127], v[130:133], v[138:141], v[112:127]
	v_mfma_f32_32x32x16_bf16 v[96:111], v[134:137], v[138:141], v[96:111]
	ds_read_b128 v[130:133], v234
	ds_read_b128 v[134:137], v234 offset:4096
	ds_read_b128 v[138:141], v204 offset:1024
	s_waitcnt lgkmcnt(0)
	v_mfma_f32_32x32x16_bf16 v[112:127], v[130:133], v[138:141], v[112:127]
	v_mfma_f32_32x32x16_bf16 v[96:111], v[134:137], v[138:141], v[96:111]
	ds_read_b128 v[130:133], v236
	ds_read_b128 v[134:137], v236 offset:4096
	ds_read_b128 v[138:141], v204 offset:2048
	s_waitcnt lgkmcnt(0)
	v_mfma_f32_32x32x16_bf16 v[112:127], v[130:133], v[138:141], v[112:127]
	v_mfma_f32_32x32x16_bf16 v[96:111], v[134:137], v[138:141], v[96:111]
	ds_read_b128 v[130:133], v235
	ds_read_b128 v[134:137], v235 offset:4096
	ds_read_b128 v[138:141], v204 offset:3072
	s_waitcnt lgkmcnt(0)
	v_mfma_f32_32x32x16_bf16 v[112:127], v[130:133], v[138:141], v[112:127]
	v_add_f32_e32 v130, v72, v73
	v_add_f32_e32 v131, v80, v81
	v_add_f32_e32 v132, v88, v89
	v_add_f32_e32 v130, v74, v130
	v_add_f32_e32 v131, v82, v131
	v_add_f32_e32 v132, v90, v132
	v_add_f32_e32 v130, v75, v130
	v_add_f32_e32 v131, v83, v131
	v_add_f32_e32 v132, v91, v132
	v_add_f32_e32 v130, v76, v130
	v_add_f32_e32 v131, v84, v131
	v_add_f32_e32 v132, v92, v132
	v_add_f32_e32 v130, v77, v130
	v_add_f32_e32 v131, v85, v131
	v_add_f32_e32 v132, v93, v132
	v_add_f32_e32 v130, v78, v130
	v_add_f32_e32 v131, v86, v131
	v_add_f32_e32 v132, v94, v132
	v_add_f32_e32 v130, v79, v130
	v_add_f32_e32 v131, v87, v131
	v_add_f32_e32 v132, v95, v132
	v_add_f32_e32 v128, v130, v128
	v_add_f32_e32 v130, v132, v131
	v_add_f32_e32 v142, v128, v130
	v_mov_b32_e32 v143, v142
	v_cvt_pk_bf16_f32 v130, v64, v65
	v_cvt_pk_bf16_f32 v131, v66, v67
	v_cvt_pk_bf16_f32 v132, v68, v69
	v_cvt_pk_bf16_f32 v133, v70, v71
	v_cvt_pk_bf16_f32 v72, v72, v73
	v_cvt_pk_bf16_f32 v73, v74, v75
	v_cvt_pk_bf16_f32 v74, v76, v77
	v_cvt_pk_bf16_f32 v75, v78, v79
	v_mfma_f32_32x32x16_bf16 v[96:111], v[134:137], v[138:141], v[96:111]
	s_nop 0
	v_permlane32_swap_b32_e32 v142, v143
	v_cvt_pk_bf16_f32 v138, v80, v81
	v_cvt_pk_bf16_f32 v139, v82, v83
	v_cvt_pk_bf16_f32 v140, v84, v85
	v_cvt_pk_bf16_f32 v141, v86, v87
	v_cvt_pk_bf16_f32 v134, v88, v89
	v_cvt_pk_bf16_f32 v135, v90, v91
	v_cvt_pk_bf16_f32 v136, v92, v93
	v_cvt_pk_bf16_f32 v137, v94, v95
	ds_read_b64_tr_b16 v[64:65], v201 offset:0
	ds_read_b64_tr_b16 v[66:67], v201 offset:0x800
	ds_read_b64_tr_b16 v[68:69], v201 offset:0x1000
	ds_read_b64_tr_b16 v[70:71], v201 offset:0x1800
	ds_read_b64_tr_b16 v[76:77], v201 offset:0x2000
	ds_read_b64_tr_b16 v[78:79], v201 offset:0x2800
	ds_read_b64_tr_b16 v[80:81], v201 offset:0x3000
	ds_read_b64_tr_b16 v[82:83], v201 offset:0x3800
	s_waitcnt lgkmcnt(0)
	s_nop 0
	v_mfma_f32_32x32x16_bf16 v[0:15], v[64:67], v[130:133], v[0:15]
	v_max_f32_e32 v64, v97, v97
	v_max_f32_e32 v65, v96, v96
	v_max_f32_e32 v64, v65, v64
	v_max3_f32 v65, v112, v113, v114
	v_max3_f32 v64, v64, v98, v99
	v_max3_f32 v65, v65, v115, v116
	v_max3_f32 v64, v64, v100, v101
	v_mfma_f32_32x32x16_bf16 v[0:15], v[68:71], v[72:75], v[0:15]
	v_max3_f32 v65, v65, v117, v118
	v_max3_f32 v64, v64, v102, v103
	v_max3_f32 v65, v65, v119, v120
	v_max3_f32 v64, v64, v104, v105
	v_max3_f32 v65, v65, v121, v122
	v_max3_f32 v64, v64, v106, v107
	v_max3_f32 v65, v65, v123, v124
	v_mfma_f32_32x32x16_bf16 v[0:15], v[76:79], v[138:141], v[0:15]
	v_max3_f32 v64, v64, v108, v109
	v_max3_f32 v65, v65, v125, v126
	v_max3_f32 v64, v64, v110, v111
	v_max3_f32 v84, v65, v127, v64
	ds_read_b64_tr_b16 v[64:65], v201 offset:0x200
	ds_read_b64_tr_b16 v[66:67], v201 offset:0xa00
	ds_read_b64_tr_b16 v[68:69], v201 offset:0x1200
	v_mfma_f32_32x32x16_bf16 v[0:15], v[80:83], v[134:137], v[0:15]
	ds_read_b64_tr_b16 v[70:71], v201 offset:0x1a00
	ds_read_b64_tr_b16 v[76:77], v201 offset:0x2200
	ds_read_b64_tr_b16 v[78:79], v201 offset:0x2a00
	ds_read_b64_tr_b16 v[80:81], v201 offset:0x3200
	ds_read_b64_tr_b16 v[82:83], v201 offset:0x3a00
	s_waitcnt lgkmcnt(0)
	v_mfma_f32_32x32x16_bf16 v[48:63], v[64:67], v[130:133], v[48:63]
	v_mov_b32_e32 v64, v84
	s_nop 1
	v_permlane32_swap_b32_e32 v84, v64
	v_max_f32_e32 v64, v64, v64
	v_max_f32_e32 v65, v84, v84
	v_max_f32_e32 v64, v65, v64
	v_sub_f32_e32 v65, v64, v227
	v_mfma_f32_32x32x16_bf16 v[48:63], v[68:71], v[72:75], v[48:63]
	v_cmp_ge_f32_e32 vcc, s34, v65
	v_max_f32_e32 v65, v227, v227
	v_max_f32_e32 v64, v65, v64
	v_sub_f32_e32 v65, v227, v64
	v_mul_f32_e32 v65, 0x3dd53b94, v65
	v_exp_f32_e32 v65, v65
	s_cmp_eq_u64 vcc, exec
	v_mfma_f32_32x32x16_bf16 v[48:63], v[76:79], v[138:141], v[48:63]
	s_cselect_b64 vcc, -1, 0
	v_cndmask_b32_e32 v64, v64, v227, vcc
	v_cndmask_b32_e64 v128, v65, 1.0, vcc
	v_mul_f32_e32 v144, 0xbdd53b94, v64
	ds_read_b64_tr_b16 v[64:65], v201 offset:0x400
	ds_read_b64_tr_b16 v[66:67], v201 offset:0xc00
	ds_read_b64_tr_b16 v[68:69], v201 offset:0x1400
	v_mfma_f32_32x32x16_bf16 v[48:63], v[80:83], v[134:137], v[48:63]
	ds_read_b64_tr_b16 v[70:71], v201 offset:0x1c00
	ds_read_b64_tr_b16 v[76:77], v201 offset:0x2400
	ds_read_b64_tr_b16 v[78:79], v201 offset:0x2c00
	ds_read_b64_tr_b16 v[80:81], v201 offset:0x3400
	ds_read_b64_tr_b16 v[82:83], v201 offset:0x3c00
	s_waitcnt lgkmcnt(0)
	v_fmamk_f32 v112, v112, 0x3dd53b94, v144
	v_fmamk_f32 v113, v113, 0x3dd53b94, v144
	v_fmamk_f32 v114, v114, 0x3dd53b94, v144
	v_fmamk_f32 v115, v115, 0x3dd53b94, v144
	v_fmamk_f32 v116, v116, 0x3dd53b94, v144
	v_fmamk_f32 v117, v117, 0x3dd53b94, v144
	v_fmamk_f32 v118, v118, 0x3dd53b94, v144
	v_fmamk_f32 v119, v119, 0x3dd53b94, v144
	v_fmamk_f32 v120, v120, 0x3dd53b94, v144
	v_fmamk_f32 v121, v121, 0x3dd53b94, v144
	v_fmamk_f32 v122, v122, 0x3dd53b94, v144
	v_fmamk_f32 v123, v123, 0x3dd53b94, v144
	v_fmamk_f32 v124, v124, 0x3dd53b94, v144
	v_fmamk_f32 v125, v125, 0x3dd53b94, v144
	v_fmamk_f32 v126, v126, 0x3dd53b94, v144
	v_fmamk_f32 v127, v127, 0x3dd53b94, v144
	v_mfma_f32_32x32x16_bf16 v[32:47], v[64:67], v[130:133], v[32:47]
	v_fma_f32 v84, v100, s54, v144
	v_fma_f32 v85, v101, s54, v144
	v_fma_f32 v86, v102, s54, v144
	v_fma_f32 v87, v103, s54, v144
	v_fma_f32 v88, v104, s54, v144
	v_fma_f32 v89, v105, s54, v144
	v_pk_fma_f32 v[90:91], v[106:107], s[54:55], v[144:145] op_sel_hi:[1,0,0]
	v_exp_f32_e32 v64, v112
	v_exp_f32_e32 v65, v113
	v_exp_f32_e32 v66, v114
	v_mfma_f32_32x32x16_bf16 v[32:47], v[68:71], v[72:75], v[32:47]
	v_exp_f32_e32 v67, v115
	v_exp_f32_e32 v68, v116
	v_exp_f32_e32 v69, v117
	v_exp_f32_e32 v70, v118
	v_exp_f32_e32 v71, v119
	v_pk_fma_f32 v[94:95], v[110:111], s[54:55], v[144:145] op_sel_hi:[1,0,0]
	v_pk_fma_f32 v[92:93], v[108:109], s[54:55], v[144:145] op_sel_hi:[1,0,0]
	v_mfma_f32_32x32x16_bf16 v[32:47], v[76:79], v[138:141], v[32:47]
	ds_read_b64_tr_b16 v[76:77], v201 offset:0x600
	ds_read_b64_tr_b16 v[78:79], v201 offset:0xe00
	v_mfma_f32_32x32x16_bf16 v[32:47], v[80:83], v[134:137], v[32:47]
	v_fma_f32 v80, v96, s54, v144
	v_fma_f32 v81, v97, s54, v144
	ds_read_b64_tr_b16 v[96:97], v201 offset:0x1600
	v_fma_f32 v82, v98, s54, v144
	v_fma_f32 v83, v99, s54, v144
	ds_read_b64_tr_b16 v[98:99], v201 offset:0x1e00
	ds_read_b64_tr_b16 v[100:101], v201 offset:0x2600
	ds_read_b64_tr_b16 v[102:103], v201 offset:0x2e00
	ds_read_b64_tr_b16 v[104:105], v201 offset:0x3600
	ds_read_b64_tr_b16 v[106:107], v201 offset:0x3e00
	s_waitcnt lgkmcnt(0)
	v_mfma_f32_32x32x16_bf16 v[16:31], v[76:79], v[130:133], v[16:31]
	v_exp_f32_e32 v76, v124
	v_exp_f32_e32 v77, v125
	v_exp_f32_e32 v78, v126
	v_exp_f32_e32 v79, v127
	v_cmp_gt_f32_e32 vcc, 1.0, v128
	v_mfma_f32_32x32x16_bf16 v[16:31], v[96:99], v[72:75], v[16:31]
	v_exp_f32_e32 v72, v120
	v_exp_f32_e32 v73, v121
	v_exp_f32_e32 v74, v122
	v_exp_f32_e32 v75, v123
	s_barrier
	v_mfma_f32_32x32x16_bf16 v[16:31], v[100:103], v[138:141], v[16:31]
	v_mfma_f32_32x32x16_bf16 v[16:31], v[104:107], v[134:137], v[16:31]
	s_cbranch_vccz .LBB0_851
	v_pk_mul_f32 v[14:15], v[14:15], v[128:129] op_sel_hi:[1,0]
	v_pk_mul_f32 v[12:13], v[12:13], v[128:129] op_sel_hi:[1,0]
	v_pk_mul_f32 v[10:11], v[10:11], v[128:129] op_sel_hi:[1,0]
	v_pk_mul_f32 v[8:9], v[8:9], v[128:129] op_sel_hi:[1,0]
	v_pk_mul_f32 v[6:7], v[6:7], v[128:129] op_sel_hi:[1,0]
	v_pk_mul_f32 v[4:5], v[4:5], v[128:129] op_sel_hi:[1,0]
	v_pk_mul_f32 v[2:3], v[2:3], v[128:129] op_sel_hi:[1,0]
	v_pk_mul_f32 v[0:1], v[0:1], v[128:129] op_sel_hi:[1,0]
	v_pk_mul_f32 v[62:63], v[62:63], v[128:129] op_sel_hi:[1,0]
	v_pk_mul_f32 v[60:61], v[60:61], v[128:129] op_sel_hi:[1,0]
	v_pk_mul_f32 v[58:59], v[58:59], v[128:129] op_sel_hi:[1,0]
	v_pk_mul_f32 v[56:57], v[56:57], v[128:129] op_sel_hi:[1,0]
	v_pk_mul_f32 v[54:55], v[54:55], v[128:129] op_sel_hi:[1,0]
	v_pk_mul_f32 v[52:53], v[52:53], v[128:129] op_sel_hi:[1,0]
	v_pk_mul_f32 v[50:51], v[50:51], v[128:129] op_sel_hi:[1,0]
	v_pk_mul_f32 v[48:49], v[48:49], v[128:129] op_sel_hi:[1,0]
	v_pk_mul_f32 v[46:47], v[128:129], v[46:47] op_sel_hi:[0,1]
	v_pk_mul_f32 v[44:45], v[128:129], v[44:45] op_sel_hi:[0,1]
	v_pk_mul_f32 v[42:43], v[128:129], v[42:43] op_sel_hi:[0,1]
	v_pk_mul_f32 v[40:41], v[128:129], v[40:41] op_sel_hi:[0,1]
	v_pk_mul_f32 v[38:39], v[128:129], v[38:39] op_sel_hi:[0,1]
	v_pk_mul_f32 v[36:37], v[128:129], v[36:37] op_sel_hi:[0,1]
	v_pk_mul_f32 v[34:35], v[128:129], v[34:35] op_sel_hi:[0,1]
	v_pk_mul_f32 v[32:33], v[128:129], v[32:33] op_sel_hi:[0,1]
	v_pk_mul_f32 v[30:31], v[128:129], v[30:31] op_sel_hi:[0,1]
	v_pk_mul_f32 v[28:29], v[128:129], v[28:29] op_sel_hi:[0,1]
	v_pk_mul_f32 v[26:27], v[128:129], v[26:27] op_sel_hi:[0,1]
	v_pk_mul_f32 v[24:25], v[128:129], v[24:25] op_sel_hi:[0,1]
	v_pk_mul_f32 v[22:23], v[128:129], v[22:23] op_sel_hi:[0,1]
	v_pk_mul_f32 v[20:21], v[128:129], v[20:21] op_sel_hi:[0,1]
	v_pk_mul_f32 v[18:19], v[128:129], v[18:19] op_sel_hi:[0,1]
	v_pk_mul_f32 v[16:17], v[128:129], v[16:17] op_sel_hi:[0,1]
	s_branch .LBB0_851

.LBB0_880:
	v_add_u32_e32 v21, 32, v185
	v_and_b32_e32 v17, 0xfffff0, v185
	v_lshlrev_b32_e32 v18, 1, v185
	v_and_b32_e32 v22, 0xfffff0, v21
	v_lshlrev_b32_e32 v23, 1, v21
	v_and_b32_e32 v16, 63, v184
	v_and_or_b32 v17, v18, 8, v17
	v_and_or_b32 v22, v23, 8, v22
	v_lshrrev_b32_e32 v17, 1, v17
	v_lshrrev_b32_e32 v19, 5, v186
	v_lshrrev_b32_e32 v22, 1, v22
	v_lshlrev_b32_e32 v23, 4, v16
	v_lshrrev_b32_e32 v18, 1, v185
	v_or_b32_e32 v17, v17, v19
	v_and_b32_e32 v20, 3, v185
	v_or_b32_e32 v19, v22, v19
	v_lshlrev_b32_e32 v22, 3, v16
	v_and_b32_e32 v23, 0xc0, v23
	v_lshlrev_b32_e32 v16, 1, v16
	v_and_or_b32 v18, v18, 4, v20
	v_lshlrev_b32_e32 v20, 1, v186
	v_and_or_b32 v23, v22, 24, v23
	v_and_b32_e32 v16, 32, v16
	v_and_b32_e32 v22, 0x100, v22
	v_lshlrev_b32_e32 v17, 9, v17
	v_lshlrev_b32_e32 v18, 6, v18
	v_or3_b32 v114, v23, v16, v22
	v_and_b32_e32 v16, 48, v20
	v_or3_b32 v17, v17, v18, v16
	v_add_u32_e32 v212, 0, v17
	v_lshrrev_b32_e32 v17, 3, v212
	v_xor_b32_e32 v17, v17, v212
	v_and_b32_e32 v17, 0x100, v17
	v_xor_b32_e32 v212, v212, v17
	v_lshlrev_b32_e32 v17, 3, v17
	v_xor_b32_e32 v212, v212, v17
	v_lshlrev_b32_e32 v19, 9, v19
	v_cvt_pk_bf16_f32 v138, v176, v177
	v_cvt_pk_bf16_f32 v139, v170, v171
	v_cvt_pk_bf16_f32 v140, v164, v165
	v_cvt_pk_bf16_f32 v141, v144, v145
	v_cvt_pk_bf16_f32 v154, v142, v143
	v_cvt_pk_bf16_f32 v155, v136, v137
	v_cvt_pk_bf16_f32 v156, v134, v135
	v_cvt_pk_bf16_f32 v157, v132, v133
	v_cvt_pk_bf16_f32 v158, v130, v131
	v_cvt_pk_bf16_f32 v159, v126, v127
	v_cvt_pk_bf16_f32 v160, v124, v125
	v_cvt_pk_bf16_f32 v161, v122, v123
	v_cvt_pk_bf16_f32 v150, v120, v121
	v_cvt_pk_bf16_f32 v151, v118, v119
	v_cvt_pk_bf16_f32 v152, v116, v117
	v_cvt_pk_bf16_f32 v153, v112, v113
	v_cvt_pk_bf16_f32 v146, v108, v109
	v_cvt_pk_bf16_f32 v147, v110, v111
	v_cvt_pk_bf16_f32 v148, v104, v105
	v_cvt_pk_bf16_f32 v149, v106, v107
	v_cvt_pk_bf16_f32 v142, v100, v101
	v_cvt_pk_bf16_f32 v143, v102, v103
	v_cvt_pk_bf16_f32 v144, v96, v97
	v_cvt_pk_bf16_f32 v145, v98, v99
	v_cvt_pk_bf16_f32 v134, v92, v93
	v_cvt_pk_bf16_f32 v135, v94, v95
	v_cvt_pk_bf16_f32 v136, v88, v89
	v_cvt_pk_bf16_f32 v137, v90, v91
	v_cvt_pk_bf16_f32 v130, v84, v85
	v_cvt_pk_bf16_f32 v131, v86, v87
	v_cvt_pk_bf16_f32 v132, v80, v81
	v_cvt_pk_bf16_f32 v133, v82, v83
	s_waitcnt vmcnt(0)
	ds_write_b128 v212, v[8:11]
	v_lshlrev_b32_e32 v8, 8, v185
	v_and_b32_e32 v9, 0x70, v184
	v_or3_b32 v16, v19, v18, v16
	v_bitop3_b32 v8, v20, v8, v9 bitop3:0xde
	v_add_u32_e32 v213, 0, v16
	v_lshrrev_b32_e32 v16, 3, v213
	v_xor_b32_e32 v16, v16, v213
	v_and_b32_e32 v16, 0x100, v16
	v_xor_b32_e32 v213, v213, v16
	v_lshlrev_b32_e32 v16, 3, v16
	v_xor_b32_e32 v213, v213, v16
	v_add_u32_e32 v214, 0, v8
	ds_write_b128 v213, v[12:15]
	ds_write_b128 v214, v[4:7] offset:32768
	v_lshlrev_b32_e32 v4, 8, v21
	v_bitop3_b32 v4, v20, v4, v9 bitop3:0xde
	v_add_u32_e32 v215, 0, v4
	ds_write_b128 v215, v[0:3] offset:32768
	v_lshlrev_b32_e32 v0, 4, v163
	v_lshlrev_b32_e32 v56, 8, v163
	v_and_b32_e32 v57, 0x70, v0
	v_bitop3_b32 v0, v162, v56, v57 bitop3:0xde
	v_add_u32_e32 v216, 0, v0
	s_waitcnt lgkmcnt(0)
	s_barrier
	ds_read_b128 v[16:19], v216 offset:32768
	ds_read_b128 v[20:23], v216 offset:40960
	s_waitcnt lgkmcnt(1)
	v_mfma_f32_32x32x16_bf16 v[32:47], v[16:19], v[138:141], 0
	v_or_b32_e32 v48, 32, v162
	v_bitop3_b32 v48, v48, v56, v57 bitop3:0xde
	v_add_u32_e32 v218, 0, v48
	ds_read_b128 v[48:51], v218 offset:32768
	ds_read_b128 v[52:55], v218 offset:40960
	s_cmp_lg_u32 0, -1
	s_cselect_b32 s53, 0, 0
	s_add_u32 s16, s10, s96
	s_waitcnt lgkmcnt(2)
	v_mfma_f32_32x32x16_bf16 v[16:31], v[20:23], v[138:141], 0
	s_addc_u32 s17, s11, s97
	v_mov_b32_e32 v199, v129
	s_add_u32 s18, s8, s96
	s_addc_u32 s19, s9, s97
	v_lshl_add_u64 v[60:61], s[18:19], 0, v[198:199]
	s_add_u32 s2, s16, s96
	s_addc_u32 s3, s17, s97
	s_waitcnt lgkmcnt(1)
	v_mfma_f32_32x32x16_bf16 v[32:47], v[48:51], v[154:157], v[32:47]
	v_or_b32_e32 v48, 64, v162
	v_bitop3_b32 v48, v48, v56, v57 bitop3:0xde
	v_add_u32_e32 v219, 0, v48
	v_lshl_add_u64 v[64:65], s[2:3], 0, v[128:129]
	s_mov_b32 s72, s73
	s_mov_b32 s74, s73
	s_mov_b32 s75, s73
	s_waitcnt lgkmcnt(0)
	v_mfma_f32_32x32x16_bf16 v[16:31], v[52:55], v[154:157], v[16:31]
	ds_read_b128 v[48:51], v219 offset:32768
	ds_read_b128 v[52:55], v219 offset:40960
	s_mov_b32 s76, s73
	s_mov_b32 s77, s73
	s_mov_b32 s78, s73
	s_mov_b32 s79, s73
	s_mov_b32 s80, s73
	s_mov_b32 s81, s73
	s_waitcnt lgkmcnt(1)
	v_mfma_f32_32x32x16_bf16 v[32:47], v[48:51], v[158:161], v[32:47]
	v_or_b32_e32 v48, 0x60, v162
	v_bitop3_b32 v48, v48, v56, v57 bitop3:0xde
	v_add_u32_e32 v220, 0, v48
	s_mov_b32 s82, s73
	s_mov_b32 s83, s73
	s_mov_b32 s84, s73
	s_mov_b32 s85, s73
	s_waitcnt lgkmcnt(0)
	v_mfma_f32_32x32x16_bf16 v[16:31], v[52:55], v[158:161], v[16:31]
	ds_read_b128 v[48:51], v220 offset:32768
	ds_read_b128 v[52:55], v220 offset:40960
	s_mov_b32 s86, s73
	s_mov_b32 s87, s73
	v_mov_b64_e32 v[0:1], s[72:73]
	v_mov_b64_e32 v[14:15], s[86:87]
	v_add_u32_e32 v209, s53, v114
	v_mov_b64_e32 v[2:3], s[74:75]
	s_waitcnt lgkmcnt(1)
	v_mfma_f32_32x32x16_bf16 v[32:47], v[48:51], v[150:153], v[32:47]
	v_or_b32_e32 v48, 0x80, v162
	v_bitop3_b32 v48, v48, v56, v57 bitop3:0xde
	v_add_u32_e32 v221, 0, v48
	v_mov_b64_e32 v[4:5], s[76:77]
	v_mov_b64_e32 v[6:7], s[78:79]
	v_mov_b64_e32 v[8:9], s[80:81]
	v_mov_b64_e32 v[10:11], s[82:83]
	s_waitcnt lgkmcnt(0)
	v_mfma_f32_32x32x16_bf16 v[16:31], v[52:55], v[150:153], v[16:31]
	ds_read_b128 v[48:51], v221 offset:32768
	ds_read_b128 v[52:55], v221 offset:40960
	v_mov_b64_e32 v[12:13], s[84:85]
	s_mov_b32 s39, 4
	v_mov_b32_e32 v217, 0
	v_readlane_b32 s80, v255, 48
	s_movk_i32 s79, 0xff
	s_movk_i32 s84, 0xffe0
	s_waitcnt lgkmcnt(1)
	v_mfma_f32_32x32x16_bf16 v[32:47], v[48:51], v[146:149], v[32:47]
	v_or_b32_e32 v48, 0xa0, v162
	v_bitop3_b32 v48, v48, v56, v57 bitop3:0xde
	v_add_u32_e32 v222, 0, v48
	s_waitcnt lgkmcnt(0)
	v_mfma_f32_32x32x16_bf16 v[16:31], v[52:55], v[146:149], v[16:31]
	ds_read_b128 v[48:51], v222 offset:32768
	ds_read_b128 v[52:55], v222 offset:40960
	s_waitcnt lgkmcnt(1)
	v_mfma_f32_32x32x16_bf16 v[32:47], v[48:51], v[142:145], v[32:47]
	v_or_b32_e32 v48, 0xc0, v162
	v_bitop3_b32 v48, v48, v56, v57 bitop3:0xde
	v_add_u32_e32 v224, 0, v48
	s_waitcnt lgkmcnt(0)
	v_mfma_f32_32x32x16_bf16 v[16:31], v[52:55], v[142:145], v[16:31]
	ds_read_b128 v[48:51], v224 offset:32768
	ds_read_b128 v[52:55], v224 offset:40960
	s_waitcnt lgkmcnt(1)
	v_mfma_f32_32x32x16_bf16 v[32:47], v[48:51], v[134:137], v[32:47]
	v_or_b32_e32 v48, 0xe0, v162
	v_bitop3_b32 v48, v48, v56, v57 bitop3:0xde
	v_add_u32_e32 v223, 0, v48
	v_lshl_add_u64 v[56:57], s[18:19], 0, v[128:129]
	s_waitcnt lgkmcnt(0)
	v_mfma_f32_32x32x16_bf16 v[16:31], v[52:55], v[134:137], v[16:31]
	ds_read_b128 v[48:51], v223 offset:32768
	ds_read_b128 v[52:55], v223 offset:40960
	global_load_dwordx4 v[56:59], v[56:57], off
	s_nop 0
	global_load_dwordx4 v[60:63], v[60:61], off
	s_nop 0
	global_load_dwordx4 v[162:165], v[64:65], off
	v_lshl_add_u64 v[64:65], s[2:3], 0, v[198:199]
	s_waitcnt lgkmcnt(1)
	v_mfma_f32_32x32x16_bf16 v[32:47], v[48:51], v[130:133], v[32:47]
	global_load_dwordx4 v[166:169], v[64:65], off
	s_waitcnt lgkmcnt(0)
	v_mfma_f32_32x32x16_bf16 v[16:31], v[52:55], v[130:133], v[16:31]
	s_nop 8
	v_lshl_add_u64 v[48:49], s[16:17], 0, v[128:129]
	global_load_dwordx4 v[48:51], v[48:49], off
	v_lshl_add_u64 v[52:53], s[16:17], 0, v[198:199]
	global_load_dwordx4 v[52:55], v[52:53], off
	s_add_u32 s16, s18, s96
	s_addc_u32 s17, s19, s97
	v_lshl_add_u64 v[64:65], s[16:17], 0, v[128:129]
	global_load_dwordx4 v[170:173], v[64:65], off
	v_lshl_add_u64 v[64:65], s[16:17], 0, v[198:199]
	global_load_dwordx4 v[174:177], v[64:65], off
	s_and_b64 s[2:3], s[14:15], exec
	s_cselect_b32 s14, 3, 35
	s_waitcnt vmcnt(4)
	s_waitcnt vmcnt(3)
	ds_write_b128 v212, v[48:51] offset:16384
	s_waitcnt vmcnt(2)
	ds_write_b128 v213, v[52:55] offset:16384
	ds_write_b128 v214, v[56:59] offset:49152
	ds_write_b128 v215, v[60:63] offset:49152
	v_exp_f32_e32 v64, v32
	v_exp_f32_e32 v65, v33
	v_exp_f32_e32 v66, v34
	v_exp_f32_e32 v67, v35
	v_exp_f32_e32 v68, v36
	v_exp_f32_e32 v69, v37
	v_exp_f32_e32 v70, v38
	v_exp_f32_e32 v71, v39
	v_exp_f32_e32 v72, v40
	v_exp_f32_e32 v73, v41
	v_exp_f32_e32 v74, v42
	v_exp_f32_e32 v80, v16
	v_exp_f32_e32 v81, v17
	v_exp_f32_e32 v75, v43
	v_exp_f32_e32 v76, v44
	v_exp_f32_e32 v77, v45
	v_exp_f32_e32 v78, v46
	v_exp_f32_e32 v79, v47
	v_exp_f32_e32 v82, v18
	v_exp_f32_e32 v83, v19
	v_lshl_add_u64 v[16:17], s[12:13], 0, v[128:129]
	v_lshl_add_u64 v[18:19], s[12:13], 0, v[198:199]
	v_exp_f32_e32 v94, v30
	v_exp_f32_e32 v95, v31
	v_exp_f32_e32 v92, v28
	v_exp_f32_e32 v93, v29
	v_exp_f32_e32 v196, v26
	v_exp_f32_e32 v197, v27
	v_exp_f32_e32 v194, v24
	v_exp_f32_e32 v195, v25
	v_exp_f32_e32 v86, v22
	v_exp_f32_e32 v87, v23
	v_exp_f32_e32 v84, v20
	v_exp_f32_e32 v85, v21
	s_addk_i32 s53, 0x4000
	v_lshl_add_u64 v[200:201], s[64:65], 0, v[16:17]
	v_lshl_add_u64 v[202:203], s[64:65], 0, v[18:19]
	v_lshl_add_u64 v[204:205], s[66:67], 0, v[16:17]
	v_lshl_add_u64 v[206:207], s[66:67], 0, v[18:19]
	v_mov_b64_e32 v[62:63], v[14:15]
	v_mov_b64_e32 v[46:47], v[14:15]
	v_mov_b64_e32 v[30:31], v[14:15]
	v_add_u32_e32 v211, s53, v114
	v_mov_b64_e32 v[60:61], v[12:13]
	v_mov_b64_e32 v[58:59], v[10:11]
	v_mov_b64_e32 v[56:57], v[8:9]
	v_mov_b64_e32 v[54:55], v[6:7]
	v_mov_b64_e32 v[52:53], v[4:5]
	v_mov_b64_e32 v[50:51], v[2:3]
	v_mov_b64_e32 v[48:49], v[0:1]
	v_mov_b64_e32 v[44:45], v[12:13]
	v_mov_b64_e32 v[42:43], v[10:11]
	v_mov_b64_e32 v[40:41], v[8:9]
	v_mov_b64_e32 v[38:39], v[6:7]
	v_mov_b64_e32 v[36:37], v[4:5]
	v_mov_b64_e32 v[34:35], v[2:3]
	v_mov_b64_e32 v[32:33], v[0:1]
	v_mov_b64_e32 v[28:29], v[12:13]
	v_mov_b64_e32 v[26:27], v[10:11]
	v_mov_b64_e32 v[24:25], v[8:9]
	v_mov_b64_e32 v[22:23], v[6:7]
	v_mov_b64_e32 v[20:21], v[4:5]
	v_mov_b64_e32 v[18:19], v[2:3]
	v_mov_b64_e32 v[16:17], v[0:1]
	s_mov_b32 s53, 0x38e38e39
	s_waitcnt lgkmcnt(0)
	s_barrier

.Lgqa_slow_880:
	v_add_u32_e32 v21, 32, v185
	v_and_b32_e32 v17, 0xfffff0, v185
	v_lshlrev_b32_e32 v18, 1, v185
	v_and_b32_e32 v22, 0xfffff0, v21
	v_lshlrev_b32_e32 v23, 1, v21
	v_and_b32_e32 v16, 63, v184
	v_and_or_b32 v17, v18, 8, v17
	v_and_or_b32 v22, v23, 8, v22
	v_lshrrev_b32_e32 v17, 1, v17
	v_lshrrev_b32_e32 v19, 5, v186
	v_lshrrev_b32_e32 v22, 1, v22
	v_lshlrev_b32_e32 v23, 4, v16
	v_lshrrev_b32_e32 v18, 1, v185
	v_or_b32_e32 v17, v17, v19
	v_and_b32_e32 v20, 3, v185
	v_or_b32_e32 v19, v22, v19
	v_lshlrev_b32_e32 v22, 3, v16
	v_and_b32_e32 v23, 0xc0, v23
	v_lshlrev_b32_e32 v16, 1, v16
	v_and_or_b32 v18, v18, 4, v20
	v_lshlrev_b32_e32 v20, 1, v186
	v_and_or_b32 v23, v22, 24, v23
	v_and_b32_e32 v16, 32, v16
	v_and_b32_e32 v22, 0x100, v22
	v_lshlrev_b32_e32 v17, 9, v17
	v_lshlrev_b32_e32 v18, 6, v18
	v_or3_b32 v114, v23, v16, v22
	v_and_b32_e32 v16, 48, v20
	v_or3_b32 v17, v17, v18, v16
	v_add_u32_e32 v212, 0, v17
	v_lshrrev_b32_e32 v17, 3, v212
	v_xor_b32_e32 v17, v17, v212
	v_and_b32_e32 v17, 0x100, v17
	v_xor_b32_e32 v212, v212, v17
	v_lshlrev_b32_e32 v17, 3, v17
	v_xor_b32_e32 v212, v212, v17
	v_lshlrev_b32_e32 v19, 9, v19
	v_cvt_pk_bf16_f32 v138, v176, v177
	v_cvt_pk_bf16_f32 v139, v170, v171
	v_cvt_pk_bf16_f32 v140, v164, v165
	v_cvt_pk_bf16_f32 v141, v144, v145
	v_cvt_pk_bf16_f32 v154, v142, v143
	v_cvt_pk_bf16_f32 v155, v136, v137
	v_cvt_pk_bf16_f32 v156, v134, v135
	v_cvt_pk_bf16_f32 v157, v132, v133
	v_cvt_pk_bf16_f32 v158, v130, v131
	v_cvt_pk_bf16_f32 v159, v126, v127
	v_cvt_pk_bf16_f32 v160, v124, v125
	v_cvt_pk_bf16_f32 v161, v122, v123
	v_cvt_pk_bf16_f32 v150, v120, v121
	v_cvt_pk_bf16_f32 v151, v118, v119
	v_cvt_pk_bf16_f32 v152, v116, v117
	v_cvt_pk_bf16_f32 v153, v112, v113
	v_cvt_pk_bf16_f32 v146, v108, v109
	v_cvt_pk_bf16_f32 v147, v110, v111
	v_cvt_pk_bf16_f32 v148, v104, v105
	v_cvt_pk_bf16_f32 v149, v106, v107
	v_cvt_pk_bf16_f32 v142, v100, v101
	v_cvt_pk_bf16_f32 v143, v102, v103
	v_cvt_pk_bf16_f32 v144, v96, v97
	v_cvt_pk_bf16_f32 v145, v98, v99
	v_cvt_pk_bf16_f32 v134, v92, v93
	v_cvt_pk_bf16_f32 v135, v94, v95
	v_cvt_pk_bf16_f32 v136, v88, v89
	v_cvt_pk_bf16_f32 v137, v90, v91
	v_cvt_pk_bf16_f32 v130, v84, v85
	v_cvt_pk_bf16_f32 v131, v86, v87
	v_cvt_pk_bf16_f32 v132, v80, v81
	v_cvt_pk_bf16_f32 v133, v82, v83
	s_waitcnt vmcnt(0)
	ds_write_b128 v212, v[8:11]
	v_lshlrev_b32_e32 v8, 8, v185
	v_and_b32_e32 v9, 0x70, v184
	v_or3_b32 v16, v19, v18, v16
	v_bitop3_b32 v8, v20, v8, v9 bitop3:0xde
	v_add_u32_e32 v213, 0, v16
	v_lshrrev_b32_e32 v16, 3, v213
	v_xor_b32_e32 v16, v16, v213
	v_and_b32_e32 v16, 0x100, v16
	v_xor_b32_e32 v213, v213, v16
	v_lshlrev_b32_e32 v16, 3, v16
	v_xor_b32_e32 v213, v213, v16
	v_add_u32_e32 v214, 0, v8
	ds_write_b128 v213, v[12:15]
	ds_write_b128 v214, v[4:7] offset:32768
	v_lshlrev_b32_e32 v4, 8, v21
	v_bitop3_b32 v4, v20, v4, v9 bitop3:0xde
	v_add_u32_e32 v215, 0, v4
	ds_write_b128 v215, v[0:3] offset:32768
	v_lshlrev_b32_e32 v0, 4, v163
	v_lshlrev_b32_e32 v56, 8, v163
	v_and_b32_e32 v57, 0x70, v0
	v_bitop3_b32 v0, v162, v56, v57 bitop3:0xde
	v_add_u32_e32 v216, 0, v0
	s_waitcnt lgkmcnt(0)
	s_barrier
	ds_read_b128 v[16:19], v216 offset:32768
	ds_read_b128 v[20:23], v216 offset:40960
	s_waitcnt lgkmcnt(1)
	v_mfma_f32_32x32x16_bf16 v[32:47], v[16:19], v[138:141], 0
	v_or_b32_e32 v48, 32, v162
	v_bitop3_b32 v48, v48, v56, v57 bitop3:0xde
	v_add_u32_e32 v218, 0, v48
	ds_read_b128 v[48:51], v218 offset:32768
	ds_read_b128 v[52:55], v218 offset:40960
	s_cmp_lg_u32 0, -1
	s_cselect_b32 s53, 0, 0
	s_add_u32 s16, s10, s96
	s_waitcnt lgkmcnt(2)
	v_mfma_f32_32x32x16_bf16 v[16:31], v[20:23], v[138:141], 0
	s_addc_u32 s17, s11, s97
	v_mov_b32_e32 v199, v129
	s_add_u32 s18, s8, s96
	s_addc_u32 s19, s9, s97
	v_lshl_add_u64 v[60:61], s[18:19], 0, v[198:199]
	s_add_u32 s2, s16, s96
	s_addc_u32 s3, s17, s97
	s_waitcnt lgkmcnt(1)
	v_mfma_f32_32x32x16_bf16 v[32:47], v[48:51], v[154:157], v[32:47]
	v_or_b32_e32 v48, 64, v162
	v_bitop3_b32 v48, v48, v56, v57 bitop3:0xde
	v_add_u32_e32 v219, 0, v48
	v_lshl_add_u64 v[64:65], s[2:3], 0, v[128:129]
	s_mov_b32 s72, s73
	s_mov_b32 s74, s73
	s_mov_b32 s75, s73
	s_waitcnt lgkmcnt(0)
	v_mfma_f32_32x32x16_bf16 v[16:31], v[52:55], v[154:157], v[16:31]
	ds_read_b128 v[48:51], v219 offset:32768
	ds_read_b128 v[52:55], v219 offset:40960
	s_mov_b32 s76, s73
	s_mov_b32 s77, s73
	s_mov_b32 s78, s73
	s_mov_b32 s79, s73
	s_mov_b32 s80, s73
	s_mov_b32 s81, s73
	s_waitcnt lgkmcnt(1)
	v_mfma_f32_32x32x16_bf16 v[32:47], v[48:51], v[158:161], v[32:47]
	v_or_b32_e32 v48, 0x60, v162
	v_bitop3_b32 v48, v48, v56, v57 bitop3:0xde
	v_add_u32_e32 v220, 0, v48
	s_mov_b32 s82, s73
	s_mov_b32 s83, s73
	s_mov_b32 s84, s73
	s_mov_b32 s85, s73
	s_waitcnt lgkmcnt(0)
	v_mfma_f32_32x32x16_bf16 v[16:31], v[52:55], v[158:161], v[16:31]
	ds_read_b128 v[48:51], v220 offset:32768
	ds_read_b128 v[52:55], v220 offset:40960
	s_mov_b32 s86, s73
	s_mov_b32 s87, s73
	v_mov_b64_e32 v[0:1], s[72:73]
	v_mov_b64_e32 v[14:15], s[86:87]
	v_add_u32_e32 v209, s53, v114
	v_mov_b64_e32 v[2:3], s[74:75]
	s_waitcnt lgkmcnt(1)
	v_mfma_f32_32x32x16_bf16 v[32:47], v[48:51], v[150:153], v[32:47]
	v_or_b32_e32 v48, 0x80, v162
	v_bitop3_b32 v48, v48, v56, v57 bitop3:0xde
	v_add_u32_e32 v221, 0, v48
	v_mov_b64_e32 v[4:5], s[76:77]
	v_mov_b64_e32 v[6:7], s[78:79]
	v_mov_b64_e32 v[8:9], s[80:81]
	v_mov_b64_e32 v[10:11], s[82:83]
	s_waitcnt lgkmcnt(0)
	v_mfma_f32_32x32x16_bf16 v[16:31], v[52:55], v[150:153], v[16:31]
	ds_read_b128 v[48:51], v221 offset:32768
	ds_read_b128 v[52:55], v221 offset:40960
	v_mov_b64_e32 v[12:13], s[84:85]
	s_mov_b32 s39, 4
	v_mov_b32_e32 v217, 0
	v_readlane_b32 s80, v255, 48
	s_movk_i32 s79, 0xff
	s_movk_i32 s84, 0xffe0
	s_waitcnt lgkmcnt(1)
	v_mfma_f32_32x32x16_bf16 v[32:47], v[48:51], v[146:149], v[32:47]
	v_or_b32_e32 v48, 0xa0, v162
	v_bitop3_b32 v48, v48, v56, v57 bitop3:0xde
	v_add_u32_e32 v222, 0, v48
	s_waitcnt lgkmcnt(0)
	v_mfma_f32_32x32x16_bf16 v[16:31], v[52:55], v[146:149], v[16:31]
	ds_read_b128 v[48:51], v222 offset:32768
	ds_read_b128 v[52:55], v222 offset:40960
	s_waitcnt lgkmcnt(1)
	v_mfma_f32_32x32x16_bf16 v[32:47], v[48:51], v[142:145], v[32:47]
	v_or_b32_e32 v48, 0xc0, v162
	v_bitop3_b32 v48, v48, v56, v57 bitop3:0xde
	v_add_u32_e32 v224, 0, v48
	s_waitcnt lgkmcnt(0)
	v_mfma_f32_32x32x16_bf16 v[16:31], v[52:55], v[142:145], v[16:31]
	ds_read_b128 v[48:51], v224 offset:32768
	ds_read_b128 v[52:55], v224 offset:40960
	s_waitcnt lgkmcnt(1)
	v_mfma_f32_32x32x16_bf16 v[32:47], v[48:51], v[134:137], v[32:47]
	v_or_b32_e32 v48, 0xe0, v162
	v_bitop3_b32 v48, v48, v56, v57 bitop3:0xde
	v_add_u32_e32 v223, 0, v48
	v_lshl_add_u64 v[56:57], s[18:19], 0, v[128:129]
	s_waitcnt lgkmcnt(0)
	v_mfma_f32_32x32x16_bf16 v[16:31], v[52:55], v[134:137], v[16:31]
	ds_read_b128 v[48:51], v223 offset:32768
	ds_read_b128 v[52:55], v223 offset:40960
	global_load_dwordx4 v[56:59], v[56:57], off
	s_nop 0
	global_load_dwordx4 v[60:63], v[60:61], off
	s_nop 0
	global_load_dwordx4 v[162:165], v[64:65], off
	v_lshl_add_u64 v[64:65], s[2:3], 0, v[198:199]
	s_waitcnt lgkmcnt(1)
	v_mfma_f32_32x32x16_bf16 v[32:47], v[48:51], v[130:133], v[32:47]
	global_load_dwordx4 v[166:169], v[64:65], off
	s_waitcnt lgkmcnt(0)
	v_mfma_f32_32x32x16_bf16 v[16:31], v[52:55], v[130:133], v[16:31]
	s_nop 8
	v_max_f32_e32 v48, v33, v33
	v_max_f32_e32 v49, v32, v32
	v_max_f32_e32 v48, v49, v48
	v_max_f32_e32 v49, v41, v41
	v_max_f32_e32 v50, v40, v40
	v_max_f32_e32 v49, v50, v49
	v_max3_f32 v48, v48, v34, v35
	v_max_f32_e32 v50, v25, v25
	v_max_f32_e32 v51, v24, v24
	v_max_f32_e32 v50, v51, v50
	v_max3_f32 v51, v16, v17, v18
	v_max3_f32 v50, v50, v26, v27
	v_max3_f32 v49, v49, v42, v43
	v_max3_f32 v51, v51, v19, v20
	v_max3_f32 v50, v50, v28, v29
	v_max3_f32 v48, v48, v36, v37
	v_max3_f32 v49, v49, v44, v45
	v_max3_f32 v51, v51, v21, v22
	v_max3_f32 v50, v50, v30, v31
	v_max3_f32 v48, v48, v38, v39
	v_max3_f32 v49, v49, v46, v47
	v_max3_f32 v50, v51, v23, v50
	v_max3_f32 v48, v48, v49, v50
	v_mov_b32_e32 v49, v48
	s_nop 1
	v_permlane32_swap_b32_e32 v48, v49
	v_max_f32_e32 v49, v49, v49
	v_max_f32_e32 v48, v48, v48
	v_max_f32_e32 v66, v48, v49
	v_add_f32_e32 v48, 0x7149f2ca, v66
	v_cmp_ge_f32_e32 vcc, s31, v48
	v_lshl_add_u64 v[48:49], s[16:17], 0, v[128:129]
	global_load_dwordx4 v[48:51], v[48:49], off
	v_lshl_add_u64 v[52:53], s[16:17], 0, v[198:199]
	global_load_dwordx4 v[52:55], v[52:53], off
	s_add_u32 s16, s18, s96
	s_addc_u32 s17, s19, s97
	v_lshl_add_u64 v[64:65], s[16:17], 0, v[128:129]
	global_load_dwordx4 v[170:173], v[64:65], off
	v_lshl_add_u64 v[64:65], s[16:17], 0, v[198:199]
	global_load_dwordx4 v[174:177], v[64:65], off
	s_and_b64 s[2:3], s[14:15], exec
	s_cselect_b32 s14, 3, 35
	s_cmp_eq_u64 vcc, exec
	s_waitcnt vmcnt(4)
	s_waitcnt vmcnt(3)
	ds_write_b128 v212, v[48:51] offset:16384
	s_waitcnt vmcnt(2)
	ds_write_b128 v213, v[52:55] offset:16384
	ds_write_b128 v214, v[56:59] offset:49152
	ds_write_b128 v215, v[60:63] offset:49152
	s_cselect_b64 vcc, -1, 0
	v_max_f32_e32 v49, 0xf149f2ca, v66
	v_cndmask_b32_e32 v226, v49, v230, vcc
	v_mul_f32_e32 v48, 0xbe0293ee, v226
	v_fmamk_f32 v32, v32, 0x3e0293ee, v48
	v_exp_f32_e32 v64, v32
	v_fmamk_f32 v32, v33, 0x3e0293ee, v48
	v_exp_f32_e32 v65, v32
	v_fmamk_f32 v32, v34, 0x3e0293ee, v48
	v_exp_f32_e32 v66, v32
	v_fmamk_f32 v32, v35, 0x3e0293ee, v48
	v_exp_f32_e32 v67, v32
	v_fmamk_f32 v32, v36, 0x3e0293ee, v48
	v_exp_f32_e32 v68, v32
	v_fmamk_f32 v32, v37, 0x3e0293ee, v48
	v_exp_f32_e32 v69, v32
	v_fmamk_f32 v32, v38, 0x3e0293ee, v48
	v_exp_f32_e32 v70, v32
	v_fmamk_f32 v32, v39, 0x3e0293ee, v48
	v_exp_f32_e32 v71, v32
	v_fmamk_f32 v32, v40, 0x3e0293ee, v48
	v_exp_f32_e32 v72, v32
	v_fmamk_f32 v32, v41, 0x3e0293ee, v48
	v_exp_f32_e32 v73, v32
	v_fmamk_f32 v32, v42, 0x3e0293ee, v48
	v_exp_f32_e32 v74, v32
	v_fmamk_f32 v32, v43, 0x3e0293ee, v48
	v_pk_fma_f32 v[80:81], v[16:17], s[52:53], v[48:49] op_sel_hi:[1,0,0]
	v_sub_f32_e32 v16, 0xf149f2ca, v49
	v_exp_f32_e32 v75, v32
	v_fmamk_f32 v32, v44, 0x3e0293ee, v48
	v_mul_f32_e32 v16, 0x3e0293ee, v16
	v_exp_f32_e32 v76, v32
	v_fmamk_f32 v32, v45, 0x3e0293ee, v48
	v_exp_f32_e32 v16, v16
	v_exp_f32_e32 v77, v32
	v_fmamk_f32 v32, v46, 0x3e0293ee, v48
	v_exp_f32_e32 v78, v32
	v_fmamk_f32 v32, v47, 0x3e0293ee, v48
	v_exp_f32_e32 v79, v32
	v_pk_fma_f32 v[82:83], v[18:19], s[52:53], v[48:49] op_sel_hi:[1,0,0]
	v_cndmask_b32_e64 v225, v16, 1.0, vcc
	v_lshl_add_u64 v[16:17], s[12:13], 0, v[128:129]
	v_lshl_add_u64 v[18:19], s[12:13], 0, v[198:199]
	v_pk_fma_f32 v[94:95], v[30:31], s[52:53], v[48:49] op_sel_hi:[1,0,0]
	v_pk_fma_f32 v[92:93], v[28:29], s[52:53], v[48:49] op_sel_hi:[1,0,0]
	v_pk_fma_f32 v[90:91], v[26:27], s[52:53], v[48:49] op_sel_hi:[1,0,0]
	v_pk_fma_f32 v[88:89], v[24:25], s[52:53], v[48:49] op_sel_hi:[1,0,0]
	v_pk_fma_f32 v[86:87], v[22:23], s[52:53], v[48:49] op_sel_hi:[1,0,0]
	v_pk_fma_f32 v[84:85], v[20:21], s[52:53], v[48:49] op_sel_hi:[1,0,0]
	s_addk_i32 s53, 0x4000
	v_lshl_add_u64 v[200:201], s[64:65], 0, v[16:17]
	v_lshl_add_u64 v[202:203], s[64:65], 0, v[18:19]
	v_lshl_add_u64 v[204:205], s[66:67], 0, v[16:17]
	v_lshl_add_u64 v[206:207], s[66:67], 0, v[18:19]
	v_mov_b64_e32 v[62:63], v[14:15]
	v_mov_b64_e32 v[46:47], v[14:15]
	v_mov_b64_e32 v[30:31], v[14:15]
	v_add_u32_e32 v211, s53, v114
	v_mov_b64_e32 v[60:61], v[12:13]
	v_mov_b64_e32 v[58:59], v[10:11]
	v_mov_b64_e32 v[56:57], v[8:9]
	v_mov_b64_e32 v[54:55], v[6:7]
	v_mov_b64_e32 v[52:53], v[4:5]
	v_mov_b64_e32 v[50:51], v[2:3]
	v_mov_b64_e32 v[48:49], v[0:1]
	v_mov_b64_e32 v[44:45], v[12:13]
	v_mov_b64_e32 v[42:43], v[10:11]
	v_mov_b64_e32 v[40:41], v[8:9]
	v_mov_b64_e32 v[38:39], v[6:7]
	v_mov_b64_e32 v[36:37], v[4:5]
	v_mov_b64_e32 v[34:35], v[2:3]
	v_mov_b64_e32 v[32:33], v[0:1]
	v_mov_b64_e32 v[28:29], v[12:13]
	v_mov_b64_e32 v[26:27], v[10:11]
	v_mov_b64_e32 v[24:25], v[8:9]
	v_mov_b64_e32 v[22:23], v[6:7]
	v_mov_b64_e32 v[20:21], v[4:5]
	v_mov_b64_e32 v[18:19], v[2:3]
	v_mov_b64_e32 v[16:17], v[0:1]
	s_mov_b32 s53, 0x38e38e39
	s_waitcnt lgkmcnt(0)
	s_barrier
